# bf16 pack idiom -> v_cvt_pk_bf16_f32 extended (618 pairs) with wide-store WAR pads
# speedup vs baseline: 1.0078x; 1.0009x over previous
.LBB0_55:
	v_lshl_add_u64 v[68:69], v[44:45], 0, s[6:7]
	v_lshl_add_u64 v[70:71], v[42:43], 0, s[6:7]
	v_lshl_add_u64 v[72:73], v[40:41], 0, s[6:7]
	v_lshl_add_u64 v[74:75], v[38:39], 0, s[6:7]
	v_lshl_add_u64 v[76:77], v[36:37], 0, s[6:7]
	v_lshl_add_u64 v[78:79], v[34:35], 0, s[6:7]
	v_lshl_add_u64 v[80:81], v[32:33], 0, s[6:7]
	v_lshl_add_u64 v[82:83], v[30:31], 0, s[6:7]
	global_load_dword v67, v[68:69], off nt
	s_nop 0
	global_load_dword v68, v[70:71], off nt
	global_load_dword v69, v[72:73], off nt
	s_nop 0
	global_load_dword v70, v[74:75], off nt
	global_load_dword v71, v[76:77], off nt
	global_load_dword v72, v[78:79], off nt
	global_load_dword v73, v[80:81], off nt
	s_nop 0
	global_load_dword v74, v[82:83], off nt
	s_add_u32 s6, s6, 0x2c000
	s_addc_u32 s7, s7, 0
	v_add_u32_e32 v75, 0x400, v8
	s_cmp_lg_u32 s6, 0xb0000
	s_waitcnt vmcnt(6)
	ds_write2_b32 v8, v67, v68 offset1:66
	s_waitcnt vmcnt(4)
	ds_write2_b32 v8, v69, v70 offset0:132 offset1:198
	s_waitcnt vmcnt(2)
	ds_write2_b32 v75, v71, v72 offset0:8 offset1:74
	s_waitcnt vmcnt(0)
	ds_write2_b32 v75, v73, v74 offset0:140 offset1:206
	v_add_u32_e32 v8, 0x840, v8
	s_cbranch_scc1 .LBB0_55
	s_waitcnt lgkmcnt(0)
	ds_read2_b32 v[34:35], v47 offset1:8
	ds_read2_b32 v[38:39], v47 offset0:33 offset1:41
	ds_read2_b32 v[40:41], v47 offset0:66 offset1:74
	ds_read2_b32 v[42:43], v47 offset0:99 offset1:107
	ds_read2_b32 v[44:45], v47 offset0:132 offset1:140
	s_waitcnt lgkmcnt(4)
	s_waitcnt lgkmcnt(3)
	ds_read2_b32 v[68:69], v47 offset0:165 offset1:173
	v_cvt_pk_bf16_f32 v30, v34, v38
	s_waitcnt lgkmcnt(3)
	s_waitcnt lgkmcnt(2)
	ds_read2_b32 v[70:71], v47 offset0:198 offset1:206
	ds_read2_b32 v[72:73], v47 offset0:231 offset1:239
	s_lshl_b32 s0, s46, 1
	v_cvt_pk_bf16_f32 v31, v40, v42
	s_waitcnt lgkmcnt(3)
	s_and_b32 s0, s0, 0x3fe0
	s_waitcnt lgkmcnt(2)
	s_add_i32 s6, s0, 0xffffe600
	s_lshl_b32 s0, s46, 7
	v_cvt_pk_bf16_f32 v32, v44, v68
	s_waitcnt lgkmcnt(1)
	v_add_u32_e32 v74, s6, v46
	s_and_b32 s0, s0, 0x780
	s_waitcnt lgkmcnt(0)
	v_ashrrev_i32_e32 v75, 31, v74
	v_lshl_add_u64 v[36:37], v[14:15], 0, s[0:1]
	v_lshlrev_b64 v[74:75], 11, v[74:75]
	v_cvt_pk_bf16_f32 v33, v70, v72
	v_lshl_add_u64 v[74:75], v[36:37], 0, v[74:75]
	global_store_dwordx4 v[74:75], v[30:33], off
	s_nop 1
	v_cvt_pk_bf16_f32 v30, v35, v39
	v_cvt_pk_bf16_f32 v31, v41, v43
	v_cvt_pk_bf16_f32 v32, v45, v69
	v_add_u32_e32 v34, s6, v48
	v_ashrrev_i32_e32 v35, 31, v34
	v_lshlrev_b64 v[34:35], 11, v[34:35]
	v_cvt_pk_bf16_f32 v33, v71, v73
	ds_read2_b32 v[38:39], v47 offset0:16 offset1:24
	v_lshl_add_u64 v[34:35], v[36:37], 0, v[34:35]
	global_store_dwordx4 v[34:35], v[30:33], off
	ds_read2_b32 v[34:35], v47 offset0:49 offset1:57
	ds_read2_b32 v[40:41], v47 offset0:82 offset1:90
	ds_read2_b32 v[42:43], v47 offset0:115 offset1:123
	s_waitcnt lgkmcnt(3)
	s_waitcnt lgkmcnt(2)
	ds_read2_b32 v[44:45], v47 offset0:148 offset1:156
	ds_read2_b32 v[68:69], v47 offset0:181 offset1:189
	v_cvt_pk_bf16_f32 v30, v38, v34
	s_waitcnt lgkmcnt(3)
	s_waitcnt lgkmcnt(2)
	ds_read2_b32 v[70:71], v47 offset0:214 offset1:222
	ds_read2_b32 v[72:73], v47 offset0:247 offset1:255
	v_cvt_pk_bf16_f32 v31, v40, v42
	s_waitcnt lgkmcnt(3)
	s_waitcnt lgkmcnt(2)
	v_cvt_pk_bf16_f32 v32, v44, v68
	s_waitcnt lgkmcnt(1)
	v_add_u32_e32 v74, s6, v49
	s_waitcnt lgkmcnt(0)
	v_ashrrev_i32_e32 v75, 31, v74
	v_lshlrev_b64 v[74:75], 11, v[74:75]
	v_cvt_pk_bf16_f32 v33, v70, v72
	v_lshl_add_u64 v[74:75], v[36:37], 0, v[74:75]
	global_store_dwordx4 v[74:75], v[30:33], off
	s_nop 1
	v_cvt_pk_bf16_f32 v30, v39, v35
	v_cvt_pk_bf16_f32 v31, v41, v43
	v_cvt_pk_bf16_f32 v32, v45, v69
	v_add_u32_e32 v34, s6, v50
	v_ashrrev_i32_e32 v35, 31, v34
	v_lshlrev_b64 v[34:35], 11, v[34:35]
	v_cvt_pk_bf16_f32 v33, v71, v73
	v_lshl_add_u64 v[34:35], v[36:37], 0, v[34:35]
	global_store_dwordx4 v[34:35], v[30:33], off
	s_waitcnt lgkmcnt(0)

.LBB0_60:
	v_lshl_add_u64 v[68:69], v[44:45], 0, s[6:7]
	v_lshl_add_u64 v[70:71], v[42:43], 0, s[6:7]
	v_lshl_add_u64 v[72:73], v[40:41], 0, s[6:7]
	v_lshl_add_u64 v[74:75], v[38:39], 0, s[6:7]
	v_lshl_add_u64 v[76:77], v[36:37], 0, s[6:7]
	v_lshl_add_u64 v[78:79], v[34:35], 0, s[6:7]
	v_lshl_add_u64 v[80:81], v[32:33], 0, s[6:7]
	v_lshl_add_u64 v[82:83], v[30:31], 0, s[6:7]
	global_load_dword v67, v[68:69], off nt
	s_nop 0
	global_load_dword v68, v[70:71], off nt
	global_load_dword v69, v[72:73], off nt
	s_nop 0
	global_load_dword v70, v[74:75], off nt
	global_load_dword v71, v[76:77], off nt
	global_load_dword v72, v[78:79], off nt
	global_load_dword v73, v[80:81], off nt
	s_nop 0
	global_load_dword v74, v[82:83], off nt
	s_add_u32 s6, s6, 0x10000
	s_addc_u32 s7, s7, 0
	v_add_u32_e32 v75, 0x400, v8
	s_cmp_lg_u32 s6, 0x40000
	s_waitcnt vmcnt(6)
	ds_write2_b32 v8, v67, v68 offset1:66
	s_waitcnt vmcnt(4)
	ds_write2_b32 v8, v69, v70 offset0:132 offset1:198
	s_waitcnt vmcnt(2)
	ds_write2_b32 v75, v71, v72 offset0:8 offset1:74
	s_waitcnt vmcnt(0)
	ds_write2_b32 v75, v73, v74 offset0:140 offset1:206
	v_add_u32_e32 v8, 0x840, v8
	s_cbranch_scc1 .LBB0_60
	s_lshr_b32 s0, s0, 9
	s_lshl_b32 s6, s46, 5
	s_waitcnt lgkmcnt(0)
	s_and_b32 s8, s6, 0x3e0
	s_lshl_b64 s[6:7], s[0:1], 21
	ds_read2_b32 v[34:35], v47 offset1:8
	s_add_u32 s0, s24, s6
	ds_read2_b32 v[38:39], v47 offset0:33 offset1:41
	s_addc_u32 s7, s25, s7
	s_lshl_b32 s6, s9, 1
	s_add_u32 s6, s0, s6
	ds_read2_b32 v[40:41], v47 offset0:66 offset1:74
	s_addc_u32 s7, s7, 0
	v_lshlrev_b32_e32 v8, 1, v12
	ds_read2_b32 v[42:43], v47 offset0:99 offset1:107
	v_lshl_add_u64 v[36:37], s[6:7], 0, v[8:9]
	s_waitcnt lgkmcnt(3)
	s_waitcnt lgkmcnt(2)
	ds_read2_b32 v[44:45], v47 offset0:132 offset1:140
	ds_read2_b32 v[68:69], v47 offset0:165 offset1:173
	v_cvt_pk_bf16_f32 v30, v34, v38
	s_waitcnt lgkmcnt(3)
	s_waitcnt lgkmcnt(2)
	ds_read2_b32 v[70:71], v47 offset0:198 offset1:206
	ds_read2_b32 v[72:73], v47 offset0:231 offset1:239
	v_cvt_pk_bf16_f32 v31, v40, v42
	s_waitcnt lgkmcnt(3)
	s_waitcnt lgkmcnt(2)
	v_cvt_pk_bf16_f32 v32, v44, v68
	s_waitcnt lgkmcnt(1)
	v_add_u32_e32 v74, s8, v46
	s_waitcnt lgkmcnt(0)
	v_ashrrev_i32_e32 v75, 31, v74
	v_lshlrev_b64 v[74:75], 11, v[74:75]
	v_cvt_pk_bf16_f32 v33, v70, v72
	v_lshl_add_u64 v[74:75], v[36:37], 0, v[74:75]
	global_store_dwordx4 v[74:75], v[30:33], off
	s_nop 1
	v_cvt_pk_bf16_f32 v30, v35, v39
	v_cvt_pk_bf16_f32 v31, v41, v43
	v_cvt_pk_bf16_f32 v32, v45, v69
	v_add_u32_e32 v34, s8, v48
	v_ashrrev_i32_e32 v35, 31, v34
	v_lshlrev_b64 v[34:35], 11, v[34:35]
	v_cvt_pk_bf16_f32 v33, v71, v73
	ds_read2_b32 v[38:39], v47 offset0:16 offset1:24
	v_lshl_add_u64 v[34:35], v[36:37], 0, v[34:35]
	global_store_dwordx4 v[34:35], v[30:33], off
	ds_read2_b32 v[34:35], v47 offset0:49 offset1:57
	ds_read2_b32 v[40:41], v47 offset0:82 offset1:90
	ds_read2_b32 v[42:43], v47 offset0:115 offset1:123
	s_waitcnt lgkmcnt(3)
	s_waitcnt lgkmcnt(2)
	ds_read2_b32 v[44:45], v47 offset0:148 offset1:156
	ds_read2_b32 v[68:69], v47 offset0:181 offset1:189
	v_cvt_pk_bf16_f32 v30, v38, v34
	s_waitcnt lgkmcnt(3)
	s_waitcnt lgkmcnt(2)
	ds_read2_b32 v[70:71], v47 offset0:214 offset1:222
	ds_read2_b32 v[72:73], v47 offset0:247 offset1:255
	v_cvt_pk_bf16_f32 v31, v40, v42
	s_waitcnt lgkmcnt(3)
	s_waitcnt lgkmcnt(2)
	v_cvt_pk_bf16_f32 v32, v44, v68
	s_waitcnt lgkmcnt(1)
	v_add_u32_e32 v74, s8, v49
	s_waitcnt lgkmcnt(0)
	v_ashrrev_i32_e32 v75, 31, v74
	v_lshlrev_b64 v[74:75], 11, v[74:75]
	v_cvt_pk_bf16_f32 v33, v70, v72
	v_lshl_add_u64 v[74:75], v[36:37], 0, v[74:75]
	global_store_dwordx4 v[74:75], v[30:33], off
	s_nop 1
	v_cvt_pk_bf16_f32 v30, v39, v35
	v_cvt_pk_bf16_f32 v31, v41, v43
	v_cvt_pk_bf16_f32 v32, v45, v69
	v_add_u32_e32 v34, s8, v50
	v_ashrrev_i32_e32 v35, 31, v34
	v_lshlrev_b64 v[34:35], 11, v[34:35]
	v_cvt_pk_bf16_f32 v33, v71, v73
	v_lshl_add_u64 v[34:35], v[36:37], 0, v[34:35]
	global_store_dwordx4 v[34:35], v[30:33], off
	s_waitcnt lgkmcnt(0)

.LBB0_65:
	v_lshl_add_u64 v[68:69], v[44:45], 0, s[10:11]
	v_lshl_add_u64 v[70:71], v[42:43], 0, s[10:11]
	v_lshl_add_u64 v[72:73], v[40:41], 0, s[10:11]
	v_lshl_add_u64 v[74:75], v[38:39], 0, s[10:11]
	v_lshl_add_u64 v[76:77], v[36:37], 0, s[10:11]
	v_lshl_add_u64 v[78:79], v[34:35], 0, s[10:11]
	v_lshl_add_u64 v[80:81], v[32:33], 0, s[10:11]
	v_lshl_add_u64 v[82:83], v[30:31], 0, s[10:11]
	global_load_dword v67, v[68:69], off nt
	s_nop 0
	global_load_dword v68, v[70:71], off nt
	global_load_dword v69, v[72:73], off nt
	s_nop 0
	global_load_dword v70, v[74:75], off nt
	global_load_dword v71, v[76:77], off nt
	global_load_dword v72, v[78:79], off nt
	global_load_dword v73, v[80:81], off nt
	s_nop 0
	global_load_dword v74, v[82:83], off nt
	s_add_u32 s10, s10, 0x24000
	s_addc_u32 s11, s11, 0
	v_add_u32_e32 v75, 0x400, v8
	s_cmp_lg_u32 s10, 0x90000
	s_waitcnt vmcnt(6)
	ds_write2_b32 v8, v67, v68 offset1:66
	s_waitcnt vmcnt(4)
	ds_write2_b32 v8, v69, v70 offset0:132 offset1:198
	s_waitcnt vmcnt(2)
	ds_write2_b32 v75, v71, v72 offset0:8 offset1:74
	s_waitcnt vmcnt(0)
	ds_write2_b32 v75, v73, v74 offset0:140 offset1:206
	v_add_u32_e32 v8, 0x840, v8
	s_cbranch_scc1 .LBB0_65
	s_waitcnt lgkmcnt(0)
	s_mul_hi_i32 s7, s0, 0x480000
	s_mul_i32 s0, s0, 0x480000
	ds_read2_b32 v[34:35], v47 offset1:8
	s_add_u32 s0, s26, s0
	ds_read2_b32 v[38:39], v47 offset0:33 offset1:41
	s_addc_u32 s7, s27, s7
	s_lshl_b64 s[8:9], s[8:9], 1
	s_add_u32 s8, s0, s8
	ds_read2_b32 v[40:41], v47 offset0:66 offset1:74
	s_addc_u32 s9, s7, s9
	v_lshlrev_b32_e32 v8, 1, v12
	ds_read2_b32 v[42:43], v47 offset0:99 offset1:107
	v_lshl_add_u64 v[36:37], s[8:9], 0, v[8:9]
	s_waitcnt lgkmcnt(3)
	s_waitcnt lgkmcnt(2)
	ds_read2_b32 v[44:45], v47 offset0:132 offset1:140
	ds_read2_b32 v[68:69], v47 offset0:165 offset1:173
	v_cvt_pk_bf16_f32 v30, v34, v38
	s_waitcnt lgkmcnt(3)
	s_waitcnt lgkmcnt(2)
	ds_read2_b32 v[70:71], v47 offset0:198 offset1:206
	ds_read2_b32 v[72:73], v47 offset0:231 offset1:239
	v_cvt_pk_bf16_f32 v31, v40, v42
	s_waitcnt lgkmcnt(3)
	s_waitcnt lgkmcnt(2)
	v_cvt_pk_bf16_f32 v32, v44, v68
	s_waitcnt lgkmcnt(1)
	v_add_u32_e32 v74, s6, v46
	s_waitcnt lgkmcnt(0)
	v_ashrrev_i32_e32 v75, 31, v74
	v_lshlrev_b64 v[74:75], 11, v[74:75]
	v_cvt_pk_bf16_f32 v33, v70, v72
	v_lshl_add_u64 v[74:75], v[36:37], 0, v[74:75]
	global_store_dwordx4 v[74:75], v[30:33], off
	s_nop 1
	v_cvt_pk_bf16_f32 v30, v35, v39
	v_cvt_pk_bf16_f32 v31, v41, v43
	v_cvt_pk_bf16_f32 v32, v45, v69
	v_add_u32_e32 v34, s6, v48
	v_ashrrev_i32_e32 v35, 31, v34
	v_lshlrev_b64 v[34:35], 11, v[34:35]
	v_cvt_pk_bf16_f32 v33, v71, v73
	ds_read2_b32 v[38:39], v47 offset0:16 offset1:24
	v_lshl_add_u64 v[34:35], v[36:37], 0, v[34:35]
	global_store_dwordx4 v[34:35], v[30:33], off
	ds_read2_b32 v[34:35], v47 offset0:49 offset1:57
	ds_read2_b32 v[40:41], v47 offset0:82 offset1:90
	ds_read2_b32 v[42:43], v47 offset0:115 offset1:123
	s_waitcnt lgkmcnt(3)
	s_waitcnt lgkmcnt(2)
	ds_read2_b32 v[44:45], v47 offset0:148 offset1:156
	ds_read2_b32 v[68:69], v47 offset0:181 offset1:189
	v_cvt_pk_bf16_f32 v30, v38, v34
	s_waitcnt lgkmcnt(3)
	s_waitcnt lgkmcnt(2)
	ds_read2_b32 v[70:71], v47 offset0:214 offset1:222
	ds_read2_b32 v[72:73], v47 offset0:247 offset1:255
	v_cvt_pk_bf16_f32 v31, v40, v42
	s_waitcnt lgkmcnt(3)
	s_waitcnt lgkmcnt(2)
	v_cvt_pk_bf16_f32 v32, v44, v68
	s_waitcnt lgkmcnt(1)
	v_add_u32_e32 v74, s6, v49
	s_waitcnt lgkmcnt(0)
	v_ashrrev_i32_e32 v75, 31, v74
	v_lshlrev_b64 v[74:75], 11, v[74:75]
	v_cvt_pk_bf16_f32 v33, v70, v72
	v_lshl_add_u64 v[74:75], v[36:37], 0, v[74:75]
	global_store_dwordx4 v[74:75], v[30:33], off
	s_nop 1
	v_cvt_pk_bf16_f32 v30, v39, v35
	v_cvt_pk_bf16_f32 v31, v41, v43
	v_cvt_pk_bf16_f32 v32, v45, v69
	v_add_u32_e32 v34, s6, v50
	v_ashrrev_i32_e32 v35, 31, v34
	v_lshlrev_b64 v[34:35], 11, v[34:35]
	v_cvt_pk_bf16_f32 v33, v71, v73
	v_lshl_add_u64 v[34:35], v[36:37], 0, v[34:35]
	global_store_dwordx4 v[34:35], v[30:33], off
	s_waitcnt lgkmcnt(0)
	s_branch .LBB0_34

.LBB0_153:
	v_cvt_pk_bf16_f32 v114, v130, v131
	v_cvt_pk_bf16_f32 v115, v132, v133
	s_lshl_b32 s4, s4, 8
	v_cvt_pk_bf16_f32 v116, v134, v135
	s_ashr_i32 s5, s4, 31
	v_lshl_add_u32 v168, s54, 8, v164
	v_lshl_add_u64 v[162:163], s[4:5], 1, v[154:155]
	v_mad_i64_i32 v[118:119], s[4:5], v168, s86, v[162:163]
	v_cvt_pk_bf16_f32 v117, v136, v137
	global_store_dwordx4 v[118:119], v[114:117], off
	s_nop 1
	v_cvt_pk_bf16_f32 v114, v138, v139
	v_cvt_pk_bf16_f32 v115, v140, v141
	v_cvt_pk_bf16_f32 v116, v142, v143
	v_cvt_pk_bf16_f32 v117, v144, v145
	global_store_dwordx4 v[118:119], v[114:117], off offset:256
	s_andn2_b64 vcc, exec, s[62:63]
	s_mov_b64 s[38:39], -1
	v_cndmask_b32_e64 v114, 0, 1, s[62:63]
	v_cmp_ne_u32_e64 s[4:5], 1, v114
	s_cbranch_vccnz .LBB0_157
	v_mov_b64_e32 v[116:117], v[112:113]
	v_mov_b64_e32 v[128:129], v[100:101]
	v_mov_b64_e32 v[124:125], v[104:105]
	v_mov_b64_e32 v[120:121], v[108:109]
	s_and_b64 vcc, exec, s[2:3]
	v_mov_b64_e32 v[114:115], v[110:111]
	v_mov_b64_e32 v[126:127], v[98:99]
	v_mov_b64_e32 v[122:123], v[102:103]
	v_mov_b64_e32 v[118:119], v[106:107]
	s_cbranch_vccnz .LBB0_156
	v_pk_mul_f32 v[116:117], v[112:113], s[24:25] op_sel_hi:[1,0]
	v_pk_mul_f32 v[114:115], v[110:111], s[24:25] op_sel_hi:[1,0]
	v_pk_mul_f32 v[120:121], v[108:109], s[24:25] op_sel_hi:[1,0]
	v_pk_mul_f32 v[118:119], v[106:107], s[24:25] op_sel_hi:[1,0]
	v_pk_mul_f32 v[124:125], v[104:105], s[24:25] op_sel_hi:[1,0]
	v_pk_mul_f32 v[122:123], v[102:103], s[24:25] op_sel_hi:[1,0]
	v_pk_mul_f32 v[128:129], v[100:101], s[24:25] op_sel_hi:[1,0]
	v_pk_mul_f32 v[126:127], v[98:99], s[24:25] op_sel_hi:[1,0]

.LBB0_159:
	v_or_b32_e32 v98, 16, v168
	v_mad_i64_i32 v[102:103], s[38:39], v98, s86, v[162:163]
	v_cvt_pk_bf16_f32 v98, v114, v115
	v_cvt_pk_bf16_f32 v99, v116, v117
	v_cvt_pk_bf16_f32 v100, v118, v119
	v_cvt_pk_bf16_f32 v101, v120, v121
	global_store_dwordx4 v[102:103], v[98:101], off
	s_nop 1
	v_cvt_pk_bf16_f32 v98, v122, v123
	v_cvt_pk_bf16_f32 v99, v124, v125
	v_cvt_pk_bf16_f32 v100, v126, v127
	v_cvt_pk_bf16_f32 v101, v128, v129
	s_and_b64 vcc, exec, s[4:5]
	s_mov_b64 s[38:39], -1
	global_store_dwordx4 v[102:103], v[98:101], off offset:256
	s_cbranch_vccnz .LBB0_163
	s_nop 0
	v_mov_b64_e32 v[100:101], v[96:97]
	v_mov_b64_e32 v[112:113], v[84:85]
	v_mov_b64_e32 v[108:109], v[88:89]
	v_mov_b64_e32 v[104:105], v[92:93]
	s_and_b64 vcc, exec, s[2:3]
	v_mov_b64_e32 v[98:99], v[94:95]
	v_mov_b64_e32 v[110:111], v[82:83]
	v_mov_b64_e32 v[106:107], v[86:87]
	v_mov_b64_e32 v[102:103], v[90:91]
	s_cbranch_vccnz .LBB0_162
	v_pk_mul_f32 v[100:101], v[96:97], s[24:25] op_sel_hi:[1,0]
	v_pk_mul_f32 v[98:99], v[94:95], s[24:25] op_sel_hi:[1,0]
	v_pk_mul_f32 v[104:105], v[92:93], s[24:25] op_sel_hi:[1,0]
	v_pk_mul_f32 v[102:103], v[90:91], s[24:25] op_sel_hi:[1,0]
	v_pk_mul_f32 v[108:109], v[88:89], s[24:25] op_sel_hi:[1,0]
	v_pk_mul_f32 v[106:107], v[86:87], s[24:25] op_sel_hi:[1,0]
	v_pk_mul_f32 v[112:113], v[84:85], s[24:25] op_sel_hi:[1,0]
	v_pk_mul_f32 v[110:111], v[82:83], s[24:25] op_sel_hi:[1,0]

.LBB0_165:
	v_or_b32_e32 v82, 32, v168
	v_mad_i64_i32 v[86:87], s[38:39], v82, s86, v[162:163]
	v_cvt_pk_bf16_f32 v82, v98, v99
	v_cvt_pk_bf16_f32 v83, v100, v101
	v_cvt_pk_bf16_f32 v84, v102, v103
	v_cvt_pk_bf16_f32 v85, v104, v105
	global_store_dwordx4 v[86:87], v[82:85], off
	s_nop 1
	v_cvt_pk_bf16_f32 v82, v106, v107
	v_cvt_pk_bf16_f32 v83, v108, v109
	v_cvt_pk_bf16_f32 v84, v110, v111
	v_cvt_pk_bf16_f32 v85, v112, v113
	s_and_b64 vcc, exec, s[4:5]
	s_mov_b64 s[38:39], -1
	global_store_dwordx4 v[86:87], v[82:85], off offset:256
	s_cbranch_vccnz .LBB0_169
	s_nop 0
	v_mov_b64_e32 v[84:85], v[80:81]
	v_mov_b64_e32 v[96:97], v[68:69]
	v_mov_b64_e32 v[92:93], v[72:73]
	v_mov_b64_e32 v[88:89], v[76:77]
	s_and_b64 vcc, exec, s[2:3]
	v_mov_b64_e32 v[82:83], v[78:79]
	v_mov_b64_e32 v[94:95], v[66:67]
	v_mov_b64_e32 v[90:91], v[70:71]
	v_mov_b64_e32 v[86:87], v[74:75]
	s_cbranch_vccnz .LBB0_168
	v_pk_mul_f32 v[84:85], v[80:81], s[24:25] op_sel_hi:[1,0]
	v_pk_mul_f32 v[82:83], v[78:79], s[24:25] op_sel_hi:[1,0]
	v_pk_mul_f32 v[88:89], v[76:77], s[24:25] op_sel_hi:[1,0]
	v_pk_mul_f32 v[86:87], v[74:75], s[24:25] op_sel_hi:[1,0]
	v_pk_mul_f32 v[92:93], v[72:73], s[24:25] op_sel_hi:[1,0]
	v_pk_mul_f32 v[90:91], v[70:71], s[24:25] op_sel_hi:[1,0]
	v_pk_mul_f32 v[96:97], v[68:69], s[24:25] op_sel_hi:[1,0]
	v_pk_mul_f32 v[94:95], v[66:67], s[24:25] op_sel_hi:[1,0]

.LBB0_171:
	v_or_b32_e32 v66, 48, v168
	v_mad_i64_i32 v[70:71], s[38:39], v66, s86, v[162:163]
	v_cvt_pk_bf16_f32 v66, v82, v83
	v_cvt_pk_bf16_f32 v67, v84, v85
	v_cvt_pk_bf16_f32 v68, v86, v87
	v_cvt_pk_bf16_f32 v69, v88, v89
	global_store_dwordx4 v[70:71], v[66:69], off
	s_nop 1
	v_cvt_pk_bf16_f32 v66, v90, v91
	v_cvt_pk_bf16_f32 v67, v92, v93
	v_cvt_pk_bf16_f32 v68, v94, v95
	v_cvt_pk_bf16_f32 v69, v96, v97
	s_and_b64 vcc, exec, s[4:5]
	s_mov_b64 s[38:39], -1
	global_store_dwordx4 v[70:71], v[66:69], off offset:256
	s_cbranch_vccnz .LBB0_175
	s_nop 0
	v_mov_b64_e32 v[68:69], v[64:65]
	v_mov_b64_e32 v[80:81], v[52:53]
	v_mov_b64_e32 v[76:77], v[56:57]
	v_mov_b64_e32 v[72:73], v[60:61]
	s_and_b64 vcc, exec, s[2:3]
	v_mov_b64_e32 v[66:67], v[62:63]
	v_mov_b64_e32 v[78:79], v[50:51]
	v_mov_b64_e32 v[74:75], v[54:55]
	v_mov_b64_e32 v[70:71], v[58:59]
	s_cbranch_vccnz .LBB0_174
	v_pk_mul_f32 v[68:69], v[64:65], s[24:25] op_sel_hi:[1,0]
	v_pk_mul_f32 v[66:67], v[62:63], s[24:25] op_sel_hi:[1,0]
	v_pk_mul_f32 v[72:73], v[60:61], s[24:25] op_sel_hi:[1,0]
	v_pk_mul_f32 v[70:71], v[58:59], s[24:25] op_sel_hi:[1,0]
	v_pk_mul_f32 v[76:77], v[56:57], s[24:25] op_sel_hi:[1,0]
	v_pk_mul_f32 v[74:75], v[54:55], s[24:25] op_sel_hi:[1,0]
	v_pk_mul_f32 v[80:81], v[52:53], s[24:25] op_sel_hi:[1,0]
	v_pk_mul_f32 v[78:79], v[50:51], s[24:25] op_sel_hi:[1,0]

.LBB0_177:
	v_add_u32_e32 v50, 0x80, v168
	v_mad_i64_i32 v[54:55], s[38:39], v50, s86, v[162:163]
	v_cvt_pk_bf16_f32 v50, v66, v67
	v_cvt_pk_bf16_f32 v51, v68, v69
	v_cvt_pk_bf16_f32 v52, v70, v71
	v_cvt_pk_bf16_f32 v53, v72, v73
	global_store_dwordx4 v[54:55], v[50:53], off
	s_nop 1
	v_cvt_pk_bf16_f32 v50, v74, v75
	v_cvt_pk_bf16_f32 v51, v76, v77
	v_cvt_pk_bf16_f32 v52, v78, v79
	v_cvt_pk_bf16_f32 v53, v80, v81
	s_and_b64 vcc, exec, s[4:5]
	s_mov_b64 s[38:39], -1
	global_store_dwordx4 v[54:55], v[50:53], off offset:256
	s_cbranch_vccnz .LBB0_181
	s_nop 0
	v_mov_b64_e32 v[52:53], v[48:49]
	v_mov_b64_e32 v[64:65], v[36:37]
	v_mov_b64_e32 v[60:61], v[40:41]
	v_mov_b64_e32 v[56:57], v[44:45]
	s_and_b64 vcc, exec, s[2:3]
	v_mov_b64_e32 v[50:51], v[46:47]
	v_mov_b64_e32 v[62:63], v[34:35]
	v_mov_b64_e32 v[58:59], v[38:39]
	v_mov_b64_e32 v[54:55], v[42:43]
	s_cbranch_vccnz .LBB0_180
	v_pk_mul_f32 v[52:53], v[48:49], s[24:25] op_sel_hi:[1,0]
	v_pk_mul_f32 v[50:51], v[46:47], s[24:25] op_sel_hi:[1,0]
	v_pk_mul_f32 v[56:57], v[44:45], s[24:25] op_sel_hi:[1,0]
	v_pk_mul_f32 v[54:55], v[42:43], s[24:25] op_sel_hi:[1,0]
	v_pk_mul_f32 v[60:61], v[40:41], s[24:25] op_sel_hi:[1,0]
	v_pk_mul_f32 v[58:59], v[38:39], s[24:25] op_sel_hi:[1,0]
	v_pk_mul_f32 v[64:65], v[36:37], s[24:25] op_sel_hi:[1,0]
	v_pk_mul_f32 v[62:63], v[34:35], s[24:25] op_sel_hi:[1,0]

.LBB0_183:
	v_add_u32_e32 v34, 0x90, v168
	v_mad_i64_i32 v[38:39], s[38:39], v34, s86, v[162:163]
	v_cvt_pk_bf16_f32 v34, v50, v51
	v_cvt_pk_bf16_f32 v35, v52, v53
	v_cvt_pk_bf16_f32 v36, v54, v55
	v_cvt_pk_bf16_f32 v37, v56, v57
	global_store_dwordx4 v[38:39], v[34:37], off
	s_nop 1
	v_cvt_pk_bf16_f32 v34, v58, v59
	v_cvt_pk_bf16_f32 v35, v60, v61
	v_cvt_pk_bf16_f32 v36, v62, v63
	v_cvt_pk_bf16_f32 v37, v64, v65
	s_and_b64 vcc, exec, s[4:5]
	s_mov_b64 s[38:39], -1
	global_store_dwordx4 v[38:39], v[34:37], off offset:256
	s_cbranch_vccnz .LBB0_187
	s_nop 0
	v_mov_b64_e32 v[36:37], v[32:33]
	v_mov_b64_e32 v[48:49], v[20:21]
	v_mov_b64_e32 v[44:45], v[24:25]
	v_mov_b64_e32 v[40:41], v[28:29]
	s_and_b64 vcc, exec, s[2:3]
	v_mov_b64_e32 v[34:35], v[30:31]
	v_mov_b64_e32 v[46:47], v[18:19]
	v_mov_b64_e32 v[42:43], v[22:23]
	v_mov_b64_e32 v[38:39], v[26:27]
	s_cbranch_vccnz .LBB0_186
	v_pk_mul_f32 v[36:37], v[32:33], s[24:25] op_sel_hi:[1,0]
	v_pk_mul_f32 v[34:35], v[30:31], s[24:25] op_sel_hi:[1,0]
	v_pk_mul_f32 v[40:41], v[28:29], s[24:25] op_sel_hi:[1,0]
	v_pk_mul_f32 v[38:39], v[26:27], s[24:25] op_sel_hi:[1,0]
	v_pk_mul_f32 v[44:45], v[24:25], s[24:25] op_sel_hi:[1,0]
	v_pk_mul_f32 v[42:43], v[22:23], s[24:25] op_sel_hi:[1,0]
	v_pk_mul_f32 v[48:49], v[20:21], s[24:25] op_sel_hi:[1,0]
	v_pk_mul_f32 v[46:47], v[18:19], s[24:25] op_sel_hi:[1,0]

.LBB0_189:
	v_add_u32_e32 v18, 0xa0, v168
	v_mad_i64_i32 v[22:23], s[38:39], v18, s86, v[162:163]
	v_cvt_pk_bf16_f32 v18, v34, v35
	v_cvt_pk_bf16_f32 v19, v36, v37
	v_cvt_pk_bf16_f32 v20, v38, v39
	v_cvt_pk_bf16_f32 v21, v40, v41
	global_store_dwordx4 v[22:23], v[18:21], off
	s_nop 1
	v_cvt_pk_bf16_f32 v18, v42, v43
	v_cvt_pk_bf16_f32 v19, v44, v45
	v_cvt_pk_bf16_f32 v20, v46, v47
	v_cvt_pk_bf16_f32 v21, v48, v49
	s_and_b64 vcc, exec, s[4:5]
	s_mov_b64 s[4:5], -1
	global_store_dwordx4 v[22:23], v[18:21], off offset:256
	s_cbranch_vccnz .LBB0_193
	s_nop 0
	v_mov_b64_e32 v[20:21], v[16:17]
	v_mov_b64_e32 v[32:33], v[4:5]
	v_mov_b64_e32 v[28:29], v[8:9]
	v_mov_b64_e32 v[24:25], v[12:13]
	s_and_b64 vcc, exec, s[2:3]
	v_mov_b64_e32 v[18:19], v[14:15]
	v_mov_b64_e32 v[30:31], v[2:3]
	v_mov_b64_e32 v[26:27], v[6:7]
	v_mov_b64_e32 v[22:23], v[10:11]
	s_cbranch_vccnz .LBB0_192
	v_pk_mul_f32 v[20:21], v[16:17], s[24:25] op_sel_hi:[1,0]
	v_pk_mul_f32 v[18:19], v[14:15], s[24:25] op_sel_hi:[1,0]
	v_pk_mul_f32 v[24:25], v[12:13], s[24:25] op_sel_hi:[1,0]
	v_pk_mul_f32 v[22:23], v[10:11], s[24:25] op_sel_hi:[1,0]
	v_pk_mul_f32 v[28:29], v[8:9], s[24:25] op_sel_hi:[1,0]
	v_pk_mul_f32 v[26:27], v[6:7], s[24:25] op_sel_hi:[1,0]
	v_pk_mul_f32 v[32:33], v[4:5], s[24:25] op_sel_hi:[1,0]
	v_pk_mul_f32 v[30:31], v[2:3], s[24:25] op_sel_hi:[1,0]

.LBB0_195:
	v_add_u32_e32 v2, 0xb0, v168
	v_mad_i64_i32 v[6:7], s[2:3], v2, s86, v[162:163]
	v_cvt_pk_bf16_f32 v2, v18, v19
	v_cvt_pk_bf16_f32 v3, v20, v21
	v_cvt_pk_bf16_f32 v4, v22, v23
	v_cvt_pk_bf16_f32 v5, v24, v25
	global_store_dwordx4 v[6:7], v[2:5], off
	s_nop 1
	v_cvt_pk_bf16_f32 v2, v26, v27
	v_cvt_pk_bf16_f32 v3, v28, v29
	v_cvt_pk_bf16_f32 v4, v30, v31
	v_cvt_pk_bf16_f32 v5, v32, v33
	s_mov_b64 s[2:3], -1
	s_and_b64 vcc, exec, s[46:47]
	global_store_dwordx4 v[6:7], v[2:5], off offset:256
	s_cbranch_vccz .LBB0_139
	s_and_b64 vcc, exec, s[6:7]
	s_cbranch_vccz .LBB0_138
	s_barrier
	s_branch .LBB0_138

.LBB0_342:
	s_cmp_lg_u32 0, -1
	s_cselect_b32 s0, 0, 0
	s_addk_i32 s0, 0x6000
	v_add3_u32 v8, v237, s0, v233
	s_add_i32 s0, s33, 0x4000
	v_add_f32_e32 v2, v243, v2
	s_and_b32 s0, s0, 0xffff
	v_add3_u32 v16, v8, v236, s0
	ds_read_b64_tr_b16 v[8:9],v16 offset:0
	ds_read_b64_tr_b16 v[10:11],v16 offset:512
	ds_read_b64_tr_b16 v[12:13],v16 offset:1024
	ds_read_b64_tr_b16 v[14:15],v16 offset:1536
	ds_read_b64_tr_b16 v[82:83],v16 offset:2048
	ds_read_b64_tr_b16 v[84:85],v16 offset:2560
	ds_read_b64_tr_b16 v[86:87],v16 offset:3072
	ds_read_b64_tr_b16 v[88:89],v16 offset:3584
	s_waitcnt lgkmcnt(0)
	s_nop 0
	v_mfma_f32_32x32x16_bf16 v[66:81], v[138:141], v[8:11], v[66:81]
	ds_read_b64_tr_b16 v[8:9],v16 offset:4096
	ds_read_b64_tr_b16 v[10:11],v16 offset:4608
	v_mfma_f32_32x32x16_bf16 v[66:81], v[134:137], v[12:15], v[66:81]
	ds_read_b64_tr_b16 v[12:13],v16 offset:5120
	ds_read_b64_tr_b16 v[14:15],v16 offset:5632
	v_mfma_f32_32x32x16_bf16 v[66:81], v[130:133], v[82:85], v[66:81]
	ds_read_b64_tr_b16 v[82:83],v16 offset:6144
	ds_read_b64_tr_b16 v[84:85],v16 offset:6656
	ds_read_b64_tr_b16 v[90:91],v16 offset:7168
	ds_read_b64_tr_b16 v[92:93],v16 offset:7680
	s_waitcnt lgkmcnt(0)
	v_mfma_f32_32x32x16_bf16 v[66:81], v[4:7], v[86:89], v[66:81]
	v_mfma_f32_32x32x16_bf16 v[50:65], v[138:141], v[8:11], v[50:65]
	v_add_u32_e32 v16, 0x2000, v16
	ds_read_b64_tr_b16 v[8:9],v16 offset:0
	ds_read_b64_tr_b16 v[10:11],v16 offset:512
	v_mfma_f32_32x32x16_bf16 v[50:65], v[134:137], v[12:15], v[50:65]
	ds_read_b64_tr_b16 v[12:13],v16 offset:1024
	ds_read_b64_tr_b16 v[14:15],v16 offset:1536
	v_mfma_f32_32x32x16_bf16 v[50:65], v[130:133], v[82:85], v[50:65]
	ds_read_b64_tr_b16 v[82:83],v16 offset:2048
	ds_read_b64_tr_b16 v[84:85],v16 offset:2560
	ds_read_b64_tr_b16 v[86:87],v16 offset:3072
	ds_read_b64_tr_b16 v[88:89],v16 offset:3584
	s_waitcnt lgkmcnt(0)
	v_mfma_f32_32x32x16_bf16 v[50:65], v[4:7], v[90:93], v[50:65]
	v_mfma_f32_32x32x16_bf16 v[34:49], v[138:141], v[8:11], v[34:49]
	ds_read_b64_tr_b16 v[8:9],v16 offset:4096
	ds_read_b64_tr_b16 v[10:11],v16 offset:4608
	v_mfma_f32_32x32x16_bf16 v[34:49], v[134:137], v[12:15], v[34:49]
	ds_read_b64_tr_b16 v[12:13],v16 offset:5120
	ds_read_b64_tr_b16 v[14:15],v16 offset:5632
	v_mfma_f32_32x32x16_bf16 v[34:49], v[130:133], v[82:85], v[34:49]
	ds_read_b64_tr_b16 v[82:83],v16 offset:6144
	ds_read_b64_tr_b16 v[84:85],v16 offset:6656
	ds_read_b64_tr_b16 v[90:91],v16 offset:7168
	ds_read_b64_tr_b16 v[92:93],v16 offset:7680
	s_waitcnt lgkmcnt(0)
	v_mfma_f32_32x32x16_bf16 v[34:49], v[4:7], v[86:89], v[34:49]
	v_mfma_f32_32x32x16_bf16 v[18:33], v[138:141], v[8:11], v[18:33]
	v_mov_b32_e32 v8, v2
	s_nop 1
	v_permlane32_swap_b32_e32 v2, v8
	v_cmp_gt_u32_e32 vcc, 32, v230
	v_mfma_f32_32x32x16_bf16 v[18:33], v[134:137], v[12:15], v[18:33]
	v_mfma_f32_32x32x16_bf16 v[18:33], v[130:133], v[82:85], v[18:33]
	v_mfma_f32_32x32x16_bf16 v[18:33], v[4:7], v[90:93], v[18:33]
	s_and_saveexec_b64 s[0:1], vcc
	v_add_f32_e32 v2, v2, v8
	ds_write_b32 v235, v2 offset:128
	s_or_b64 exec, exec, s[0:1]
	s_waitcnt lgkmcnt(0)
	ds_read_b128 v[4:7], v234 offset:128
	ds_read_b128 v[8:11], v234 offset:160
	s_lshl_b32 s0, s84, 8
	s_add_u32 s2, s6, s0
	s_addc_u32 s3, s7, 0
	s_waitcnt lgkmcnt(1)
	v_rcp_f32_e32 v14, v4
	v_rcp_f32_e32 v15, v5
	v_rcp_f32_e32 v16, v6
	v_rcp_f32_e32 v17, v7
	ds_read_b128 v[4:7], v234 offset:192
	s_lshl_b64 s[0:1], s[34:35], 11
	s_add_u32 s0, s2, s0
	s_addc_u32 s1, s3, s1
	s_lshl_b32 s2, s83, 12
	s_add_i32 s2, s2, 0
	v_lshlrev_b32_e32 v2, 1, v232
	s_add_i32 s2, s2, 0x16800
	v_and_b32_e32 v2, 0x70, v2
	s_waitcnt lgkmcnt(1)
	v_rcp_f32_e32 v82, v8
	v_rcp_f32_e32 v83, v9
	v_rcp_f32_e32 v84, v10
	v_rcp_f32_e32 v85, v11
	ds_read_b128 v[8:11], v234 offset:224
	s_waitcnt lgkmcnt(1)
	v_rcp_f32_e32 v86, v4
	v_lshlrev_b32_e32 v4, 1, v231
	v_add_u32_e32 v95, s2, v2
	v_lshl_add_u64 v[12:13], s[0:1], 0, v[2:3]
	v_lshlrev_b32_e32 v2, 9, v229
	v_add3_u32 v97, s2, v4, v2
	v_mul_f32_e32 v2, v66, v14
	v_cvt_pk_bf16_f32 v2, v2, s0
	ds_write_b16 v97, v2
	v_mul_f32_e32 v2, v50, v14
	v_cvt_pk_bf16_f32 v2, v2, s0
	ds_write_b16 v97, v2 offset:64
	v_mul_f32_e32 v2, v67, v15
	v_cvt_pk_bf16_f32 v2, v2, s0
	ds_write_b16 v97, v2 offset:128
	v_mul_f32_e32 v2, v51, v15
	v_cvt_pk_bf16_f32 v2, v2, s0
	ds_write_b16 v97, v2 offset:192
	v_mul_f32_e32 v2, v68, v16
	v_cvt_pk_bf16_f32 v2, v2, s0
	ds_write_b16 v97, v2 offset:256
	v_mul_f32_e32 v2, v52, v16
	v_cvt_pk_bf16_f32 v2, v2, s0
	ds_write_b16 v97, v2 offset:320
	v_mul_f32_e32 v2, v69, v17
	v_cvt_pk_bf16_f32 v2, v2, s0
	ds_write_b16 v97, v2 offset:384
	v_mul_f32_e32 v2, v53, v17
	v_cvt_pk_bf16_f32 v2, v2, s0
	ds_write_b16 v97, v2 offset:448
	v_mul_f32_e32 v2, v70, v82
	v_cvt_pk_bf16_f32 v2, v2, s0
	ds_write_b16 v97, v2 offset:1024
	v_mul_f32_e32 v2, v54, v82
	v_cvt_pk_bf16_f32 v2, v2, s0
	ds_write_b16 v97, v2 offset:1088
	v_mul_f32_e32 v2, v71, v83
	v_cvt_pk_bf16_f32 v2, v2, s0
	ds_write_b16 v97, v2 offset:1152
	v_mul_f32_e32 v2, v55, v83
	v_cvt_pk_bf16_f32 v2, v2, s0
	ds_write_b16 v97, v2 offset:1216
	v_mul_f32_e32 v2, v72, v84
	v_cvt_pk_bf16_f32 v2, v2, s0
	ds_write_b16 v97, v2 offset:1280
	v_mul_f32_e32 v2, v56, v84
	v_cvt_pk_bf16_f32 v2, v2, s0
	ds_write_b16 v97, v2 offset:1344
	v_mul_f32_e32 v2, v73, v85
	v_cvt_pk_bf16_f32 v2, v2, s0
	ds_write_b16 v97, v2 offset:1408
	v_mul_f32_e32 v2, v57, v85
	v_cvt_pk_bf16_f32 v2, v2, s0
	v_rcp_f32_e32 v87, v5
	ds_write_b16 v97, v2 offset:1472
	v_mul_f32_e32 v2, v74, v86
	v_cvt_pk_bf16_f32 v2, v2, s0
	ds_write_b16 v97, v2 offset:2048
	v_mul_f32_e32 v2, v58, v86
	v_cvt_pk_bf16_f32 v2, v2, s0
	v_rcp_f32_e32 v88, v6
	ds_write_b16 v97, v2 offset:2112
	v_mul_f32_e32 v2, v75, v87
	v_cvt_pk_bf16_f32 v2, v2, s0
	ds_write_b16 v97, v2 offset:2176
	v_mul_f32_e32 v2, v59, v87
	v_cvt_pk_bf16_f32 v2, v2, s0
	v_rcp_f32_e32 v89, v7
	ds_write_b16 v97, v2 offset:2240
	v_mul_f32_e32 v2, v76, v88
	v_cvt_pk_bf16_f32 v2, v2, s0
	ds_write_b16 v97, v2 offset:2304
	v_mul_f32_e32 v2, v60, v88
	v_cvt_pk_bf16_f32 v2, v2, s0
	s_waitcnt lgkmcnt(14)
	v_rcp_f32_e32 v90, v8
	ds_write_b16 v97, v2 offset:2368
	v_mul_f32_e32 v2, v77, v89
	v_cvt_pk_bf16_f32 v2, v2, s0
	ds_write_b16 v97, v2 offset:2432
	v_mul_f32_e32 v2, v61, v89
	v_cvt_pk_bf16_f32 v2, v2, s0
	v_rcp_f32_e32 v91, v9
	ds_write_b16 v97, v2 offset:2496
	v_mul_f32_e32 v2, v78, v90
	v_cvt_pk_bf16_f32 v2, v2, s0
	ds_write_b16 v97, v2 offset:3072
	v_mul_f32_e32 v2, v62, v90
	v_cvt_pk_bf16_f32 v2, v2, s0
	v_rcp_f32_e32 v92, v10
	ds_write_b16 v97, v2 offset:3136
	v_mul_f32_e32 v2, v79, v91
	v_cvt_pk_bf16_f32 v2, v2, s0
	ds_write_b16 v97, v2 offset:3200
	v_mul_f32_e32 v2, v63, v91
	v_cvt_pk_bf16_f32 v2, v2, s0
	v_rcp_f32_e32 v93, v11
	ds_write_b16 v97, v2 offset:3264
	v_mul_f32_e32 v2, v80, v92
	v_cvt_pk_bf16_f32 v2, v2, s0
	ds_write_b16 v97, v2 offset:3328
	v_mul_f32_e32 v2, v64, v92
	v_cvt_pk_bf16_f32 v2, v2, s0
	ds_write_b16 v97, v2 offset:3392
	v_mul_f32_e32 v2, v81, v93
	v_cvt_pk_bf16_f32 v2, v2, s0
	ds_write_b16 v97, v2 offset:3456
	v_mul_f32_e32 v2, v65, v93
	v_lshrrev_b32_e32 v94, 3, v230
	v_cvt_pk_bf16_f32 v2, v2, s0
	ds_write_b16 v97, v2 offset:3520
	v_or_b32_e32 v52, 8, v94
	v_lshl_add_u32 v96, v94, 7, v95
	s_waitcnt lgkmcnt(0)
	v_lshl_add_u32 v58, v52, 7, v95
	ds_read_b128 v[4:7], v96
	ds_read_b128 v[8:11], v58
	v_lshlrev_b32_e32 v2, 11, v94
	v_lshl_add_u64 v[50:51], v[12:13], 0, v[2:3]
	v_lshlrev_b32_e32 v2, 11, v52
	v_lshl_add_u64 v[52:53], v[12:13], 0, v[2:3]
	v_or_b32_e32 v2, 16, v94
	v_or_b32_e32 v56, 24, v94
	v_lshl_add_u32 v59, v2, 7, v95
	v_lshl_add_u32 v60, v56, 7, v95
	s_waitcnt lgkmcnt(1)
	global_store_dwordx4 v[50:51], v[4:7], off
	ds_read_b128 v[4:7], v59
	s_waitcnt lgkmcnt(1)
	global_store_dwordx4 v[52:53], v[8:11], off
	ds_read_b128 v[8:11], v60
	v_lshlrev_b32_e32 v2, 11, v2
	v_lshl_add_u64 v[54:55], v[12:13], 0, v[2:3]
	v_lshlrev_b32_e32 v2, 11, v56
	v_lshl_add_u64 v[56:57], v[12:13], 0, v[2:3]
	v_mul_f32_e32 v2, v34, v14
	s_waitcnt lgkmcnt(1)
	global_store_dwordx4 v[54:55], v[4:7], off
	s_waitcnt lgkmcnt(0)
	global_store_dwordx4 v[56:57], v[8:11], off
	v_cvt_pk_bf16_f32 v2, v2, s0
	s_waitcnt lgkmcnt(0)
	ds_write_b16 v97, v2
	v_mul_f32_e32 v2, v18, v14
	v_cvt_pk_bf16_f32 v2, v2, s0
	ds_write_b16 v97, v2 offset:64
	v_mul_f32_e32 v2, v35, v15
	v_cvt_pk_bf16_f32 v2, v2, s0
	ds_write_b16 v97, v2 offset:128
	v_mul_f32_e32 v2, v19, v15
	v_cvt_pk_bf16_f32 v2, v2, s0
	ds_write_b16 v97, v2 offset:192
	v_mul_f32_e32 v2, v36, v16
	v_cvt_pk_bf16_f32 v2, v2, s0
	ds_write_b16 v97, v2 offset:256
	v_mul_f32_e32 v2, v20, v16
	v_cvt_pk_bf16_f32 v2, v2, s0
	ds_write_b16 v97, v2 offset:320
	v_mul_f32_e32 v2, v37, v17
	v_cvt_pk_bf16_f32 v2, v2, s0
	ds_write_b16 v97, v2 offset:384
	v_mul_f32_e32 v2, v21, v17
	v_cvt_pk_bf16_f32 v2, v2, s0
	ds_write_b16 v97, v2 offset:448
	v_mul_f32_e32 v2, v38, v82
	v_cvt_pk_bf16_f32 v2, v2, s0
	ds_write_b16 v97, v2 offset:1024
	v_mul_f32_e32 v2, v22, v82
	v_cvt_pk_bf16_f32 v2, v2, s0
	ds_write_b16 v97, v2 offset:1088
	v_mul_f32_e32 v2, v39, v83
	v_cvt_pk_bf16_f32 v2, v2, s0
	ds_write_b16 v97, v2 offset:1152
	v_mul_f32_e32 v2, v23, v83
	v_cvt_pk_bf16_f32 v2, v2, s0
	ds_write_b16 v97, v2 offset:1216
	v_mul_f32_e32 v2, v40, v84
	v_cvt_pk_bf16_f32 v2, v2, s0
	ds_write_b16 v97, v2 offset:1280
	v_mul_f32_e32 v2, v24, v84
	v_cvt_pk_bf16_f32 v2, v2, s0
	ds_write_b16 v97, v2 offset:1344
	v_mul_f32_e32 v2, v41, v85
	v_cvt_pk_bf16_f32 v2, v2, s0
	ds_write_b16 v97, v2 offset:1408
	v_mul_f32_e32 v2, v25, v85
	v_cvt_pk_bf16_f32 v2, v2, s0
	ds_write_b16 v97, v2 offset:1472
	v_mul_f32_e32 v2, v42, v86
	v_cvt_pk_bf16_f32 v2, v2, s0
	ds_write_b16 v97, v2 offset:2048
	v_mul_f32_e32 v2, v26, v86
	v_cvt_pk_bf16_f32 v2, v2, s0
	ds_write_b16 v97, v2 offset:2112
	v_mul_f32_e32 v2, v43, v87
	v_cvt_pk_bf16_f32 v2, v2, s0
	ds_write_b16 v97, v2 offset:2176
	v_mul_f32_e32 v2, v27, v87
	v_cvt_pk_bf16_f32 v2, v2, s0
	ds_write_b16 v97, v2 offset:2240
	v_mul_f32_e32 v2, v44, v88
	v_cvt_pk_bf16_f32 v2, v2, s0
	ds_write_b16 v97, v2 offset:2304
	v_mul_f32_e32 v2, v28, v88
	v_cvt_pk_bf16_f32 v2, v2, s0
	ds_write_b16 v97, v2 offset:2368
	v_mul_f32_e32 v2, v45, v89
	v_cvt_pk_bf16_f32 v2, v2, s0
	ds_write_b16 v97, v2 offset:2432
	v_mul_f32_e32 v2, v29, v89
	v_cvt_pk_bf16_f32 v2, v2, s0
	ds_write_b16 v97, v2 offset:2496
	v_mul_f32_e32 v2, v46, v90
	v_cvt_pk_bf16_f32 v2, v2, s0
	ds_write_b16 v97, v2 offset:3072
	v_mul_f32_e32 v2, v30, v90
	v_cvt_pk_bf16_f32 v2, v2, s0
	ds_write_b16 v97, v2 offset:3136
	v_mul_f32_e32 v2, v47, v91
	v_cvt_pk_bf16_f32 v2, v2, s0
	ds_write_b16 v97, v2 offset:3200
	v_mul_f32_e32 v2, v31, v91
	v_cvt_pk_bf16_f32 v2, v2, s0
	ds_write_b16 v97, v2 offset:3264
	v_mul_f32_e32 v2, v48, v92
	v_cvt_pk_bf16_f32 v2, v2, s0
	ds_write_b16 v97, v2 offset:3328
	v_mul_f32_e32 v2, v32, v92
	v_cvt_pk_bf16_f32 v2, v2, s0
	ds_write_b16 v97, v2 offset:3392
	v_mul_f32_e32 v2, v49, v93
	v_cvt_pk_bf16_f32 v2, v2, s0
	ds_write_b16 v97, v2 offset:3456
	v_mul_f32_e32 v2, v33, v93
	v_cvt_pk_bf16_f32 v2, v2, s0
	ds_write_b16 v97, v2 offset:3520
	s_waitcnt lgkmcnt(0)
	ds_read_b128 v[4:7], v96
	ds_read_b128 v[8:11], v58
	ds_read_b128 v[12:15], v59
	ds_read_b128 v[16:19], v60
	s_waitcnt lgkmcnt(3)
	global_store_dwordx4 v[50:51], v[4:7], off offset:128
	s_waitcnt lgkmcnt(2)
	global_store_dwordx4 v[52:53], v[8:11], off offset:128
	s_waitcnt lgkmcnt(1)
	global_store_dwordx4 v[54:55], v[12:15], off offset:128
	s_waitcnt lgkmcnt(0)
	global_store_dwordx4 v[56:57], v[16:19], off offset:128
	s_waitcnt lgkmcnt(0)
	s_waitcnt lgkmcnt(0)
	s_barrier
	s_cmp_lt_u32 s21, 2
	s_cbranch_scc1 .LBB0_259
	v_mov_b32_e32 v6, v0
	s_lshl_b32 s0, s82, 8
	v_ashrrev_i32_e32 v4, 1, v6
	s_or_b32 s0, s8, s0
	s_mov_b32 s1, s9
	v_ashrrev_i32_e32 v5, 31, v4
	v_lshl_add_u64 v[12:13], s[0:1], 0, v[4:5]
	v_lshlrev_b32_e32 v2, 6, v6
	v_lshlrev_b64 v[4:5], 11, v[12:13]
	v_and_b32_e32 v7, 64, v2
	v_lshl_add_u64 v[4:5], s[6:7], 0, v[4:5]
	v_lshlrev_b32_e32 v2, 1, v7
	v_lshl_add_u64 v[4:5], v[4:5], 0, v[2:3]
	s_waitcnt vmcnt(0)
	s_barrier
	global_load_dwordx2 v[16:17], v[4:5], off sc1
	global_load_dwordx2 v[18:19], v[4:5], off offset:256 sc1
	global_load_dwordx2 v[24:25], v[4:5], off offset:8 sc1
	global_load_dwordx2 v[26:27], v[4:5], off offset:264 sc1
	global_load_dwordx2 v[30:31], v[4:5], off offset:16 sc1
	global_load_dwordx2 v[34:35], v[4:5], off offset:272 sc1
	global_load_dwordx2 v[42:43], v[4:5], off offset:24 sc1
	global_load_dwordx2 v[50:51], v[4:5], off offset:280 sc1
	v_lshlrev_b32_e32 v6, 2, v6
	v_bitop3_b32 v83, v6, 4, v228 bitop3:0x6c
	v_lshlrev_b32_e32 v82, 2, v7
	global_load_dwordx2 v[54:55], v[4:5], off offset:32 sc1
	global_load_dwordx2 v[60:61], v[4:5], off offset:288 sc1
	global_load_dwordx2 v[74:75], v[4:5], off offset:40 sc1
	global_load_dwordx2 v[84:85], v[4:5], off offset:296 sc1
	global_load_dwordx2 v[86:87], v[4:5], off offset:48 sc1
	global_load_dwordx2 v[88:89], v[4:5], off offset:304 sc1
	global_load_dwordx2 v[90:91], v[4:5], off offset:56 sc1
	global_load_dwordx2 v[28:29], v[4:5], off offset:312 sc1
	global_load_dwordx2 v[58:59], v[4:5], off offset:64 sc1
	global_load_dwordx2 v[36:37], v[4:5], off offset:320 sc1
	global_load_dwordx2 v[66:67], v[4:5], off offset:72 sc1
	global_load_dwordx2 v[44:45], v[4:5], off offset:328 sc1
	global_load_dwordx2 v[62:63], v[4:5], off offset:80 sc1
	global_load_dwordx2 v[52:53], v[4:5], off offset:336 sc1
	global_load_dwordx2 v[76:77], v[4:5], off offset:88 sc1
	global_load_dwordx2 v[32:33], v[4:5], off offset:344 sc1
	global_load_dwordx2 v[68:69], v[4:5], off offset:96 sc1
	global_load_dwordx2 v[38:39], v[4:5], off offset:352 sc1
	global_load_dwordx2 v[80:81], v[4:5], off offset:104 sc1
	global_load_dwordx2 v[20:21], v[4:5], off offset:360 sc1
	global_load_dwordx2 v[46:47], v[4:5], off offset:112 sc1
	global_load_dwordx2 v[22:23], v[4:5], off offset:368 sc1
	global_load_dwordx2 v[56:57], v[4:5], off offset:120 sc1
	global_load_dwordx2 v[48:49], v[4:5], off offset:376 sc1
	s_nop 0
	global_load_dwordx4 v[4:7], v82, s[58:59] offset:16
	global_load_dwordx4 v[8:11], v82, s[58:59]
	v_mov_b64_e32 v[14:15], s[24:25]
	v_mad_u64_u32 v[14:15], s[0:1], v12, s5, v[14:15]
	v_mad_i32_i24 v15, v13, s5, v15
	v_lshl_add_u64 v[12:13], v[14:15], 0, v[2:3]
	s_mov_b32 s0, 0xf800000
	s_waitcnt vmcnt(33)
	v_lshlrev_b32_e32 v41, 16, v17
	v_lshlrev_b32_e32 v40, 16, v16
	s_waitcnt vmcnt(32)
	v_lshlrev_b32_e32 v65, 16, v19
	v_lshlrev_b32_e32 v64, 16, v18
	v_and_b32_e32 v17, 0xffff0000, v17
	v_and_b32_e32 v16, 0xffff0000, v16
	v_and_b32_e32 v19, 0xffff0000, v19
	v_and_b32_e32 v18, 0xffff0000, v18
	s_waitcnt vmcnt(29)
	v_lshlrev_b32_e32 v95, 16, v31
	v_lshlrev_b32_e32 v94, 16, v30
	s_waitcnt vmcnt(28)
	v_lshlrev_b32_e32 v97, 16, v35
	v_lshlrev_b32_e32 v96, 16, v34
	v_and_b32_e32 v31, 0xffff0000, v31
	v_and_b32_e32 v30, 0xffff0000, v30
	v_and_b32_e32 v35, 0xffff0000, v35
	v_and_b32_e32 v34, 0xffff0000, v34
	v_pk_fma_f32 v[72:73], v[214:215], v[18:19], v[16:17] neg_lo:[1,0,0] neg_hi:[1,0,0]
	v_pk_fma_f32 v[18:19], v[214:215], v[96:97], v[94:95] neg_lo:[1,0,0] neg_hi:[1,0,0]
	v_pk_fma_f32 v[16:17], v[214:215], v[34:35], v[30:31] neg_lo:[1,0,0] neg_hi:[1,0,0]
	v_lshlrev_b32_e32 v71, 16, v25
	v_lshlrev_b32_e32 v70, 16, v24
	v_lshlrev_b32_e32 v93, 16, v27
	v_lshlrev_b32_e32 v92, 16, v26
	v_and_b32_e32 v25, 0xffff0000, v25
	v_and_b32_e32 v24, 0xffff0000, v24
	v_and_b32_e32 v27, 0xffff0000, v27
	v_and_b32_e32 v26, 0xffff0000, v26
	v_mov_b32_e32 v30, v18
	v_mov_b32_e32 v31, v16
	v_mul_f32_e32 v34, v16, v16
	v_pk_fma_f32 v[78:79], v[214:215], v[64:65], v[40:41] neg_lo:[1,0,0] neg_hi:[1,0,0]
	v_pk_fma_f32 v[64:65], v[214:215], v[26:27], v[24:25] neg_lo:[1,0,0] neg_hi:[1,0,0]
	v_pk_fma_f32 v[30:31], v[30:31], v[30:31], v[34:35] op_sel_hi:[1,1,0]
	v_mov_b32_e32 v34, v19
	v_mov_b32_e32 v35, v17
	v_mul_f32_e32 v40, v17, v17
	v_pk_fma_f32 v[70:71], v[214:215], v[92:93], v[70:71] neg_lo:[1,0,0] neg_hi:[1,0,0]
	v_pk_mul_f32 v[24:25], v[72:73], v[72:73]
	v_pk_mul_f32 v[26:27], v[64:65], v[64:65]
	v_pk_fma_f32 v[34:35], v[34:35], v[34:35], v[40:41] op_sel_hi:[1,1,0]
	s_waitcnt vmcnt(27)
	v_lshlrev_b32_e32 v41, 16, v43
	v_lshlrev_b32_e32 v40, 16, v42
	s_waitcnt vmcnt(26)
	v_lshlrev_b32_e32 v93, 16, v51
	v_lshlrev_b32_e32 v92, 16, v50
	v_and_b32_e32 v43, 0xffff0000, v43
	v_and_b32_e32 v42, 0xffff0000, v42
	v_and_b32_e32 v51, 0xffff0000, v51
	v_and_b32_e32 v50, 0xffff0000, v50
	v_pk_fma_f32 v[24:25], v[78:79], v[78:79], v[24:25]
	v_pk_fma_f32 v[26:27], v[70:71], v[70:71], v[26:27]
	v_pk_fma_f32 v[40:41], v[214:215], v[92:93], v[40:41] neg_lo:[1,0,0] neg_hi:[1,0,0]
	v_pk_fma_f32 v[50:51], v[214:215], v[50:51], v[42:43] neg_lo:[1,0,0] neg_hi:[1,0,0]
	v_pk_add_f32 v[24:25], v[24:25], v[24:25] op_sel:[0,1] op_sel_hi:[1,0]
	v_pk_add_f32 v[26:27], v[26:27], v[26:27] op_sel:[0,1] op_sel_hi:[1,0]
	v_pk_mul_f32 v[42:43], v[40:41], v[40:41]
	v_pk_mul_f32 v[92:93], v[50:51], v[50:51]
	v_mov_b32_e32 v25, v42
	v_mov_b32_e32 v27, v92
	v_mov_b32_e32 v31, v43
	v_mov_b32_e32 v35, v93
	v_pk_add_f32 v[24:25], v[24:25], v[26:27]
	v_pk_add_f32 v[26:27], v[30:31], v[34:35]
	s_waitcnt vmcnt(24)
	v_and_b32_e32 v31, 0xffff0000, v61
	v_pk_add_f32 v[24:25], v[24:25], v[26:27]
	v_lshlrev_b32_e32 v27, 16, v61
	v_pk_add_f32 v[92:93], v[24:25], v[24:25] op_sel:[0,1] op_sel_hi:[1,0]
	v_lshlrev_b32_e32 v25, 16, v55
	v_lshlrev_b32_e32 v24, 16, v54
	v_lshlrev_b32_e32 v26, 16, v60
	v_pk_fma_f32 v[26:27], v[214:215], v[26:27], v[24:25] neg_lo:[1,0,0] neg_hi:[1,0,0]
	v_and_b32_e32 v25, 0xffff0000, v55
	v_and_b32_e32 v24, 0xffff0000, v54
	v_and_b32_e32 v30, 0xffff0000, v60
	v_pk_fma_f32 v[34:35], v[214:215], v[30:31], v[24:25] neg_lo:[1,0,0] neg_hi:[1,0,0]
	s_waitcnt vmcnt(22)
	v_lshlrev_b32_e32 v31, 16, v85
	v_pk_mul_f32 v[24:25], v[34:35], v[34:35]
	v_lshlrev_b32_e32 v30, 16, v84
	v_pk_fma_f32 v[24:25], v[26:27], v[26:27], v[24:25]
	s_waitcnt vmcnt(0)
	v_mov_b32_e32 v15, v10
	v_pk_add_f32 v[60:61], v[24:25], v[24:25] op_sel:[0,1] op_sel_hi:[1,0]
	v_lshlrev_b32_e32 v25, 16, v75
	v_lshlrev_b32_e32 v24, 16, v74
	v_pk_fma_f32 v[42:43], v[214:215], v[30:31], v[24:25] neg_lo:[1,0,0] neg_hi:[1,0,0]
	v_and_b32_e32 v25, 0xffff0000, v75
	v_and_b32_e32 v24, 0xffff0000, v74
	v_and_b32_e32 v31, 0xffff0000, v85
	v_and_b32_e32 v30, 0xffff0000, v84
	v_pk_fma_f32 v[54:55], v[214:215], v[30:31], v[24:25] neg_lo:[1,0,0] neg_hi:[1,0,0]
	v_mov_b32_e32 v24, v42
	v_mov_b32_e32 v25, v54
	v_mul_f32_e32 v30, v54, v54
	v_pk_fma_f32 v[74:75], v[24:25], v[24:25], v[30:31] op_sel_hi:[1,1,0]
	v_mov_b32_e32 v24, v43
	v_mov_b32_e32 v25, v55
	v_mul_f32_e32 v30, v55, v55
	v_pk_fma_f32 v[84:85], v[24:25], v[24:25], v[30:31] op_sel_hi:[1,1,0]
	v_lshlrev_b32_e32 v25, 16, v87
	v_lshlrev_b32_e32 v24, 16, v86
	v_lshlrev_b32_e32 v31, 16, v89
	v_lshlrev_b32_e32 v30, 16, v88
	v_pk_fma_f32 v[24:25], v[214:215], v[30:31], v[24:25] neg_lo:[1,0,0] neg_hi:[1,0,0]
	v_and_b32_e32 v31, 0xffff0000, v87
	v_and_b32_e32 v30, 0xffff0000, v86
	v_and_b32_e32 v87, 0xffff0000, v89
	v_and_b32_e32 v86, 0xffff0000, v88
	v_pk_fma_f32 v[30:31], v[214:215], v[86:87], v[30:31] neg_lo:[1,0,0] neg_hi:[1,0,0]
	v_pk_mul_f32 v[86:87], v[24:25], v[24:25]
	v_pk_mul_f32 v[88:89], v[30:31], v[30:31]
	v_mov_b32_e32 v93, v86
	v_mov_b32_e32 v61, v88
	v_mov_b32_e32 v75, v87
	v_mov_b32_e32 v85, v89
	v_pk_add_f32 v[60:61], v[92:93], v[60:61]
	v_pk_add_f32 v[74:75], v[74:75], v[84:85]
	v_lshlrev_b32_e32 v89, 16, v37
	v_pk_add_f32 v[60:61], v[60:61], v[74:75]
	v_lshlrev_b32_e32 v75, 16, v29
	v_pk_add_f32 v[84:85], v[60:61], v[60:61] op_sel:[0,1] op_sel_hi:[1,0]
	v_lshlrev_b32_e32 v61, 16, v91
	v_lshlrev_b32_e32 v60, 16, v90
	v_lshlrev_b32_e32 v74, 16, v28
	v_pk_fma_f32 v[60:61], v[214:215], v[74:75], v[60:61] neg_lo:[1,0,0] neg_hi:[1,0,0]
	v_and_b32_e32 v75, 0xffff0000, v91
	v_and_b32_e32 v74, 0xffff0000, v90
	v_and_b32_e32 v29, 0xffff0000, v29
	v_and_b32_e32 v28, 0xffff0000, v28
	v_pk_fma_f32 v[74:75], v[214:215], v[28:29], v[74:75] neg_lo:[1,0,0] neg_hi:[1,0,0]
	v_lshlrev_b32_e32 v88, 16, v36
	v_pk_mul_f32 v[28:29], v[74:75], v[74:75]
	v_and_b32_e32 v37, 0xffff0000, v37
	v_pk_fma_f32 v[28:29], v[60:61], v[60:61], v[28:29]
	v_and_b32_e32 v36, 0xffff0000, v36
	v_pk_add_f32 v[86:87], v[28:29], v[28:29] op_sel:[0,1] op_sel_hi:[1,0]
	v_lshlrev_b32_e32 v29, 16, v59
	v_lshlrev_b32_e32 v28, 16, v58
	v_and_b32_e32 v59, 0xffff0000, v59
	v_and_b32_e32 v58, 0xffff0000, v58
	v_pk_fma_f32 v[28:29], v[214:215], v[88:89], v[28:29] neg_lo:[1,0,0] neg_hi:[1,0,0]
	v_pk_fma_f32 v[36:37], v[214:215], v[36:37], v[58:59] neg_lo:[1,0,0] neg_hi:[1,0,0]
	v_mov_b32_e32 v58, v28
	v_mov_b32_e32 v59, v36
	v_mul_f32_e32 v88, v36, v36
	v_pk_fma_f32 v[88:89], v[58:59], v[58:59], v[88:89] op_sel_hi:[1,1,0]
	v_mov_b32_e32 v58, v29
	v_mov_b32_e32 v59, v37
	v_mul_f32_e32 v90, v37, v37
	v_pk_fma_f32 v[90:91], v[58:59], v[58:59], v[90:91] op_sel_hi:[1,1,0]
	v_lshlrev_b32_e32 v59, 16, v67
	v_lshlrev_b32_e32 v58, 16, v66
	v_lshlrev_b32_e32 v93, 16, v45
	v_lshlrev_b32_e32 v92, 16, v44
	v_and_b32_e32 v67, 0xffff0000, v67
	v_and_b32_e32 v66, 0xffff0000, v66
	v_and_b32_e32 v45, 0xffff0000, v45
	v_and_b32_e32 v44, 0xffff0000, v44
	v_pk_fma_f32 v[58:59], v[214:215], v[92:93], v[58:59] neg_lo:[1,0,0] neg_hi:[1,0,0]
	v_pk_fma_f32 v[66:67], v[214:215], v[44:45], v[66:67] neg_lo:[1,0,0] neg_hi:[1,0,0]
	v_pk_mul_f32 v[44:45], v[58:59], v[58:59]
	v_pk_mul_f32 v[92:93], v[66:67], v[66:67]
	v_mov_b32_e32 v85, v44
	v_mov_b32_e32 v87, v92
	v_mov_b32_e32 v89, v45
	v_mov_b32_e32 v91, v93
	v_pk_add_f32 v[84:85], v[84:85], v[86:87]
	v_pk_add_f32 v[44:45], v[88:89], v[90:91]
	v_lshlrev_b32_e32 v87, 16, v53
	v_pk_add_f32 v[44:45], v[84:85], v[44:45]
	v_lshlrev_b32_e32 v86, 16, v52
	v_pk_add_f32 v[84:85], v[44:45], v[44:45] op_sel:[0,1] op_sel_hi:[1,0]
	v_lshlrev_b32_e32 v45, 16, v63
	v_lshlrev_b32_e32 v44, 16, v62
	v_and_b32_e32 v63, 0xffff0000, v63
	v_and_b32_e32 v62, 0xffff0000, v62
	v_and_b32_e32 v53, 0xffff0000, v53
	v_and_b32_e32 v52, 0xffff0000, v52
	v_pk_fma_f32 v[52:53], v[214:215], v[52:53], v[62:63] neg_lo:[1,0,0] neg_hi:[1,0,0]
	v_pk_fma_f32 v[44:45], v[214:215], v[86:87], v[44:45] neg_lo:[1,0,0] neg_hi:[1,0,0]
	v_pk_mul_f32 v[62:63], v[52:53], v[52:53]
	v_lshlrev_b32_e32 v89, 16, v33
	v_pk_fma_f32 v[62:63], v[44:45], v[44:45], v[62:63]
	v_lshlrev_b32_e32 v88, 16, v32
	v_pk_add_f32 v[86:87], v[62:63], v[62:63] op_sel:[0,1] op_sel_hi:[1,0]
	v_lshlrev_b32_e32 v63, 16, v77
	v_lshlrev_b32_e32 v62, 16, v76
	v_and_b32_e32 v77, 0xffff0000, v77
	v_and_b32_e32 v76, 0xffff0000, v76
	v_and_b32_e32 v33, 0xffff0000, v33
	v_and_b32_e32 v32, 0xffff0000, v32
	v_pk_fma_f32 v[62:63], v[214:215], v[88:89], v[62:63] neg_lo:[1,0,0] neg_hi:[1,0,0]
	v_pk_fma_f32 v[76:77], v[214:215], v[32:33], v[76:77] neg_lo:[1,0,0] neg_hi:[1,0,0]
	v_mov_b32_e32 v32, v62
	v_mov_b32_e32 v33, v76
	v_mul_f32_e32 v88, v76, v76
	v_pk_fma_f32 v[88:89], v[32:33], v[32:33], v[88:89] op_sel_hi:[1,1,0]
	v_mov_b32_e32 v32, v63
	v_mov_b32_e32 v33, v77
	v_mul_f32_e32 v90, v77, v77
	v_pk_fma_f32 v[90:91], v[32:33], v[32:33], v[90:91] op_sel_hi:[1,1,0]
	v_lshlrev_b32_e32 v33, 16, v69
	v_lshlrev_b32_e32 v32, 16, v68
	v_lshlrev_b32_e32 v93, 16, v39
	v_lshlrev_b32_e32 v92, 16, v38
	v_and_b32_e32 v69, 0xffff0000, v69
	v_and_b32_e32 v68, 0xffff0000, v68
	v_and_b32_e32 v39, 0xffff0000, v39
	v_and_b32_e32 v38, 0xffff0000, v38
	v_pk_fma_f32 v[32:33], v[214:215], v[92:93], v[32:33] neg_lo:[1,0,0] neg_hi:[1,0,0]
	v_pk_fma_f32 v[38:39], v[214:215], v[38:39], v[68:69] neg_lo:[1,0,0] neg_hi:[1,0,0]
	v_pk_mul_f32 v[68:69], v[32:33], v[32:33]
	v_pk_mul_f32 v[92:93], v[38:39], v[38:39]
	v_mov_b32_e32 v85, v68
	v_mov_b32_e32 v87, v92
	v_mov_b32_e32 v89, v69
	v_mov_b32_e32 v91, v93
	v_pk_add_f32 v[84:85], v[84:85], v[86:87]
	v_pk_add_f32 v[68:69], v[88:89], v[90:91]
	v_lshlrev_b32_e32 v87, 16, v21
	v_pk_add_f32 v[68:69], v[84:85], v[68:69]
	v_lshlrev_b32_e32 v86, 16, v20
	v_pk_add_f32 v[84:85], v[68:69], v[68:69] op_sel:[0,1] op_sel_hi:[1,0]
	v_lshlrev_b32_e32 v69, 16, v81
	v_lshlrev_b32_e32 v68, 16, v80
	v_and_b32_e32 v81, 0xffff0000, v81
	v_and_b32_e32 v80, 0xffff0000, v80
	v_and_b32_e32 v21, 0xffff0000, v21
	v_and_b32_e32 v20, 0xffff0000, v20
	v_pk_fma_f32 v[80:81], v[214:215], v[20:21], v[80:81] neg_lo:[1,0,0] neg_hi:[1,0,0]
	v_pk_fma_f32 v[68:69], v[214:215], v[86:87], v[68:69] neg_lo:[1,0,0] neg_hi:[1,0,0]
	v_pk_mul_f32 v[20:21], v[80:81], v[80:81]
	v_lshlrev_b32_e32 v89, 16, v23
	v_pk_fma_f32 v[20:21], v[68:69], v[68:69], v[20:21]
	v_lshlrev_b32_e32 v88, 16, v22
	v_pk_add_f32 v[86:87], v[20:21], v[20:21] op_sel:[0,1] op_sel_hi:[1,0]
	v_lshlrev_b32_e32 v21, 16, v47
	v_lshlrev_b32_e32 v20, 16, v46
	v_and_b32_e32 v47, 0xffff0000, v47
	v_and_b32_e32 v46, 0xffff0000, v46
	v_and_b32_e32 v23, 0xffff0000, v23
	v_and_b32_e32 v22, 0xffff0000, v22
	v_pk_fma_f32 v[20:21], v[214:215], v[88:89], v[20:21] neg_lo:[1,0,0] neg_hi:[1,0,0]
	v_pk_fma_f32 v[22:23], v[214:215], v[22:23], v[46:47] neg_lo:[1,0,0] neg_hi:[1,0,0]
	v_mov_b32_e32 v46, v20
	v_mov_b32_e32 v47, v22
	v_mul_f32_e32 v88, v22, v22
	v_pk_fma_f32 v[88:89], v[46:47], v[46:47], v[88:89] op_sel_hi:[1,1,0]
	v_mov_b32_e32 v46, v21
	v_mov_b32_e32 v47, v23
	v_mul_f32_e32 v90, v23, v23
	v_pk_fma_f32 v[90:91], v[46:47], v[46:47], v[90:91] op_sel_hi:[1,1,0]
	v_lshlrev_b32_e32 v47, 16, v57
	v_lshlrev_b32_e32 v46, 16, v56
	v_lshlrev_b32_e32 v93, 16, v49
	v_lshlrev_b32_e32 v92, 16, v48
	v_and_b32_e32 v57, 0xffff0000, v57
	v_and_b32_e32 v56, 0xffff0000, v56
	v_and_b32_e32 v49, 0xffff0000, v49
	v_and_b32_e32 v48, 0xffff0000, v48
	v_pk_fma_f32 v[46:47], v[214:215], v[92:93], v[46:47] neg_lo:[1,0,0] neg_hi:[1,0,0]
	v_pk_fma_f32 v[48:49], v[214:215], v[48:49], v[56:57] neg_lo:[1,0,0] neg_hi:[1,0,0]
	v_pk_mul_f32 v[56:57], v[46:47], v[46:47]
	v_pk_mul_f32 v[92:93], v[48:49], v[48:49]
	v_mov_b32_e32 v85, v56
	v_mov_b32_e32 v87, v92
	v_mov_b32_e32 v89, v57
	v_mov_b32_e32 v91, v93
	v_pk_add_f32 v[84:85], v[84:85], v[86:87]
	v_pk_add_f32 v[56:57], v[88:89], v[90:91]
	v_mov_b32_e32 v10, v9
	v_pk_add_f32 v[56:57], v[84:85], v[56:57]
	s_nop 0
	v_add_f32_e32 v56, v56, v57
	ds_bpermute_b32 v57, v83, v56
	s_waitcnt lgkmcnt(0)
	v_add_f32_e32 v2, v56, v57
	v_fmamk_f32 v2, v2, 0x3c000000, v1
	v_mul_f32_e32 v14, 0x4f800000, v2
	v_cmp_gt_f32_e32 vcc, s0, v2
	s_nop 1
	v_cndmask_b32_e32 v2, v2, v14, vcc
	v_sqrt_f32_e32 v56, v2
	v_mov_b32_e32 v14, v8
	v_add_u32_e32 v8, -1, v56
	v_fma_f32 v9, -v8, v56, v2
	v_cmp_ge_f32_e64 s[0:1], 0, v9
	v_add_u32_e32 v9, 1, v56
	s_nop 0
	v_cndmask_b32_e64 v8, v56, v8, s[0:1]
	v_fma_f32 v56, -v9, v56, v2
	v_cmp_lt_f32_e64 s[0:1], 0, v56
	s_nop 1
	v_cndmask_b32_e64 v8, v8, v9, s[0:1]
	v_mul_f32_e32 v9, 0x37800000, v8
	v_cndmask_b32_e32 v8, v8, v9, vcc
	v_cmp_class_f32_e32 vcc, v2, v226
	v_mov_b32_e32 v9, v6
	v_mov_b32_e32 v6, v5
	v_cndmask_b32_e32 v2, v8, v2, vcc
	v_div_scale_f32 v56, s[0:1], v2, v2, 1.0
	v_rcp_f32_e32 v57, v56
	v_mov_b32_e32 v8, v4
	v_fma_f32 v4, -v56, v57, 1.0
	v_fmac_f32_e32 v57, v4, v57
	v_div_scale_f32 v4, vcc, 1.0, v2, 1.0
	v_mul_f32_e32 v5, v4, v57
	v_fma_f32 v83, -v56, v5, v4
	v_fmac_f32_e32 v5, v83, v57
	v_fma_f32 v4, -v56, v5, v4
	v_div_fmas_f32 v4, v4, v57, v5
	v_div_fixup_f32 v2, v4, v2, 1.0
	v_mul_f32_e32 v2, 0x3f4ccccd, v2
	v_pk_mul_f32 v[4:5], v[78:79], v[2:3] op_sel_hi:[1,0]
	v_pk_mul_f32 v[16:17], v[16:17], v[2:3] op_sel_hi:[1,0]
	v_pk_mul_f32 v[4:5], v[14:15], v[4:5]
	v_pk_mul_f32 v[14:15], v[72:73], v[2:3] op_sel_hi:[1,0]
	s_nop 0
	v_pk_mul_f32 v[10:11], v[10:11], v[14:15]
	v_pk_mul_f32 v[14:15], v[70:71], v[2:3] op_sel_hi:[1,0]
	v_pk_mul_f32 v[8:9], v[8:9], v[14:15]
	v_pk_mul_f32 v[14:15], v[64:65], v[2:3] op_sel_hi:[1,0]
	v_pk_mul_f32 v[6:7], v[6:7], v[14:15]
	v_cvt_pk_bf16_f32 v7, v9, v7
	v_cvt_pk_bf16_f32 v6, v8, v6
	v_cvt_pk_bf16_f32 v5, v5, v11
	v_cvt_pk_bf16_f32 v4, v4, v10
	global_store_dwordx4 v[12:13], v[4:7], off offset:1024
	global_load_dwordx4 v[4:7], v82, s[58:59] offset:32
	s_nop 0
	global_load_dwordx4 v[8:11], v82, s[58:59] offset:48
	v_pk_mul_f32 v[14:15], v[18:19], v[2:3] op_sel_hi:[1,0]
	s_waitcnt vmcnt(1)
	v_mov_b32_e32 v19, v6
	v_mov_b32_e32 v6, v5
	v_mov_b32_e32 v18, v4
	v_pk_mul_f32 v[4:5], v[6:7], v[16:17]
	v_pk_mul_f32 v[6:7], v[40:41], v[2:3] op_sel_hi:[1,0]
	s_waitcnt vmcnt(0)
	v_mov_b32_e32 v16, v8
	v_mov_b32_e32 v17, v10
	v_pk_mul_f32 v[6:7], v[16:17], v[6:7]
	v_pk_mul_f32 v[16:17], v[50:51], v[2:3] op_sel_hi:[1,0]
	v_mov_b32_e32 v10, v9
	v_pk_mul_f32 v[8:9], v[10:11], v[16:17]
	v_pk_mul_f32 v[14:15], v[18:19], v[14:15]
	v_bfe_u32 v10, v9, 16, 1
	v_bfe_u32 v11, v8, 16, 1
	v_add3_u32 v8, v8, v11, s81
	v_add3_u32 v9, v9, v10, s81
	v_bfe_u32 v16, v6, 16, 1
	v_bfe_u32 v17, v7, 16, 1
	v_add3_u32 v7, v7, v17, s81
	v_add3_u32 v6, v6, v16, s81
	v_lshrrev_b32_e32 v6, 16, v6
	v_lshrrev_b32_e32 v7, 16, v7
	v_and_or_b32 v7, v9, s80, v7
	v_and_or_b32 v6, v8, s80, v6
	v_cvt_pk_bf16_f32 v5, v15, v5
	v_cvt_pk_bf16_f32 v4, v14, v4
	global_store_dwordx4 v[12:13], v[4:7], off offset:1040
	global_load_dwordx4 v[4:7], v82, s[58:59] offset:64
	s_nop 0
	global_load_dwordx4 v[8:11], v82, s[58:59] offset:80
	v_pk_mul_f32 v[14:15], v[26:27], v[2:3] op_sel_hi:[1,0]
	v_pk_mul_f32 v[18:19], v[62:63], v[2:3] op_sel_hi:[1,0]
	s_waitcnt vmcnt(1)
	v_mov_b32_e32 v16, v4
	v_mov_b32_e32 v17, v6
	v_pk_mul_f32 v[14:15], v[14:15], v[16:17]
	v_pk_mul_f32 v[16:17], v[34:35], v[2:3] op_sel_hi:[1,0]
	v_mov_b32_e32 v6, v5
	v_pk_mul_f32 v[4:5], v[16:17], v[6:7]
	v_pk_mul_f32 v[6:7], v[42:43], v[2:3] op_sel_hi:[1,0]
	s_waitcnt vmcnt(0)
	v_mov_b32_e32 v16, v8
	v_mov_b32_e32 v17, v10
	v_pk_mul_f32 v[6:7], v[6:7], v[16:17]
	v_pk_mul_f32 v[16:17], v[54:55], v[2:3] op_sel_hi:[1,0]
	v_mov_b32_e32 v10, v9
	v_pk_mul_f32 v[8:9], v[16:17], v[10:11]
	v_bfe_u32 v10, v9, 16, 1
	v_bfe_u32 v11, v8, 16, 1
	v_add3_u32 v8, v8, v11, s81
	v_add3_u32 v9, v9, v10, s81
	v_bfe_u32 v16, v6, 16, 1
	v_bfe_u32 v17, v7, 16, 1
	v_add3_u32 v7, v7, v17, s81
	v_add3_u32 v6, v6, v16, s81
	v_lshrrev_b32_e32 v6, 16, v6
	v_lshrrev_b32_e32 v7, 16, v7
	v_and_or_b32 v7, v9, s80, v7
	v_and_or_b32 v6, v8, s80, v6
	v_cvt_pk_bf16_f32 v5, v15, v5
	v_cvt_pk_bf16_f32 v4, v14, v4
	global_store_dwordx4 v[12:13], v[4:7], off offset:1056
	global_load_dwordx4 v[4:7], v82, s[58:59] offset:96
	s_nop 0
	global_load_dwordx4 v[8:11], v82, s[58:59] offset:112
	v_pk_mul_f32 v[14:15], v[24:25], v[2:3] op_sel_hi:[1,0]
	v_pk_mul_f32 v[24:25], v[76:77], v[2:3] op_sel_hi:[1,0]
	s_waitcnt vmcnt(1)
	v_mov_b32_e32 v16, v4
	v_mov_b32_e32 v17, v6
	v_pk_mul_f32 v[14:15], v[14:15], v[16:17]
	v_pk_mul_f32 v[16:17], v[30:31], v[2:3] op_sel_hi:[1,0]
	v_mov_b32_e32 v6, v5
	v_pk_mul_f32 v[4:5], v[16:17], v[6:7]
	v_pk_mul_f32 v[6:7], v[60:61], v[2:3] op_sel_hi:[1,0]
	s_waitcnt vmcnt(0)
	v_mov_b32_e32 v16, v8
	v_mov_b32_e32 v17, v10
	v_pk_mul_f32 v[6:7], v[6:7], v[16:17]
	v_pk_mul_f32 v[16:17], v[74:75], v[2:3] op_sel_hi:[1,0]
	v_mov_b32_e32 v10, v9
	v_pk_mul_f32 v[8:9], v[16:17], v[10:11]
	v_bfe_u32 v10, v9, 16, 1
	v_bfe_u32 v11, v8, 16, 1
	v_add3_u32 v8, v8, v11, s81
	v_add3_u32 v9, v9, v10, s81
	v_bfe_u32 v16, v6, 16, 1
	v_bfe_u32 v17, v7, 16, 1
	v_add3_u32 v7, v7, v17, s81
	v_add3_u32 v6, v6, v16, s81
	v_lshrrev_b32_e32 v6, 16, v6
	v_lshrrev_b32_e32 v7, 16, v7
	v_and_or_b32 v7, v9, s80, v7
	v_and_or_b32 v6, v8, s80, v6
	v_cvt_pk_bf16_f32 v5, v15, v5
	v_cvt_pk_bf16_f32 v4, v14, v4
	global_store_dwordx4 v[12:13], v[4:7], off offset:1072
	global_load_dwordx4 v[4:7], v82, s[58:59] offset:128
	s_nop 0
	global_load_dwordx4 v[8:11], v82, s[58:59] offset:144
	v_pk_mul_f32 v[14:15], v[28:29], v[2:3] op_sel_hi:[1,0]
	s_waitcnt vmcnt(1)
	v_mov_b32_e32 v16, v4
	v_mov_b32_e32 v17, v6
	v_pk_mul_f32 v[14:15], v[14:15], v[16:17]
	v_pk_mul_f32 v[16:17], v[36:37], v[2:3] op_sel_hi:[1,0]
	v_mov_b32_e32 v6, v5
	v_pk_mul_f32 v[4:5], v[16:17], v[6:7]
	v_pk_mul_f32 v[6:7], v[58:59], v[2:3] op_sel_hi:[1,0]
	s_waitcnt vmcnt(0)
	v_mov_b32_e32 v16, v8
	v_mov_b32_e32 v17, v10
	v_pk_mul_f32 v[6:7], v[6:7], v[16:17]
	v_pk_mul_f32 v[16:17], v[66:67], v[2:3] op_sel_hi:[1,0]
	v_mov_b32_e32 v10, v9
	v_pk_mul_f32 v[8:9], v[16:17], v[10:11]
	v_bfe_u32 v10, v9, 16, 1
	v_bfe_u32 v11, v8, 16, 1
	v_add3_u32 v8, v8, v11, s81
	v_add3_u32 v9, v9, v10, s81
	v_bfe_u32 v16, v6, 16, 1
	v_bfe_u32 v17, v7, 16, 1
	v_add3_u32 v7, v7, v17, s81
	v_add3_u32 v6, v6, v16, s81
	v_lshrrev_b32_e32 v6, 16, v6
	v_lshrrev_b32_e32 v7, 16, v7
	v_and_or_b32 v7, v9, s80, v7
	v_and_or_b32 v6, v8, s80, v6
	v_cvt_pk_bf16_f32 v5, v15, v5
	v_cvt_pk_bf16_f32 v4, v14, v4
	global_store_dwordx4 v[12:13], v[4:7], off offset:1088
	global_load_dwordx4 v[4:7], v82, s[58:59] offset:160
	s_nop 0
	global_load_dwordx4 v[8:11], v82, s[58:59] offset:176
	v_pk_mul_f32 v[16:17], v[52:53], v[2:3] op_sel_hi:[1,0]
	v_pk_mul_f32 v[14:15], v[44:45], v[2:3] op_sel_hi:[1,0]
	s_waitcnt vmcnt(1)
	v_mov_b32_e32 v27, v6
	v_mov_b32_e32 v6, v5
	s_waitcnt vmcnt(0)
	v_mov_b32_e32 v5, v10
	v_mov_b32_e32 v10, v9
	v_mov_b32_e32 v26, v4
	v_mov_b32_e32 v4, v8
	v_pk_mul_f32 v[6:7], v[16:17], v[6:7]
	v_pk_mul_f32 v[10:11], v[24:25], v[10:11]
	v_pk_mul_f32 v[8:9], v[14:15], v[26:27]
	v_pk_mul_f32 v[4:5], v[18:19], v[4:5]
	v_bfe_u32 v14, v11, 16, 1
	v_bfe_u32 v15, v10, 16, 1
	v_bfe_u32 v16, v7, 16, 1
	v_bfe_u32 v17, v6, 16, 1
	v_add3_u32 v17, v6, v17, s81
	v_add3_u32 v16, v7, v16, s81
	v_add3_u32 v6, v10, v15, s81
	v_add3_u32 v7, v11, v14, s81
	v_bfe_u32 v10, v8, 16, 1
	v_bfe_u32 v11, v9, 16, 1
	v_bfe_u32 v14, v4, 16, 1
	v_bfe_u32 v15, v5, 16, 1
	v_add3_u32 v5, v5, v15, s81
	v_add3_u32 v4, v4, v14, s81
	v_add3_u32 v9, v9, v11, s81
	v_add3_u32 v8, v8, v10, s81
	v_lshrrev_b32_e32 v8, 16, v8
	v_lshrrev_b32_e32 v9, 16, v9
	v_lshrrev_b32_e32 v4, 16, v4
	v_lshrrev_b32_e32 v5, 16, v5
	v_and_or_b32 v7, v7, s80, v5
	v_and_or_b32 v6, v6, s80, v4
	v_and_or_b32 v5, v16, s80, v9
	v_and_or_b32 v4, v17, s80, v8
	global_store_dwordx4 v[12:13], v[4:7], off offset:1104
	global_load_dwordx4 v[4:7], v82, s[58:59] offset:192
	s_nop 0
	global_load_dwordx4 v[8:11], v82, s[58:59] offset:208
	v_pk_mul_f32 v[14:15], v[32:33], v[2:3] op_sel_hi:[1,0]
	v_pk_mul_f32 v[18:19], v[68:69], v[2:3] op_sel_hi:[1,0]
	v_pk_mul_f32 v[16:17], v[38:39], v[2:3] op_sel_hi:[1,0]
	v_pk_mul_f32 v[24:25], v[80:81], v[2:3] op_sel_hi:[1,0]
	s_waitcnt vmcnt(1)
	v_mov_b32_e32 v26, v4
	v_mov_b32_e32 v27, v6
	v_mov_b32_e32 v6, v5
	s_waitcnt vmcnt(0)
	v_mov_b32_e32 v4, v8
	v_mov_b32_e32 v5, v10
	v_mov_b32_e32 v10, v9
	v_pk_mul_f32 v[8:9], v[14:15], v[26:27]
	v_pk_mul_f32 v[4:5], v[18:19], v[4:5]
	v_pk_mul_f32 v[6:7], v[16:17], v[6:7]
	v_pk_mul_f32 v[10:11], v[24:25], v[10:11]
	v_bfe_u32 v18, v8, 16, 1
	v_bfe_u32 v19, v9, 16, 1
	v_bfe_u32 v16, v7, 16, 1
	v_bfe_u32 v17, v6, 16, 1
	v_add3_u32 v9, v9, v19, s81
	v_add3_u32 v8, v8, v18, s81
	v_add3_u32 v17, v6, v17, s81
	v_add3_u32 v16, v7, v16, s81
	v_lshrrev_b32_e32 v8, 16, v8
	v_lshrrev_b32_e32 v9, 16, v9
	v_cvt_pk_bf16_f32 v7, v5, v11
	v_cvt_pk_bf16_f32 v6, v4, v10
	v_and_or_b32 v5, v16, s80, v9
	v_and_or_b32 v4, v17, s80, v8
	global_store_dwordx4 v[12:13], v[4:7], off offset:1120
	global_load_dwordx4 v[4:7], v82, s[58:59] offset:224
	s_nop 0
	global_load_dwordx4 v[8:11], v82, s[58:59] offset:240
	v_pk_mul_f32 v[14:15], v[20:21], v[2:3] op_sel_hi:[1,0]
	v_pk_mul_f32 v[16:17], v[22:23], v[2:3] op_sel_hi:[1,0]
	v_pk_mul_f32 v[18:19], v[46:47], v[2:3] op_sel_hi:[1,0]
	v_pk_mul_f32 v[20:21], v[48:49], v[2:3] op_sel_hi:[1,0]
	s_waitcnt vmcnt(1)
	v_mov_b32_e32 v22, v4
	v_mov_b32_e32 v23, v6
	v_mov_b32_e32 v6, v5
	s_waitcnt vmcnt(0)
	v_mov_b32_e32 v4, v8
	v_mov_b32_e32 v5, v10
	v_mov_b32_e32 v10, v9
	v_pk_mul_f32 v[8:9], v[14:15], v[22:23]
	v_pk_mul_f32 v[6:7], v[16:17], v[6:7]
	v_pk_mul_f32 v[4:5], v[18:19], v[4:5]
	v_pk_mul_f32 v[10:11], v[20:21], v[10:11]
	v_bfe_u32 v15, v7, 16, 1
	v_bfe_u32 v17, v8, 16, 1
	v_bfe_u32 v18, v9, 16, 1
	v_bfe_u32 v19, v4, 16, 1
	v_bfe_u32 v14, v10, 16, 1
	v_bfe_u32 v16, v6, 16, 1
	v_add3_u32 v15, v7, v15, s81
	v_add3_u32 v4, v4, v19, s81
	v_add3_u32 v7, v9, v18, s81
	v_add3_u32 v8, v8, v17, s81
	v_add3_u32 v16, v6, v16, s81
	v_add3_u32 v6, v10, v14, s81
	v_lshrrev_b32_e32 v8, 16, v8
	v_lshrrev_b32_e32 v9, 16, v7
	v_lshrrev_b32_e32 v4, 16, v4
	v_cvt_pk_bf16_f32 v7, v5, v11
	v_and_or_b32 v6, v6, s80, v4
	v_and_or_b32 v5, v15, s80, v9
	v_and_or_b32 v4, v16, s80, v8
	global_store_dwordx4 v[12:13], v[4:7], off offset:1136
	s_branch .LBB0_259

.LBB0_532:
	s_or_b64 exec, exec, s[0:1]
	ds_read_b128 v[44:47], v53 offset:3888
	v_mov_b32_e32 v48, v34
	v_mov_b32_e32 v49, v34
	s_movk_i32 s0, 0x7fff
	s_mov_b32 s1, 0xffff0000
	s_waitcnt lgkmcnt(0)
	v_pk_fma_f32 v[34:35], v[34:35], v[36:37], v[44:45] neg_lo:[0,0,1] neg_hi:[0,0,1]
	v_xor_b32_e32 v47, 0x80000000, v47
	v_xor_b32_e32 v46, 0x80000000, v46
	v_pk_fma_f32 v[36:37], v[48:49], v[42:43], v[46:47]
	v_cvt_pk_bf16_f32 v34, v34, v35
	v_cvt_pk_bf16_f32 v35, v36, v37
	ds_write_b64 v51, v[34:35] offset:40984
	s_waitcnt lgkmcnt(0)
	s_barrier
	ds_read_b128 v[34:37], v55 offset:40960
	ds_read_b128 v[42:45], v55 offset:41024
	s_waitcnt vmcnt(11) lgkmcnt(1)
	v_mfma_f32_16x16x32_bf16 v[18:21], v[18:21], v[34:37], 0
	s_mov_b32 s3, 0
	s_waitcnt vmcnt(9)
	v_mfma_f32_16x16x32_bf16 v[22:25], v[22:25], v[34:37], 0
	s_waitcnt vmcnt(7)
	v_mfma_f32_16x16x32_bf16 v[26:29], v[26:29], v[34:37], 0
	s_waitcnt vmcnt(5)
	v_mfma_f32_16x16x32_bf16 v[30:33], v[30:33], v[34:37], 0
	s_waitcnt lgkmcnt(0)
	v_mfma_f32_16x16x32_bf16 v[14:17], v[14:17], v[42:45], v[18:21]
	v_mfma_f32_16x16x32_bf16 v[10:13], v[10:13], v[42:45], v[22:25]
	v_mfma_f32_16x16x32_bf16 v[6:9], v[6:9], v[42:45], v[26:29]
	s_waitcnt vmcnt(0)
	s_nop 4
	v_pk_mul_f32 v[16:17], v[16:17], v[102:103]
	v_pk_mul_f32 v[14:15], v[14:15], v[100:101]
	v_bfe_u32 v19, v16, 16, 1
	v_bfe_u32 v1, v14, 16, 1
	v_bfe_u32 v18, v15, 16, 1
	v_bfe_u32 v20, v17, 16, 1
	v_add3_u32 v1, v14, v1, s0
	v_add3_u32 v14, v15, v18, s0
	v_add3_u32 v15, v16, v19, s0
	v_add3_u32 v16, v17, v20, s0
	v_lshrrev_b32_e32 v1, 16, v1
	v_lshrrev_b32_e32 v15, 16, v15
	v_and_or_b32 v14, v14, s1, v1
	v_and_or_b32 v15, v16, s1, v15
	global_store_dwordx2 v[38:39], v[14:15], off offset:896
	v_mfma_f32_16x16x32_bf16 v[2:5], v[2:5], v[42:45], v[30:33]
	v_pk_mul_f32 v[12:13], v[12:13], v[106:107]
	v_pk_mul_f32 v[10:11], v[10:11], v[104:105]
	v_bfe_u32 v1, v10, 16, 1
	v_bfe_u32 v14, v11, 16, 1
	v_add3_u32 v1, v10, v1, s0
	v_add3_u32 v10, v11, v14, s0
	v_lshrrev_b32_e32 v1, 16, v1
	v_and_or_b32 v10, v10, s1, v1
	v_cvt_pk_bf16_f32 v11, v12, v13
	global_store_dwordx2 v[38:39], v[10:11], off offset:928
	v_pk_mul_f32 v[8:9], v[8:9], v[110:111]
	v_pk_mul_f32 v[6:7], v[6:7], v[108:109]
	v_bfe_u32 v1, v6, 16, 1
	v_bfe_u32 v10, v7, 16, 1
	v_add3_u32 v1, v6, v1, s0
	v_add3_u32 v6, v7, v10, s0
	v_lshrrev_b32_e32 v1, 16, v1
	v_and_or_b32 v6, v6, s1, v1
	v_cvt_pk_bf16_f32 v7, v8, v9
	global_store_dwordx2 v[38:39], v[6:7], off offset:960
	v_pk_mul_f32 v[4:5], v[4:5], v[114:115]
	v_pk_mul_f32 v[2:3], v[2:3], v[112:113]
	v_bfe_u32 v1, v2, 16, 1
	v_bfe_u32 v6, v3, 16, 1
	v_add3_u32 v1, v2, v1, s0
	v_add3_u32 v2, v3, v6, s0
	v_lshrrev_b32_e32 v1, 16, v1
	v_and_or_b32 v2, v2, s1, v1
	v_cvt_pk_bf16_f32 v3, v4, v5
	global_store_dwordx2 v[38:39], v[2:3], off offset:992
	s_barrier
	s_waitcnt vmcnt(0)
	s_barrier
	s_mov_b64 s[0:1], exec
	v_readlane_b32 s4, v254, 2
	v_readlane_b32 s5, v254, 3
	s_and_b64 s[4:5], s[0:1], s[4:5]
	s_mov_b64 exec, s[4:5]
	s_cbranch_execz .LBB0_584
	s_mov_b32 s2, 0
	s_lshl_b64 s[2:3], s[2:3], 2
	v_readlane_b32 s4, v254, 0
	v_readlane_b32 s5, v254, 1
	s_add_u32 s2, s4, s2
	s_addc_u32 s3, s5, s3
	s_add_i32 s4, 0, 0x20160
	v_mov_b32_e32 v1, s4
	s_waitcnt vmcnt(0) expcnt(0) lgkmcnt(0)
	ds_read_b32 v3, v1
	s_add_i32 s4, 0, 0x20164
	v_mov_b32_e32 v1, s4
	ds_read_b32 v1, v1
	s_waitcnt lgkmcnt(1)
	v_cmp_ne_u32_e32 vcc, 0, v3
	s_cbranch_vccnz .LBB0_548
	v_readlane_b32 s4, v254, 20
	v_readlane_b32 s5, v254, 21
	s_load_dwordx2 s[8:9], s[4:5], 0x4
	s_add_u32 s4, s2, 0x1000
	s_addc_u32 s5, s3, 0
	s_add_u32 s6, s2, 0x1100
	s_addc_u32 s7, s3, 0
	v_readlane_b32 s10, v254, 22
	s_waitcnt lgkmcnt(0)
	s_mul_i32 s26, s8, s10
	s_add_u32 s8, s2, 0x1200
	s_mul_i32 s26, s26, s9
	s_addc_u32 s9, s3, 0
	s_add_u32 s10, s2, 0x1300
	s_addc_u32 s11, s3, 0
	s_mov_b32 s27, 1
	v_mov_b32_e32 v17, 0
	s_branch .LBB0_536

.LBB0_620:
	s_waitcnt vmcnt(7)
	v_lshlrev_b32_e32 v93, 16, v43
	v_lshlrev_b32_e32 v92, 16, v42
	v_and_b32_e32 v95, 0xffff0000, v43
	v_and_b32_e32 v94, 0xffff0000, v42
	v_pk_add_f32 v[96:97], v[92:93], v[94:95]
	v_and_b32_e32 v99, 0xffff0000, v45
	v_add_f32_e32 v85, v96, v97
	v_lshlrev_b32_e32 v97, 16, v45
	v_lshlrev_b32_e32 v96, 16, v44
	v_and_b32_e32 v98, 0xffff0000, v44
	v_pk_add_f32 v[100:101], v[96:97], v[98:99]
	s_waitcnt vmcnt(6)
	v_lshlrev_b32_e32 v80, 16, v46
	v_and_b32_e32 v81, 0xffff0000, v46
	v_lshlrev_b32_e32 v82, 16, v47
	v_and_b32_e32 v83, 0xffff0000, v47
	v_pk_add_f32 v[100:101], v[100:101], v[100:101] op_sel_hi:[0,1]
	v_lshlrev_b32_e32 v84, 16, v48
	v_and_b32_e32 v86, 0xffff0000, v48
	v_lshlrev_b32_e32 v88, 16, v49
	v_and_b32_e32 v90, 0xffff0000, v49
	v_add_f32_e32 v91, 0, v85
	v_add_f32_e32 v85, v80, v81
	v_add_f32_e32 v87, v82, v83
	v_mov_b32_e32 v89, v101
	v_pk_add_f32 v[102:103], v[84:85], v[86:87]
	v_pk_add_f32 v[100:101], v[88:89], v[90:91]
	s_nop 0
	v_pk_add_f32 v[100:101], v[102:103], v[100:101]
	s_nop 0
	v_add_f32_e32 v85, v100, v101
	s_waitcnt lgkmcnt(0)
	s_nop 1
	v_add_f32_dpp v85, v85, v85 quad_perm:[1,0,3,2] row_mask:0xf bank_mask:0xf
	s_nop 1
	v_add_f32_dpp v85, v85, v85 quad_perm:[2,3,0,1] row_mask:0xf bank_mask:0xf
	s_nop 1
	v_add_f32_dpp v85, v85, v85 row_half_mirror row_mask:0xf bank_mask:0xf
	s_nop 1
	v_add_f32_dpp v85, v85, v85 row_mirror row_mask:0xf bank_mask:0xf
	v_mov_b32_e32 v87, v85
	s_nop 1
	v_permlane16_swap_b32_e32 v85, v87
	v_add_f32_e32 v85, v85, v87
	v_mov_b32_e32 v87, v85
	s_nop 1
	v_permlane32_swap_b32_e32 v85, v87
	v_add_f32_e32 v85, v85, v87
	v_fmac_f32_e32 v94, 0xba800000, v85
	v_fmac_f32_e32 v95, 0xba800000, v85
	v_fmac_f32_e32 v93, 0xba800000, v85
	v_fmac_f32_e32 v92, 0xba800000, v85
	v_mov_b32_e32 v100, v93
	v_mov_b32_e32 v101, v95
	v_mov_b32_e32 v93, v94
	v_pk_mul_f32 v[102:103], v[100:101], v[100:101]
	v_pk_mul_f32 v[94:95], v[92:93], v[92:93]
	v_fmac_f32_e32 v98, 0xba800000, v85
	v_pk_mov_b32 v[104:105], v[94:95], v[102:103] op_sel:[1,0]
	v_mov_b32_e32 v95, v103
	v_fmac_f32_e32 v99, 0xba800000, v85
	v_fmac_f32_e32 v97, 0xba800000, v85
	v_pk_add_f32 v[94:95], v[104:105], v[94:95]
	v_fmac_f32_e32 v96, 0xba800000, v85
	v_mov_b32_e32 v102, v97
	v_mov_b32_e32 v103, v99
	v_mov_b32_e32 v97, v98
	v_pk_add_f32 v[94:95], v[94:95], v[94:95] op_sel_hi:[0,1]
	v_pk_mul_f32 v[104:105], v[102:103], v[102:103]
	v_pk_mul_f32 v[98:99], v[96:97], v[96:97]
	v_fmac_f32_e32 v80, 0xba800000, v85
	v_pk_mov_b32 v[106:107], v[98:99], v[104:105] op_sel:[1,0]
	v_mov_b32_e32 v99, v105
	v_fmac_f32_e32 v81, 0xba800000, v85
	v_fmac_f32_e32 v82, 0xba800000, v85
	v_mul_f32_e32 v94, v80, v80
	v_pk_add_f32 v[98:99], v[106:107], v[98:99]
	v_fmac_f32_e32 v83, 0xba800000, v85
	v_pk_fma_f32 v[104:105], v[80:81], v[80:81], v[94:95] op_sel_hi:[1,1,0]
	v_mul_f32_e32 v94, v82, v82
	v_pk_add_f32 v[98:99], v[98:99], v[98:99] op_sel_hi:[0,1]
	v_pk_fma_f32 v[106:107], v[82:83], v[82:83], v[94:95] op_sel_hi:[1,1,0]
	v_fmac_f32_e32 v90, 0xba800000, v85
	v_fmac_f32_e32 v88, 0xba800000, v85
	v_fmac_f32_e32 v86, 0xba800000, v85
	v_fmac_f32_e32 v84, 0xba800000, v85
	v_mul_f32_e32 v104, v84, v84
	v_mul_f32_e32 v106, v86, v86
	v_mul_f32_e32 v94, v88, v88
	v_mul_f32_e32 v98, v90, v90
	v_pk_add_f32 v[104:105], v[104:105], v[106:107]
	v_pk_add_f32 v[94:95], v[94:95], v[98:99]
	s_nop 0
	v_pk_add_f32 v[94:95], v[104:105], v[94:95]
	s_nop 0
	v_add_f32_e32 v85, v94, v95
	s_waitcnt lgkmcnt(0)
	s_nop 1
	v_add_f32_dpp v85, v85, v85 quad_perm:[1,0,3,2] row_mask:0xf bank_mask:0xf
	s_nop 1
	v_add_f32_dpp v85, v85, v85 quad_perm:[2,3,0,1] row_mask:0xf bank_mask:0xf
	s_nop 1
	v_add_f32_dpp v85, v85, v85 row_half_mirror row_mask:0xf bank_mask:0xf
	s_nop 1
	v_add_f32_dpp v85, v85, v85 row_mirror row_mask:0xf bank_mask:0xf
	v_mov_b32_e32 v87, v85
	s_nop 1
	v_permlane16_swap_b32_e32 v85, v87
	v_add_f32_e32 v85, v85, v87
	v_mov_b32_e32 v87, v85
	s_nop 1
	v_permlane32_swap_b32_e32 v85, v87
	v_add_f32_e32 v85, v85, v87
	v_fmamk_f32 v85, v85, 0x3a800000, v78
	v_mul_f32_e32 v87, 0x4f800000, v85
	v_cmp_gt_f32_e32 vcc, s6, v85
	s_nop 1
	v_cndmask_b32_e32 v85, v85, v87, vcc
	v_sqrt_f32_e32 v87, v85
	s_nop 0
	v_add_u32_e32 v89, -1, v87
	v_fma_f32 v91, -v89, v87, v85
	v_cmp_ge_f32_e64 s[0:1], 0, v91
	v_add_u32_e32 v91, 1, v87
	s_nop 0
	v_cndmask_b32_e64 v89, v87, v89, s[0:1]
	v_fma_f32 v87, -v91, v87, v85
	v_cmp_lt_f32_e64 s[0:1], 0, v87
	s_nop 1
	v_cndmask_b32_e64 v87, v89, v91, s[0:1]
	v_mul_f32_e32 v89, 0x37800000, v87
	v_cndmask_b32_e32 v87, v87, v89, vcc
	v_cmp_class_f32_e32 vcc, v85, v79
	s_nop 1
	v_cndmask_b32_e32 v85, v87, v85, vcc
	v_div_scale_f32 v87, s[0:1], v85, v85, 1.0
	v_rcp_f32_e32 v89, v87
	s_add_i32 s0, s4, 6
	s_cmp_gt_u32 s0, 12
	v_fma_f32 v91, -v87, v89, 1.0
	v_fmac_f32_e32 v89, v91, v89
	v_div_scale_f32 v91, vcc, 1.0, v85, 1.0
	v_mul_f32_e32 v94, v91, v89
	v_fma_f32 v95, -v87, v94, v91
	v_fmac_f32_e32 v94, v95, v89
	v_fma_f32 v87, -v87, v94, v91
	v_div_fmas_f32 v87, v87, v89, v94
	v_div_fixup_f32 v94, v87, v85, 1.0
	v_pk_mul_f32 v[92:93], v[92:93], v[94:95] op_sel_hi:[1,0]
	v_pk_mul_f32 v[80:81], v[80:81], v[94:95] op_sel_hi:[1,0]
	v_mov_b32_e32 v85, v86
	v_pk_fma_f32 v[92:93], v[10:11], v[92:93], v[14:15]
	v_pk_fma_f32 v[104:105], v[26:27], v[80:81], v[30:31]
	v_pk_mul_f32 v[80:81], v[84:85], v[94:95] op_sel_hi:[1,0]
	v_pk_mul_f32 v[98:99], v[100:101], v[94:95] op_sel_hi:[1,0]
	v_pk_fma_f32 v[86:87], v[18:19], v[80:81], v[22:23]
	v_pk_fma_f32 v[98:99], v[12:13], v[98:99], v[16:17]
	v_pk_mul_f32 v[82:83], v[82:83], v[94:95] op_sel_hi:[1,0]
	v_mov_b32_e32 v89, v90
	v_pk_mul_f32 v[100:101], v[102:103], v[94:95] op_sel_hi:[1,0]
	v_pk_fma_f32 v[102:103], v[28:29], v[82:83], v[32:33]
	v_pk_mul_f32 v[82:83], v[88:89], v[94:95] op_sel_hi:[1,0]
	v_cvt_pk_bf16_f32 v80, v92, v93
	v_pk_mul_f32 v[96:97], v[96:97], v[94:95] op_sel_hi:[1,0]
	v_pk_fma_f32 v[84:85], v[20:21], v[82:83], v[24:25]
	v_pk_fma_f32 v[96:97], v[2:3], v[96:97], v[6:7]
	v_cvt_pk_bf16_f32 v81, v98, v99
	v_pk_fma_f32 v[100:101], v[4:5], v[100:101], v[8:9]
	v_cvt_pk_bf16_f32 v82, v96, v97
	v_cvt_pk_bf16_f32 v83, v100, v101
	global_store_dwordx4 v[72:73], v[80:83], off offset:-1024
	s_nop 1
	v_cvt_pk_bf16_f32 v80, v104, v105
	v_cvt_pk_bf16_f32 v81, v102, v103
	v_cvt_pk_bf16_f32 v82, v86, v87
	v_cvt_pk_bf16_f32 v83, v84, v85
	global_store_dwordx4 v[70:71], v[80:83], off offset:-4096
	s_cbranch_scc1 .LBB0_622
	v_add3_u32 v42, v66, s4, 9
	v_ashrrev_i32_e32 v43, 31, v42
	v_lshlrev_b64 v[42:43], 11, v[42:43]
	v_lshl_add_u64 v[46:47], v[68:69], 0, v[42:43]
	global_load_dwordx4 v[42:45], v[46:47], off
	s_nop 0
	global_load_dwordx4 v[46:49], v[46:47], off offset:1024
.LBB0_622:
	s_waitcnt vmcnt(7)
	v_lshlrev_b32_e32 v91, 16, v51
	v_lshlrev_b32_e32 v90, 16, v50
	v_and_b32_e32 v93, 0xffff0000, v51
	v_and_b32_e32 v92, 0xffff0000, v50
	v_pk_add_f32 v[94:95], v[90:91], v[92:93]
	v_and_b32_e32 v97, 0xffff0000, v53
	v_add_f32_e32 v83, v94, v95
	v_lshlrev_b32_e32 v95, 16, v53
	v_lshlrev_b32_e32 v94, 16, v52
	v_and_b32_e32 v96, 0xffff0000, v52
	v_pk_add_f32 v[98:99], v[94:95], v[96:97]
	s_waitcnt vmcnt(6)
	v_lshlrev_b32_e32 v72, 16, v54
	v_and_b32_e32 v73, 0xffff0000, v54
	v_lshlrev_b32_e32 v80, 16, v55
	v_and_b32_e32 v81, 0xffff0000, v55
	v_pk_add_f32 v[98:99], v[98:99], v[98:99] op_sel_hi:[0,1]
	v_lshlrev_b32_e32 v82, 16, v56
	v_and_b32_e32 v84, 0xffff0000, v56
	v_lshlrev_b32_e32 v86, 16, v57
	v_and_b32_e32 v88, 0xffff0000, v57
	v_add_f32_e32 v89, 0, v83
	v_add_f32_e32 v83, v72, v73
	v_add_f32_e32 v85, v80, v81
	v_mov_b32_e32 v87, v99
	v_pk_add_f32 v[100:101], v[82:83], v[84:85]
	v_pk_add_f32 v[98:99], v[86:87], v[88:89]
	s_nop 0
	v_pk_add_f32 v[98:99], v[100:101], v[98:99]
	s_nop 0
	v_add_f32_e32 v83, v98, v99
	s_waitcnt lgkmcnt(0)
	s_nop 1
	v_add_f32_dpp v83, v83, v83 quad_perm:[1,0,3,2] row_mask:0xf bank_mask:0xf
	s_nop 1
	v_add_f32_dpp v83, v83, v83 quad_perm:[2,3,0,1] row_mask:0xf bank_mask:0xf
	s_nop 1
	v_add_f32_dpp v83, v83, v83 row_half_mirror row_mask:0xf bank_mask:0xf
	s_nop 1
	v_add_f32_dpp v83, v83, v83 row_mirror row_mask:0xf bank_mask:0xf
	v_mov_b32_e32 v85, v83
	s_nop 1
	v_permlane16_swap_b32_e32 v83, v85
	v_add_f32_e32 v83, v83, v85
	v_mov_b32_e32 v85, v83
	s_nop 1
	v_permlane32_swap_b32_e32 v83, v85
	v_add_f32_e32 v83, v83, v85
	v_fmac_f32_e32 v92, 0xba800000, v83
	v_fmac_f32_e32 v93, 0xba800000, v83
	v_fmac_f32_e32 v91, 0xba800000, v83
	v_fmac_f32_e32 v90, 0xba800000, v83
	v_mov_b32_e32 v98, v91
	v_mov_b32_e32 v99, v93
	v_mov_b32_e32 v91, v92
	v_pk_mul_f32 v[100:101], v[98:99], v[98:99]
	v_pk_mul_f32 v[92:93], v[90:91], v[90:91]
	v_fmac_f32_e32 v96, 0xba800000, v83
	v_pk_mov_b32 v[102:103], v[92:93], v[100:101] op_sel:[1,0]
	v_mov_b32_e32 v93, v101
	v_fmac_f32_e32 v97, 0xba800000, v83
	v_fmac_f32_e32 v95, 0xba800000, v83
	v_pk_add_f32 v[92:93], v[102:103], v[92:93]
	v_fmac_f32_e32 v94, 0xba800000, v83
	v_mov_b32_e32 v100, v95
	v_mov_b32_e32 v101, v97
	v_mov_b32_e32 v95, v96
	v_pk_add_f32 v[92:93], v[92:93], v[92:93] op_sel_hi:[0,1]
	v_pk_mul_f32 v[102:103], v[100:101], v[100:101]
	v_pk_mul_f32 v[96:97], v[94:95], v[94:95]
	v_fmac_f32_e32 v72, 0xba800000, v83
	v_pk_mov_b32 v[104:105], v[96:97], v[102:103] op_sel:[1,0]
	v_mov_b32_e32 v97, v103
	v_fmac_f32_e32 v73, 0xba800000, v83
	v_fmac_f32_e32 v80, 0xba800000, v83
	v_mul_f32_e32 v92, v72, v72
	v_pk_add_f32 v[96:97], v[104:105], v[96:97]
	v_fmac_f32_e32 v81, 0xba800000, v83
	v_pk_fma_f32 v[102:103], v[72:73], v[72:73], v[92:93] op_sel_hi:[1,1,0]
	v_mul_f32_e32 v92, v80, v80
	v_pk_add_f32 v[96:97], v[96:97], v[96:97] op_sel_hi:[0,1]
	v_pk_fma_f32 v[104:105], v[80:81], v[80:81], v[92:93] op_sel_hi:[1,1,0]
	v_fmac_f32_e32 v88, 0xba800000, v83
	v_fmac_f32_e32 v86, 0xba800000, v83
	v_fmac_f32_e32 v84, 0xba800000, v83
	v_fmac_f32_e32 v82, 0xba800000, v83
	v_mul_f32_e32 v102, v82, v82
	v_mul_f32_e32 v104, v84, v84
	v_mul_f32_e32 v92, v86, v86
	v_mul_f32_e32 v96, v88, v88
	v_pk_add_f32 v[102:103], v[102:103], v[104:105]
	v_pk_add_f32 v[92:93], v[92:93], v[96:97]
	s_nop 0
	v_pk_add_f32 v[92:93], v[102:103], v[92:93]
	s_nop 0
	v_add_f32_e32 v83, v92, v93
	s_waitcnt lgkmcnt(0)
	s_nop 1
	v_add_f32_dpp v83, v83, v83 quad_perm:[1,0,3,2] row_mask:0xf bank_mask:0xf
	s_nop 1
	v_add_f32_dpp v83, v83, v83 quad_perm:[2,3,0,1] row_mask:0xf bank_mask:0xf
	s_nop 1
	v_add_f32_dpp v83, v83, v83 row_half_mirror row_mask:0xf bank_mask:0xf
	s_nop 1
	v_add_f32_dpp v83, v83, v83 row_mirror row_mask:0xf bank_mask:0xf
	v_mov_b32_e32 v85, v83
	s_nop 1
	v_permlane16_swap_b32_e32 v83, v85
	v_add_f32_e32 v83, v83, v85
	v_mov_b32_e32 v85, v83
	s_nop 1
	v_permlane32_swap_b32_e32 v83, v85
	v_add_f32_e32 v83, v83, v85
	v_fmamk_f32 v83, v83, 0x3a800000, v78
	v_mul_f32_e32 v85, 0x4f800000, v83
	v_cmp_gt_f32_e32 vcc, s6, v83
	s_nop 1
	v_cndmask_b32_e32 v83, v83, v85, vcc
	v_sqrt_f32_e32 v85, v83
	s_nop 0
	v_add_u32_e32 v87, -1, v85
	v_fma_f32 v89, -v87, v85, v83
	v_cmp_ge_f32_e64 s[0:1], 0, v89
	v_add_u32_e32 v89, 1, v85
	s_nop 0
	v_cndmask_b32_e64 v87, v85, v87, s[0:1]
	v_fma_f32 v85, -v89, v85, v83
	v_cmp_lt_f32_e64 s[0:1], 0, v85
	s_nop 1
	v_cndmask_b32_e64 v85, v87, v89, s[0:1]
	v_mul_f32_e32 v87, 0x37800000, v85
	v_cndmask_b32_e32 v85, v85, v87, vcc
	v_cmp_class_f32_e32 vcc, v83, v79
	s_nop 1
	v_cndmask_b32_e32 v83, v85, v83, vcc
	v_div_scale_f32 v85, s[0:1], v83, v83, 1.0
	v_rcp_f32_e32 v87, v85
	s_add_i32 s0, s4, 7
	s_cmp_gt_u32 s0, 12
	v_fma_f32 v89, -v85, v87, 1.0
	v_fmac_f32_e32 v87, v89, v87
	v_div_scale_f32 v89, vcc, 1.0, v83, 1.0
	v_mul_f32_e32 v92, v89, v87
	v_fma_f32 v93, -v85, v92, v89
	v_fmac_f32_e32 v92, v93, v87
	v_fma_f32 v85, -v85, v92, v89
	v_div_fmas_f32 v85, v85, v87, v92
	v_div_fixup_f32 v92, v85, v83, 1.0
	v_pk_mul_f32 v[90:91], v[90:91], v[92:93] op_sel_hi:[1,0]
	v_pk_mul_f32 v[80:81], v[80:81], v[92:93] op_sel_hi:[1,0]
	v_mov_b32_e32 v83, v84
	v_pk_mul_f32 v[96:97], v[98:99], v[92:93] op_sel_hi:[1,0]
	v_pk_fma_f32 v[90:91], v[10:11], v[90:91], v[14:15]
	v_pk_mul_f32 v[98:99], v[100:101], v[92:93] op_sel_hi:[1,0]
	v_pk_fma_f32 v[100:101], v[28:29], v[80:81], v[32:33]
	v_pk_mul_f32 v[80:81], v[82:83], v[92:93] op_sel_hi:[1,0]
	v_mov_b32_e32 v87, v88
	v_pk_mul_f32 v[82:83], v[86:87], v[92:93] op_sel_hi:[1,0]
	v_pk_fma_f32 v[86:87], v[18:19], v[80:81], v[22:23]
	v_pk_fma_f32 v[96:97], v[12:13], v[96:97], v[16:17]
	v_cvt_pk_bf16_f32 v80, v90, v91
	v_pk_mul_f32 v[94:95], v[94:95], v[92:93] op_sel_hi:[1,0]
	v_pk_fma_f32 v[84:85], v[20:21], v[82:83], v[24:25]
	v_pk_fma_f32 v[94:95], v[2:3], v[94:95], v[6:7]
	v_cvt_pk_bf16_f32 v81, v96, v97
	v_pk_fma_f32 v[98:99], v[4:5], v[98:99], v[8:9]
	v_cvt_pk_bf16_f32 v82, v94, v95
	v_pk_mul_f32 v[72:73], v[72:73], v[92:93] op_sel_hi:[1,0]
	v_pk_fma_f32 v[72:73], v[26:27], v[72:73], v[30:31]
	v_cvt_pk_bf16_f32 v83, v98, v99
	global_store_dwordx4 v[70:71], v[80:83], off offset:-3072
	s_nop 1
	v_cvt_pk_bf16_f32 v80, v72, v73
	v_cvt_pk_bf16_f32 v81, v100, v101
	v_cvt_pk_bf16_f32 v82, v86, v87
	v_cvt_pk_bf16_f32 v83, v84, v85
	global_store_dwordx4 v[70:71], v[80:83], off offset:-2048
	s_cbranch_scc1 .LBB0_617
	v_add3_u32 v50, v66, s4, 10
	v_ashrrev_i32_e32 v51, 31, v50
	v_lshlrev_b64 v[50:51], 11, v[50:51]
	v_lshl_add_u64 v[54:55], v[68:69], 0, v[50:51]
	global_load_dwordx4 v[50:53], v[54:55], off
	s_nop 0
	global_load_dwordx4 v[54:57], v[54:55], off offset:1024
	s_branch .LBB0_617

.LBB0_699:
	v_mov_b32_e32 v132, v0
	s_lshl_b32 s1, s36, 8
	s_lshl_b32 s22, s80, 8
	s_add_i32 s1, s1, s74
	s_ashr_i32 s23, s22, 31
	v_and_or_b32 v134, v132, 15, s1
	v_lshrrev_b32_e32 v132, 1, v132
	s_lshl_b64 s[22:23], s[22:23], 1
	v_and_or_b32 v132, v132, 24, s75
	s_add_u32 s22, s47, s22
	s_addc_u32 s23, s50, s23
	v_lshlrev_b32_e32 v132, 1, v132
	v_ashrrev_i32_e32 v135, 31, v134
	v_lshl_add_u64 v[136:137], s[22:23], 0, v[132:133]
	v_lshlrev_b64 v[138:139], 11, v[134:135]
	v_lshl_add_u64 v[162:163], v[136:137], 0, v[138:139]
	global_load_dwordx4 v[146:149], v[162:163], off
	global_load_dwordx4 v[150:153], v[162:163], off offset:256
	v_or_b32_e32 v138, 16, v134
	v_ashrrev_i32_e32 v139, 31, v138
	v_lshlrev_b64 v[138:139], 11, v[138:139]
	v_lshl_add_u64 v[138:139], v[136:137], 0, v[138:139]
	global_load_dwordx4 v[154:157], v[138:139], off
	global_load_dwordx4 v[158:161], v[138:139], off offset:256
	s_and_b64 vcc, exec, s[2:3]
	s_mov_b64 s[2:3], -1
	s_waitcnt vmcnt(3)
	v_lshlrev_b32_e32 v164, 16, v146
	v_and_b32_e32 v165, 0xffff0000, v146
	v_lshlrev_b32_e32 v146, 16, v147
	v_and_b32_e32 v147, 0xffff0000, v147
	v_lshlrev_b32_e32 v166, 16, v148
	v_and_b32_e32 v167, 0xffff0000, v148
	v_lshlrev_b32_e32 v148, 16, v149
	v_and_b32_e32 v149, 0xffff0000, v149
	s_waitcnt vmcnt(2)
	v_lshlrev_b32_e32 v170, 16, v152
	v_and_b32_e32 v171, 0xffff0000, v152
	v_lshlrev_b32_e32 v152, 16, v153
	v_and_b32_e32 v153, 0xffff0000, v153
	v_pk_fma_f32 v[128:129], v[146:147], s[8:9], v[128:129] op_sel_hi:[1,0,1]
	v_pk_fma_f32 v[126:127], v[164:165], s[8:9], v[126:127] op_sel_hi:[1,0,1]
	v_pk_fma_f32 v[124:125], v[148:149], s[8:9], v[124:125] op_sel_hi:[1,0,1]
	v_pk_fma_f32 v[122:123], v[166:167], s[8:9], v[122:123] op_sel_hi:[1,0,1]
	v_lshlrev_b32_e32 v168, 16, v150
	v_and_b32_e32 v169, 0xffff0000, v150
	v_lshlrev_b32_e32 v150, 16, v151
	v_and_b32_e32 v151, 0xffff0000, v151
	v_pk_fma_f32 v[146:147], v[152:153], s[8:9], v[116:117] op_sel_hi:[1,0,1]
	v_pk_fma_f32 v[114:115], v[170:171], s[8:9], v[114:115] op_sel_hi:[1,0,1]
	v_bfe_u32 v116, v126, 16, 1
	v_bfe_u32 v132, v128, 16, 1
	v_bfe_u32 v145, v122, 16, 1
	v_pk_fma_f32 v[120:121], v[150:151], s[8:9], v[120:121] op_sel_hi:[1,0,1]
	v_bfe_u32 v117, v127, 16, 1
	v_bfe_u32 v135, v129, 16, 1
	v_bfe_u32 v148, v123, 16, 1
	v_bfe_u32 v165, v114, 16, 1
	v_bfe_u32 v166, v115, 16, 1
	v_add3_u32 v116, v126, v116, s79
	v_add3_u32 v126, v128, v132, s79
	v_add3_u32 v122, v122, v145, s79
	v_pk_fma_f32 v[118:119], v[168:169], s[8:9], v[118:119] op_sel_hi:[1,0,1]
	v_add3_u32 v117, v127, v117, s79
	v_add3_u32 v127, v129, v135, s79
	v_add3_u32 v123, v123, v148, s79
	v_add3_u32 v114, v114, v165, s79
	v_add3_u32 v128, v115, v166, s79
	v_lshrrev_b32_e32 v115, 16, v116
	v_lshrrev_b32_e32 v116, 16, v126
	v_lshrrev_b32_e32 v122, 16, v122
	v_bfe_u32 v153, v120, 16, 1
	v_bfe_u32 v167, v146, 16, 1
	v_lshrrev_b32_e32 v126, 16, v114
	v_and_or_b32 v114, v117, s77, v115
	v_and_or_b32 v115, v127, s77, v116
	v_and_or_b32 v116, v123, s77, v122
	v_cvt_pk_bf16_f32 v117, v124, v125
	v_bfe_u32 v164, v121, 16, 1
	v_add3_u32 v120, v120, v153, s79
	v_add3_u32 v129, v146, v167, s79
	global_store_dwordx4 v[162:163], v[114:117], off
	s_nop 1
	v_add3_u32 v121, v121, v164, s79
	v_bfe_u32 v115, v147, 16, 1
	v_lshrrev_b32_e32 v120, 16, v120
	v_lshrrev_b32_e32 v114, 16, v129
	v_add3_u32 v115, v147, v115, s79
	v_cvt_pk_bf16_f32 v118, v118, v119
	v_and_or_b32 v119, v121, s77, v120
	v_and_or_b32 v121, v115, s77, v114
	v_or_b32_e32 v114, 32, v134
	v_ashrrev_i32_e32 v115, 31, v114
	v_lshlrev_b64 v[114:115], 11, v[114:115]
	v_and_or_b32 v120, v128, s77, v126
	v_lshl_add_u64 v[114:115], v[136:137], 0, v[114:115]
	global_store_dwordx4 v[162:163], v[118:121], off offset:256
	global_load_dwordx4 v[116:119], v[114:115], off
	s_waitcnt vmcnt(4)
	v_lshlrev_b32_e32 v124, 16, v154
	v_and_b32_e32 v125, 0xffff0000, v154
	v_lshlrev_b32_e32 v128, 16, v156
	v_and_b32_e32 v129, 0xffff0000, v156
	v_lshlrev_b32_e32 v146, 16, v157
	v_and_b32_e32 v147, 0xffff0000, v157
	v_pk_fma_f32 v[110:111], v[124:125], s[8:9], v[110:111] op_sel_hi:[1,0,1]
	v_pk_fma_f32 v[124:125], v[146:147], s[8:9], v[108:109] op_sel_hi:[1,0,1]
	v_pk_fma_f32 v[108:109], v[128:129], s[8:9], v[106:107] op_sel_hi:[1,0,1]
	v_lshlrev_b32_e32 v126, 16, v155
	v_and_b32_e32 v127, 0xffff0000, v155
	v_pk_fma_f32 v[112:113], v[126:127], s[8:9], v[112:113] op_sel_hi:[1,0,1]
	v_cvt_pk_bf16_f32 v106, v110, v111
	global_load_dwordx4 v[120:123], v[114:115], off offset:256
	v_cvt_pk_bf16_f32 v107, v112, v113
	v_cvt_pk_bf16_f32 v108, v108, v109
	s_waitcnt vmcnt(4)
	v_lshlrev_b32_e32 v148, 16, v158
	v_and_b32_e32 v149, 0xffff0000, v158
	v_lshlrev_b32_e32 v154, 16, v161
	v_and_b32_e32 v155, 0xffff0000, v161
	v_cvt_pk_bf16_f32 v109, v124, v125
	v_pk_fma_f32 v[102:103], v[148:149], s[8:9], v[102:103] op_sel_hi:[1,0,1]
	global_store_dwordx4 v[138:139], v[106:109], off
	v_lshlrev_b32_e32 v150, 16, v159
	v_and_b32_e32 v151, 0xffff0000, v159
	v_pk_fma_f32 v[108:109], v[154:155], s[8:9], v[100:101] op_sel_hi:[1,0,1]
	v_pk_fma_f32 v[104:105], v[150:151], s[8:9], v[104:105] op_sel_hi:[1,0,1]
	v_cvt_pk_bf16_f32 v100, v102, v103
	v_lshlrev_b32_e32 v152, 16, v160
	v_and_b32_e32 v153, 0xffff0000, v160
	v_pk_fma_f32 v[98:99], v[152:153], s[8:9], v[98:99] op_sel_hi:[1,0,1]
	v_cvt_pk_bf16_f32 v101, v104, v105
	v_cvt_pk_bf16_f32 v102, v98, v99
	v_bfe_u32 v98, v108, 16, 1
	v_add3_u32 v98, v108, v98, s79
	v_lshrrev_b32_e32 v103, 16, v98
	v_or_b32_e32 v98, 48, v134
	v_ashrrev_i32_e32 v99, 31, v98
	v_lshlrev_b64 v[98:99], 11, v[98:99]
	v_lshl_add_u64 v[98:99], v[136:137], 0, v[98:99]
	global_load_dwordx4 v[104:107], v[98:99], off
	v_bfe_u32 v108, v109, 16, 1
	v_add3_u32 v108, v109, v108, s79
	v_and_or_b32 v103, v108, s77, v103
	global_store_dwordx4 v[138:139], v[100:103], off offset:256
	global_load_dwordx4 v[100:103], v[98:99], off offset:256
	s_waitcnt vmcnt(5)
	v_lshlrev_b32_e32 v108, 16, v116
	v_and_b32_e32 v109, 0xffff0000, v116
	v_lshlrev_b32_e32 v110, 16, v117
	v_and_b32_e32 v111, 0xffff0000, v117
	v_lshlrev_b32_e32 v112, 16, v118
	v_and_b32_e32 v113, 0xffff0000, v118
	v_lshlrev_b32_e32 v116, 16, v119
	v_and_b32_e32 v117, 0xffff0000, v119
	v_pk_fma_f32 v[94:95], v[108:109], s[8:9], v[94:95] op_sel_hi:[1,0,1]
	v_pk_fma_f32 v[108:109], v[116:117], s[8:9], v[92:93] op_sel_hi:[1,0,1]
	v_pk_fma_f32 v[92:93], v[112:113], s[8:9], v[90:91] op_sel_hi:[1,0,1]
	v_pk_fma_f32 v[96:97], v[110:111], s[8:9], v[96:97] op_sel_hi:[1,0,1]
	v_cvt_pk_bf16_f32 v90, v94, v95
	v_cvt_pk_bf16_f32 v91, v96, v97
	v_cvt_pk_bf16_f32 v92, v92, v93
	s_waitcnt vmcnt(4)
	v_lshlrev_b32_e32 v118, 16, v120
	v_and_b32_e32 v119, 0xffff0000, v120
	v_lshlrev_b32_e32 v124, 16, v122
	v_and_b32_e32 v125, 0xffff0000, v122
	v_lshlrev_b32_e32 v122, 16, v123
	v_and_b32_e32 v123, 0xffff0000, v123
	v_cvt_pk_bf16_f32 v93, v108, v109
	v_pk_fma_f32 v[86:87], v[118:119], s[8:9], v[86:87] op_sel_hi:[1,0,1]
	global_store_dwordx4 v[114:115], v[90:93], off
	v_lshlrev_b32_e32 v120, 16, v121
	v_and_b32_e32 v121, 0xffff0000, v121
	v_pk_fma_f32 v[90:91], v[122:123], s[8:9], v[84:85] op_sel_hi:[1,0,1]
	v_pk_fma_f32 v[84:85], v[124:125], s[8:9], v[82:83] op_sel_hi:[1,0,1]
	v_pk_fma_f32 v[88:89], v[120:121], s[8:9], v[88:89] op_sel_hi:[1,0,1]
	v_cvt_pk_bf16_f32 v82, v86, v87
	v_cvt_pk_bf16_f32 v83, v88, v89
	v_cvt_pk_bf16_f32 v84, v84, v85
	v_cvt_pk_bf16_f32 v85, v90, v91
	global_store_dwordx4 v[114:115], v[82:85], off offset:256
	s_waitcnt vmcnt(4)
	v_lshlrev_b32_e32 v92, 16, v104
	v_and_b32_e32 v93, 0xffff0000, v104
	v_add_u32_e32 v82, 0x80, v134
	v_ashrrev_i32_e32 v83, 31, v82
	v_lshlrev_b64 v[82:83], 11, v[82:83]
	v_lshl_add_u64 v[82:83], v[136:137], 0, v[82:83]
	global_load_dwordx4 v[84:87], v[82:83], off
	global_load_dwordx4 v[88:91], v[82:83], off offset:256
	v_lshlrev_b32_e32 v94, 16, v105
	v_and_b32_e32 v95, 0xffff0000, v105
	v_lshlrev_b32_e32 v96, 16, v106
	v_and_b32_e32 v97, 0xffff0000, v106
	v_lshlrev_b32_e32 v104, 16, v107
	v_and_b32_e32 v105, 0xffff0000, v107
	v_pk_fma_f32 v[78:79], v[92:93], s[8:9], v[78:79] op_sel_hi:[1,0,1]
	v_pk_fma_f32 v[92:93], v[104:105], s[8:9], v[76:77] op_sel_hi:[1,0,1]
	v_pk_fma_f32 v[76:77], v[96:97], s[8:9], v[74:75] op_sel_hi:[1,0,1]
	v_pk_fma_f32 v[80:81], v[94:95], s[8:9], v[80:81] op_sel_hi:[1,0,1]
	v_cvt_pk_bf16_f32 v74, v78, v79
	v_cvt_pk_bf16_f32 v75, v80, v81
	v_cvt_pk_bf16_f32 v76, v76, v77
	s_waitcnt vmcnt(4)
	v_lshlrev_b32_e32 v106, 16, v100
	v_and_b32_e32 v107, 0xffff0000, v100
	v_lshlrev_b32_e32 v108, 16, v102
	v_and_b32_e32 v109, 0xffff0000, v102
	v_lshlrev_b32_e32 v102, 16, v103
	v_and_b32_e32 v103, 0xffff0000, v103
	v_cvt_pk_bf16_f32 v77, v92, v93
	v_pk_fma_f32 v[70:71], v[106:107], s[8:9], v[70:71] op_sel_hi:[1,0,1]
	global_store_dwordx4 v[98:99], v[74:77], off
	v_lshlrev_b32_e32 v100, 16, v101
	v_and_b32_e32 v101, 0xffff0000, v101
	v_pk_fma_f32 v[76:77], v[102:103], s[8:9], v[68:69] op_sel_hi:[1,0,1]
	v_pk_fma_f32 v[72:73], v[100:101], s[8:9], v[72:73] op_sel_hi:[1,0,1]
	v_cvt_pk_bf16_f32 v68, v70, v71
	v_pk_fma_f32 v[66:67], v[108:109], s[8:9], v[66:67] op_sel_hi:[1,0,1]
	v_cvt_pk_bf16_f32 v69, v72, v73
	v_cvt_pk_bf16_f32 v70, v66, v67
	v_bfe_u32 v66, v76, 16, 1
	v_add3_u32 v66, v76, v66, s79
	v_lshrrev_b32_e32 v71, 16, v66
	v_add_u32_e32 v66, 0x90, v134
	v_ashrrev_i32_e32 v67, 31, v66
	v_lshlrev_b64 v[66:67], 11, v[66:67]
	v_lshl_add_u64 v[66:67], v[136:137], 0, v[66:67]
	global_load_dwordx4 v[72:75], v[66:67], off
	v_bfe_u32 v76, v77, 16, 1
	v_add3_u32 v76, v77, v76, s79
	v_and_or_b32 v71, v76, s77, v71
	global_store_dwordx4 v[98:99], v[68:71], off offset:256
	global_load_dwordx4 v[68:71], v[66:67], off offset:256
	s_waitcnt vmcnt(5)
	v_lshlrev_b32_e32 v76, 16, v84
	v_and_b32_e32 v77, 0xffff0000, v84
	v_lshlrev_b32_e32 v78, 16, v85
	v_and_b32_e32 v79, 0xffff0000, v85
	v_lshlrev_b32_e32 v80, 16, v86
	v_and_b32_e32 v81, 0xffff0000, v86
	v_lshlrev_b32_e32 v84, 16, v87
	v_and_b32_e32 v85, 0xffff0000, v87
	v_pk_fma_f32 v[62:63], v[76:77], s[8:9], v[62:63] op_sel_hi:[1,0,1]
	v_pk_fma_f32 v[76:77], v[84:85], s[8:9], v[60:61] op_sel_hi:[1,0,1]
	v_pk_fma_f32 v[60:61], v[80:81], s[8:9], v[58:59] op_sel_hi:[1,0,1]
	v_pk_fma_f32 v[64:65], v[78:79], s[8:9], v[64:65] op_sel_hi:[1,0,1]
	v_cvt_pk_bf16_f32 v58, v62, v63
	v_cvt_pk_bf16_f32 v59, v64, v65
	v_cvt_pk_bf16_f32 v60, v60, v61
	s_waitcnt vmcnt(4)
	v_lshlrev_b32_e32 v86, 16, v88
	v_and_b32_e32 v87, 0xffff0000, v88
	v_lshlrev_b32_e32 v92, 16, v90
	v_and_b32_e32 v93, 0xffff0000, v90
	v_lshlrev_b32_e32 v90, 16, v91
	v_and_b32_e32 v91, 0xffff0000, v91
	v_cvt_pk_bf16_f32 v61, v76, v77
	v_pk_fma_f32 v[54:55], v[86:87], s[8:9], v[54:55] op_sel_hi:[1,0,1]
	global_store_dwordx4 v[82:83], v[58:61], off
	v_lshlrev_b32_e32 v88, 16, v89
	v_and_b32_e32 v89, 0xffff0000, v89
	v_pk_fma_f32 v[58:59], v[90:91], s[8:9], v[52:53] op_sel_hi:[1,0,1]
	v_pk_fma_f32 v[52:53], v[92:93], s[8:9], v[50:51] op_sel_hi:[1,0,1]
	v_pk_fma_f32 v[56:57], v[88:89], s[8:9], v[56:57] op_sel_hi:[1,0,1]
	v_cvt_pk_bf16_f32 v50, v54, v55
	v_cvt_pk_bf16_f32 v51, v56, v57
	v_cvt_pk_bf16_f32 v52, v52, v53
	v_cvt_pk_bf16_f32 v53, v58, v59
	global_store_dwordx4 v[82:83], v[50:53], off offset:256
	s_waitcnt vmcnt(4)
	v_lshlrev_b32_e32 v60, 16, v72
	v_and_b32_e32 v61, 0xffff0000, v72
	v_add_u32_e32 v50, 0xa0, v134
	v_ashrrev_i32_e32 v51, 31, v50
	v_lshlrev_b64 v[50:51], 11, v[50:51]
	v_lshl_add_u64 v[50:51], v[136:137], 0, v[50:51]
	global_load_dwordx4 v[52:55], v[50:51], off
	global_load_dwordx4 v[56:59], v[50:51], off offset:256
	v_lshlrev_b32_e32 v62, 16, v73
	v_and_b32_e32 v63, 0xffff0000, v73
	v_lshlrev_b32_e32 v64, 16, v74
	v_and_b32_e32 v65, 0xffff0000, v74
	v_lshlrev_b32_e32 v72, 16, v75
	v_and_b32_e32 v73, 0xffff0000, v75
	v_pk_fma_f32 v[46:47], v[60:61], s[8:9], v[46:47] op_sel_hi:[1,0,1]
	v_pk_fma_f32 v[60:61], v[72:73], s[8:9], v[44:45] op_sel_hi:[1,0,1]
	v_pk_fma_f32 v[44:45], v[64:65], s[8:9], v[42:43] op_sel_hi:[1,0,1]
	v_pk_fma_f32 v[48:49], v[62:63], s[8:9], v[48:49] op_sel_hi:[1,0,1]
	v_cvt_pk_bf16_f32 v42, v46, v47
	v_cvt_pk_bf16_f32 v43, v48, v49
	v_cvt_pk_bf16_f32 v44, v44, v45
	s_waitcnt vmcnt(4)
	v_lshlrev_b32_e32 v74, 16, v68
	v_and_b32_e32 v75, 0xffff0000, v68
	v_lshlrev_b32_e32 v76, 16, v70
	v_and_b32_e32 v77, 0xffff0000, v70
	v_lshlrev_b32_e32 v70, 16, v71
	v_and_b32_e32 v71, 0xffff0000, v71
	v_cvt_pk_bf16_f32 v45, v60, v61
	v_pk_fma_f32 v[38:39], v[74:75], s[8:9], v[38:39] op_sel_hi:[1,0,1]
	global_store_dwordx4 v[66:67], v[42:45], off
	v_lshlrev_b32_e32 v68, 16, v69
	v_and_b32_e32 v69, 0xffff0000, v69
	v_pk_fma_f32 v[42:43], v[70:71], s[8:9], v[36:37] op_sel_hi:[1,0,1]
	v_pk_fma_f32 v[36:37], v[76:77], s[8:9], v[34:35] op_sel_hi:[1,0,1]
	v_pk_fma_f32 v[40:41], v[68:69], s[8:9], v[40:41] op_sel_hi:[1,0,1]
	v_cvt_pk_bf16_f32 v34, v38, v39
	v_cvt_pk_bf16_f32 v35, v40, v41
	v_bfe_u32 v38, v36, 16, 1
	v_add3_u32 v36, v36, v38, s79
	v_bfe_u32 v38, v37, 16, 1
	v_add3_u32 v37, v37, v38, s79
	v_add_u32_e32 v38, 0xb0, v134
	v_ashrrev_i32_e32 v39, 31, v38
	v_lshlrev_b64 v[38:39], 11, v[38:39]
	v_lshl_add_u64 v[44:45], v[136:137], 0, v[38:39]
	global_load_dwordx4 v[38:41], v[44:45], off
	v_lshrrev_b32_e32 v36, 16, v36
	v_and_or_b32 v36, v37, s77, v36
	v_cvt_pk_bf16_f32 v37, v42, v43
	global_store_dwordx4 v[66:67], v[34:37], off offset:256
	global_load_dwordx4 v[34:37], v[44:45], off offset:256
	s_waitcnt vmcnt(5)
	v_lshlrev_b32_e32 v42, 16, v52
	v_and_b32_e32 v43, 0xffff0000, v52
	v_lshlrev_b32_e32 v46, 16, v53
	v_and_b32_e32 v47, 0xffff0000, v53
	v_lshlrev_b32_e32 v48, 16, v54
	v_and_b32_e32 v49, 0xffff0000, v54
	v_lshlrev_b32_e32 v52, 16, v55
	v_and_b32_e32 v53, 0xffff0000, v55
	v_pk_fma_f32 v[30:31], v[42:43], s[8:9], v[30:31] op_sel_hi:[1,0,1]
	v_pk_fma_f32 v[42:43], v[52:53], s[8:9], v[28:29] op_sel_hi:[1,0,1]
	v_pk_fma_f32 v[28:29], v[48:49], s[8:9], v[26:27] op_sel_hi:[1,0,1]
	v_pk_fma_f32 v[32:33], v[46:47], s[8:9], v[32:33] op_sel_hi:[1,0,1]
	v_cvt_pk_bf16_f32 v26, v30, v31
	v_cvt_pk_bf16_f32 v27, v32, v33
	v_cvt_pk_bf16_f32 v28, v28, v29
	s_waitcnt vmcnt(4)
	v_lshlrev_b32_e32 v54, 16, v56
	v_and_b32_e32 v55, 0xffff0000, v56
	v_lshlrev_b32_e32 v60, 16, v58
	v_and_b32_e32 v61, 0xffff0000, v58
	v_lshlrev_b32_e32 v58, 16, v59
	v_and_b32_e32 v59, 0xffff0000, v59
	v_cvt_pk_bf16_f32 v29, v42, v43
	v_pk_fma_f32 v[22:23], v[54:55], s[8:9], v[22:23] op_sel_hi:[1,0,1]
	global_store_dwordx4 v[50:51], v[26:29], off
	v_lshlrev_b32_e32 v56, 16, v57
	v_and_b32_e32 v57, 0xffff0000, v57
	v_pk_fma_f32 v[26:27], v[58:59], s[8:9], v[20:21] op_sel_hi:[1,0,1]
	v_pk_fma_f32 v[20:21], v[60:61], s[8:9], v[18:19] op_sel_hi:[1,0,1]
	v_pk_fma_f32 v[24:25], v[56:57], s[8:9], v[24:25] op_sel_hi:[1,0,1]
	v_cvt_pk_bf16_f32 v18, v22, v23
	v_cvt_pk_bf16_f32 v19, v24, v25
	v_cvt_pk_bf16_f32 v20, v20, v21
	v_cvt_pk_bf16_f32 v21, v26, v27
	global_store_dwordx4 v[50:51], v[18:21], off offset:256
	s_waitcnt vmcnt(4)
	v_lshlrev_b32_e32 v22, 16, v40
	v_and_b32_e32 v23, 0xffff0000, v40
	v_lshlrev_b32_e32 v18, 16, v38
	v_and_b32_e32 v19, 0xffff0000, v38
	v_lshlrev_b32_e32 v24, 16, v41
	v_and_b32_e32 v25, 0xffff0000, v41
	v_pk_fma_f32 v[14:15], v[18:19], s[8:9], v[14:15] op_sel_hi:[1,0,1]
	v_pk_fma_f32 v[18:19], v[24:25], s[8:9], v[12:13] op_sel_hi:[1,0,1]
	v_pk_fma_f32 v[12:13], v[22:23], s[8:9], v[10:11] op_sel_hi:[1,0,1]
	v_lshlrev_b32_e32 v20, 16, v39
	v_and_b32_e32 v21, 0xffff0000, v39
	v_pk_fma_f32 v[16:17], v[20:21], s[8:9], v[16:17] op_sel_hi:[1,0,1]
	v_cvt_pk_bf16_f32 v10, v14, v15
	v_cvt_pk_bf16_f32 v11, v16, v17
	v_cvt_pk_bf16_f32 v12, v12, v13
	s_waitcnt vmcnt(2)
	v_lshlrev_b32_e32 v26, 16, v34
	v_and_b32_e32 v27, 0xffff0000, v34
	v_lshlrev_b32_e32 v30, 16, v36
	v_and_b32_e32 v31, 0xffff0000, v36
	v_lshlrev_b32_e32 v32, 16, v37
	v_and_b32_e32 v33, 0xffff0000, v37
	v_cvt_pk_bf16_f32 v13, v18, v19
	v_pk_fma_f32 v[6:7], v[26:27], s[8:9], v[6:7] op_sel_hi:[1,0,1]
	global_store_dwordx4 v[44:45], v[10:13], off
	v_lshlrev_b32_e32 v28, 16, v35
	v_and_b32_e32 v29, 0xffff0000, v35
	v_pk_fma_f32 v[10:11], v[32:33], s[8:9], v[4:5] op_sel_hi:[1,0,1]
	v_pk_fma_f32 v[4:5], v[30:31], s[8:9], v[2:3] op_sel_hi:[1,0,1]
	v_pk_fma_f32 v[8:9], v[28:29], s[8:9], v[8:9] op_sel_hi:[1,0,1]
	v_cvt_pk_bf16_f32 v2, v6, v7
	v_cvt_pk_bf16_f32 v3, v8, v9
	v_cvt_pk_bf16_f32 v4, v4, v5
	v_cvt_pk_bf16_f32 v5, v10, v11
	global_store_dwordx4 v[44:45], v[2:5], off offset:256
	s_cbranch_vccnz .LBB0_686
	s_andn2_b64 vcc, exec, s[4:5]
	s_cbranch_vccnz .LBB0_685
	s_barrier
	s_branch .LBB0_685

.LBB0_724:
	s_waitcnt vmcnt(7)
	v_lshlrev_b32_e32 v93, 16, v43
	v_lshlrev_b32_e32 v92, 16, v42
	v_and_b32_e32 v95, 0xffff0000, v43
	v_and_b32_e32 v94, 0xffff0000, v42
	v_pk_add_f32 v[96:97], v[92:93], v[94:95]
	v_and_b32_e32 v99, 0xffff0000, v45
	v_add_f32_e32 v85, v96, v97
	v_lshlrev_b32_e32 v97, 16, v45
	v_lshlrev_b32_e32 v96, 16, v44
	v_and_b32_e32 v98, 0xffff0000, v44
	v_pk_add_f32 v[100:101], v[96:97], v[98:99]
	s_waitcnt vmcnt(6)
	v_lshlrev_b32_e32 v80, 16, v46
	v_and_b32_e32 v81, 0xffff0000, v46
	v_lshlrev_b32_e32 v82, 16, v47
	v_and_b32_e32 v83, 0xffff0000, v47
	v_pk_add_f32 v[100:101], v[100:101], v[100:101] op_sel_hi:[0,1]
	v_lshlrev_b32_e32 v84, 16, v48
	v_and_b32_e32 v86, 0xffff0000, v48
	v_lshlrev_b32_e32 v88, 16, v49
	v_and_b32_e32 v90, 0xffff0000, v49
	v_add_f32_e32 v91, 0, v85
	v_add_f32_e32 v85, v80, v81
	v_add_f32_e32 v87, v82, v83
	v_mov_b32_e32 v89, v101
	v_pk_add_f32 v[102:103], v[84:85], v[86:87]
	v_pk_add_f32 v[100:101], v[88:89], v[90:91]
	s_nop 0
	v_pk_add_f32 v[100:101], v[102:103], v[100:101]
	s_nop 0
	v_add_f32_e32 v85, v100, v101
	s_waitcnt lgkmcnt(0)
	s_nop 1
	v_add_f32_dpp v85, v85, v85 quad_perm:[1,0,3,2] row_mask:0xf bank_mask:0xf
	s_nop 1
	v_add_f32_dpp v85, v85, v85 quad_perm:[2,3,0,1] row_mask:0xf bank_mask:0xf
	s_nop 1
	v_add_f32_dpp v85, v85, v85 row_half_mirror row_mask:0xf bank_mask:0xf
	s_nop 1
	v_add_f32_dpp v85, v85, v85 row_mirror row_mask:0xf bank_mask:0xf
	v_mov_b32_e32 v87, v85
	s_nop 1
	v_permlane16_swap_b32_e32 v85, v87
	v_add_f32_e32 v85, v85, v87
	v_mov_b32_e32 v87, v85
	s_nop 1
	v_permlane32_swap_b32_e32 v85, v87
	v_add_f32_e32 v85, v85, v87
	v_fmac_f32_e32 v94, 0xba800000, v85
	v_fmac_f32_e32 v95, 0xba800000, v85
	v_fmac_f32_e32 v93, 0xba800000, v85
	v_fmac_f32_e32 v92, 0xba800000, v85
	v_mov_b32_e32 v100, v93
	v_mov_b32_e32 v101, v95
	v_mov_b32_e32 v93, v94
	v_pk_mul_f32 v[102:103], v[100:101], v[100:101]
	v_pk_mul_f32 v[94:95], v[92:93], v[92:93]
	v_fmac_f32_e32 v98, 0xba800000, v85
	v_pk_mov_b32 v[104:105], v[94:95], v[102:103] op_sel:[1,0]
	v_mov_b32_e32 v95, v103
	v_fmac_f32_e32 v99, 0xba800000, v85
	v_fmac_f32_e32 v97, 0xba800000, v85
	v_pk_add_f32 v[94:95], v[104:105], v[94:95]
	v_fmac_f32_e32 v96, 0xba800000, v85
	v_mov_b32_e32 v102, v97
	v_mov_b32_e32 v103, v99
	v_mov_b32_e32 v97, v98
	v_pk_add_f32 v[94:95], v[94:95], v[94:95] op_sel_hi:[0,1]
	v_pk_mul_f32 v[104:105], v[102:103], v[102:103]
	v_pk_mul_f32 v[98:99], v[96:97], v[96:97]
	v_fmac_f32_e32 v80, 0xba800000, v85
	v_pk_mov_b32 v[106:107], v[98:99], v[104:105] op_sel:[1,0]
	v_mov_b32_e32 v99, v105
	v_fmac_f32_e32 v81, 0xba800000, v85
	v_fmac_f32_e32 v82, 0xba800000, v85
	v_mul_f32_e32 v94, v80, v80
	v_pk_add_f32 v[98:99], v[106:107], v[98:99]
	v_fmac_f32_e32 v83, 0xba800000, v85
	v_pk_fma_f32 v[104:105], v[80:81], v[80:81], v[94:95] op_sel_hi:[1,1,0]
	v_mul_f32_e32 v94, v82, v82
	v_pk_add_f32 v[98:99], v[98:99], v[98:99] op_sel_hi:[0,1]
	v_pk_fma_f32 v[106:107], v[82:83], v[82:83], v[94:95] op_sel_hi:[1,1,0]
	v_fmac_f32_e32 v90, 0xba800000, v85
	v_fmac_f32_e32 v88, 0xba800000, v85
	v_fmac_f32_e32 v86, 0xba800000, v85
	v_fmac_f32_e32 v84, 0xba800000, v85
	v_mul_f32_e32 v104, v84, v84
	v_mul_f32_e32 v106, v86, v86
	v_mul_f32_e32 v94, v88, v88
	v_mul_f32_e32 v98, v90, v90
	v_pk_add_f32 v[104:105], v[104:105], v[106:107]
	v_pk_add_f32 v[94:95], v[94:95], v[98:99]
	s_nop 0
	v_pk_add_f32 v[94:95], v[104:105], v[94:95]
	s_nop 0
	v_add_f32_e32 v85, v94, v95
	s_waitcnt lgkmcnt(0)
	s_nop 1
	v_add_f32_dpp v85, v85, v85 quad_perm:[1,0,3,2] row_mask:0xf bank_mask:0xf
	s_nop 1
	v_add_f32_dpp v85, v85, v85 quad_perm:[2,3,0,1] row_mask:0xf bank_mask:0xf
	s_nop 1
	v_add_f32_dpp v85, v85, v85 row_half_mirror row_mask:0xf bank_mask:0xf
	s_nop 1
	v_add_f32_dpp v85, v85, v85 row_mirror row_mask:0xf bank_mask:0xf
	v_mov_b32_e32 v87, v85
	s_nop 1
	v_permlane16_swap_b32_e32 v85, v87
	v_add_f32_e32 v85, v85, v87
	v_mov_b32_e32 v87, v85
	s_nop 1
	v_permlane32_swap_b32_e32 v85, v87
	v_add_f32_e32 v85, v85, v87
	v_fmamk_f32 v85, v85, 0x3a800000, v78
	v_mul_f32_e32 v87, 0x4f800000, v85
	v_cmp_gt_f32_e32 vcc, s6, v85
	s_nop 1
	v_cndmask_b32_e32 v85, v85, v87, vcc
	v_sqrt_f32_e32 v87, v85
	s_nop 0
	v_add_u32_e32 v89, -1, v87
	v_fma_f32 v91, -v89, v87, v85
	v_cmp_ge_f32_e64 s[0:1], 0, v91
	v_add_u32_e32 v91, 1, v87
	s_nop 0
	v_cndmask_b32_e64 v89, v87, v89, s[0:1]
	v_fma_f32 v87, -v91, v87, v85
	v_cmp_lt_f32_e64 s[0:1], 0, v87
	s_nop 1
	v_cndmask_b32_e64 v87, v89, v91, s[0:1]
	v_mul_f32_e32 v89, 0x37800000, v87
	v_cndmask_b32_e32 v87, v87, v89, vcc
	v_cmp_class_f32_e32 vcc, v85, v79
	s_nop 1
	v_cndmask_b32_e32 v85, v87, v85, vcc
	v_div_scale_f32 v87, s[0:1], v85, v85, 1.0
	v_rcp_f32_e32 v89, v87
	s_add_i32 s0, s4, 6
	s_cmp_gt_u32 s0, 12
	v_fma_f32 v91, -v87, v89, 1.0
	v_fmac_f32_e32 v89, v91, v89
	v_div_scale_f32 v91, vcc, 1.0, v85, 1.0
	v_mul_f32_e32 v94, v91, v89
	v_fma_f32 v95, -v87, v94, v91
	v_fmac_f32_e32 v94, v95, v89
	v_fma_f32 v87, -v87, v94, v91
	v_div_fmas_f32 v87, v87, v89, v94
	v_div_fixup_f32 v94, v87, v85, 1.0
	v_pk_mul_f32 v[92:93], v[92:93], v[94:95] op_sel_hi:[1,0]
	v_pk_mul_f32 v[80:81], v[80:81], v[94:95] op_sel_hi:[1,0]
	v_mov_b32_e32 v85, v86
	v_pk_fma_f32 v[92:93], v[6:7], v[92:93], v[14:15]
	v_pk_fma_f32 v[104:105], v[22:23], v[80:81], v[30:31]
	v_pk_mul_f32 v[80:81], v[84:85], v[94:95] op_sel_hi:[1,0]
	v_pk_mul_f32 v[98:99], v[100:101], v[94:95] op_sel_hi:[1,0]
	v_pk_fma_f32 v[86:87], v[18:19], v[80:81], v[26:27]
	v_pk_fma_f32 v[98:99], v[8:9], v[98:99], v[16:17]
	v_pk_mul_f32 v[82:83], v[82:83], v[94:95] op_sel_hi:[1,0]
	v_mov_b32_e32 v89, v90
	v_pk_mul_f32 v[100:101], v[102:103], v[94:95] op_sel_hi:[1,0]
	v_pk_fma_f32 v[102:103], v[24:25], v[82:83], v[32:33]
	v_pk_mul_f32 v[82:83], v[88:89], v[94:95] op_sel_hi:[1,0]
	v_cvt_pk_bf16_f32 v80, v92, v93
	v_pk_mul_f32 v[96:97], v[96:97], v[94:95] op_sel_hi:[1,0]
	v_pk_fma_f32 v[84:85], v[20:21], v[82:83], v[28:29]
	v_pk_fma_f32 v[96:97], v[2:3], v[96:97], v[10:11]
	v_cvt_pk_bf16_f32 v81, v98, v99
	v_pk_fma_f32 v[100:101], v[4:5], v[100:101], v[12:13]
	v_cvt_pk_bf16_f32 v82, v96, v97
	v_cvt_pk_bf16_f32 v83, v100, v101
	global_store_dwordx4 v[72:73], v[80:83], off offset:-1024
	s_nop 1
	v_cvt_pk_bf16_f32 v80, v104, v105
	v_cvt_pk_bf16_f32 v81, v102, v103
	v_cvt_pk_bf16_f32 v82, v86, v87
	v_cvt_pk_bf16_f32 v83, v84, v85
	global_store_dwordx4 v[70:71], v[80:83], off offset:-4096
	s_cbranch_scc1 .LBB0_726
	v_add3_u32 v42, v66, s4, 9
	v_ashrrev_i32_e32 v43, 31, v42
	v_lshlrev_b64 v[42:43], 11, v[42:43]
	v_lshl_add_u64 v[46:47], v[68:69], 0, v[42:43]
	global_load_dwordx4 v[42:45], v[46:47], off
	s_nop 0
	global_load_dwordx4 v[46:49], v[46:47], off offset:1024
.LBB0_726:
	s_waitcnt vmcnt(7)
	v_lshlrev_b32_e32 v91, 16, v51
	v_lshlrev_b32_e32 v90, 16, v50
	v_and_b32_e32 v93, 0xffff0000, v51
	v_and_b32_e32 v92, 0xffff0000, v50
	v_pk_add_f32 v[94:95], v[90:91], v[92:93]
	v_and_b32_e32 v97, 0xffff0000, v53
	v_add_f32_e32 v83, v94, v95
	v_lshlrev_b32_e32 v95, 16, v53
	v_lshlrev_b32_e32 v94, 16, v52
	v_and_b32_e32 v96, 0xffff0000, v52
	v_pk_add_f32 v[98:99], v[94:95], v[96:97]
	s_waitcnt vmcnt(6)
	v_lshlrev_b32_e32 v72, 16, v54
	v_and_b32_e32 v73, 0xffff0000, v54
	v_lshlrev_b32_e32 v80, 16, v55
	v_and_b32_e32 v81, 0xffff0000, v55
	v_pk_add_f32 v[98:99], v[98:99], v[98:99] op_sel_hi:[0,1]
	v_lshlrev_b32_e32 v82, 16, v56
	v_and_b32_e32 v84, 0xffff0000, v56
	v_lshlrev_b32_e32 v86, 16, v57
	v_and_b32_e32 v88, 0xffff0000, v57
	v_add_f32_e32 v89, 0, v83
	v_add_f32_e32 v83, v72, v73
	v_add_f32_e32 v85, v80, v81
	v_mov_b32_e32 v87, v99
	v_pk_add_f32 v[100:101], v[82:83], v[84:85]
	v_pk_add_f32 v[98:99], v[86:87], v[88:89]
	s_nop 0
	v_pk_add_f32 v[98:99], v[100:101], v[98:99]
	s_nop 0
	v_add_f32_e32 v83, v98, v99
	s_waitcnt lgkmcnt(0)
	s_nop 1
	v_add_f32_dpp v83, v83, v83 quad_perm:[1,0,3,2] row_mask:0xf bank_mask:0xf
	s_nop 1
	v_add_f32_dpp v83, v83, v83 quad_perm:[2,3,0,1] row_mask:0xf bank_mask:0xf
	s_nop 1
	v_add_f32_dpp v83, v83, v83 row_half_mirror row_mask:0xf bank_mask:0xf
	s_nop 1
	v_add_f32_dpp v83, v83, v83 row_mirror row_mask:0xf bank_mask:0xf
	v_mov_b32_e32 v85, v83
	s_nop 1
	v_permlane16_swap_b32_e32 v83, v85
	v_add_f32_e32 v83, v83, v85
	v_mov_b32_e32 v85, v83
	s_nop 1
	v_permlane32_swap_b32_e32 v83, v85
	v_add_f32_e32 v83, v83, v85
	v_fmac_f32_e32 v92, 0xba800000, v83
	v_fmac_f32_e32 v93, 0xba800000, v83
	v_fmac_f32_e32 v91, 0xba800000, v83
	v_fmac_f32_e32 v90, 0xba800000, v83
	v_mov_b32_e32 v98, v91
	v_mov_b32_e32 v99, v93
	v_mov_b32_e32 v91, v92
	v_pk_mul_f32 v[100:101], v[98:99], v[98:99]
	v_pk_mul_f32 v[92:93], v[90:91], v[90:91]
	v_fmac_f32_e32 v96, 0xba800000, v83
	v_pk_mov_b32 v[102:103], v[92:93], v[100:101] op_sel:[1,0]
	v_mov_b32_e32 v93, v101
	v_fmac_f32_e32 v97, 0xba800000, v83
	v_fmac_f32_e32 v95, 0xba800000, v83
	v_pk_add_f32 v[92:93], v[102:103], v[92:93]
	v_fmac_f32_e32 v94, 0xba800000, v83
	v_mov_b32_e32 v100, v95
	v_mov_b32_e32 v101, v97
	v_mov_b32_e32 v95, v96
	v_pk_add_f32 v[92:93], v[92:93], v[92:93] op_sel_hi:[0,1]
	v_pk_mul_f32 v[102:103], v[100:101], v[100:101]
	v_pk_mul_f32 v[96:97], v[94:95], v[94:95]
	v_fmac_f32_e32 v72, 0xba800000, v83
	v_pk_mov_b32 v[104:105], v[96:97], v[102:103] op_sel:[1,0]
	v_mov_b32_e32 v97, v103
	v_fmac_f32_e32 v73, 0xba800000, v83
	v_fmac_f32_e32 v80, 0xba800000, v83
	v_mul_f32_e32 v92, v72, v72
	v_pk_add_f32 v[96:97], v[104:105], v[96:97]
	v_fmac_f32_e32 v81, 0xba800000, v83
	v_pk_fma_f32 v[102:103], v[72:73], v[72:73], v[92:93] op_sel_hi:[1,1,0]
	v_mul_f32_e32 v92, v80, v80
	v_pk_add_f32 v[96:97], v[96:97], v[96:97] op_sel_hi:[0,1]
	v_pk_fma_f32 v[104:105], v[80:81], v[80:81], v[92:93] op_sel_hi:[1,1,0]
	v_fmac_f32_e32 v88, 0xba800000, v83
	v_fmac_f32_e32 v86, 0xba800000, v83
	v_fmac_f32_e32 v84, 0xba800000, v83
	v_fmac_f32_e32 v82, 0xba800000, v83
	v_mul_f32_e32 v102, v82, v82
	v_mul_f32_e32 v104, v84, v84
	v_mul_f32_e32 v92, v86, v86
	v_mul_f32_e32 v96, v88, v88
	v_pk_add_f32 v[102:103], v[102:103], v[104:105]
	v_pk_add_f32 v[92:93], v[92:93], v[96:97]
	s_nop 0
	v_pk_add_f32 v[92:93], v[102:103], v[92:93]
	s_nop 0
	v_add_f32_e32 v83, v92, v93
	s_waitcnt lgkmcnt(0)
	s_nop 1
	v_add_f32_dpp v83, v83, v83 quad_perm:[1,0,3,2] row_mask:0xf bank_mask:0xf
	s_nop 1
	v_add_f32_dpp v83, v83, v83 quad_perm:[2,3,0,1] row_mask:0xf bank_mask:0xf
	s_nop 1
	v_add_f32_dpp v83, v83, v83 row_half_mirror row_mask:0xf bank_mask:0xf
	s_nop 1
	v_add_f32_dpp v83, v83, v83 row_mirror row_mask:0xf bank_mask:0xf
	v_mov_b32_e32 v85, v83
	s_nop 1
	v_permlane16_swap_b32_e32 v83, v85
	v_add_f32_e32 v83, v83, v85
	v_mov_b32_e32 v85, v83
	s_nop 1
	v_permlane32_swap_b32_e32 v83, v85
	v_add_f32_e32 v83, v83, v85
	v_fmamk_f32 v83, v83, 0x3a800000, v78
	v_mul_f32_e32 v85, 0x4f800000, v83
	v_cmp_gt_f32_e32 vcc, s6, v83
	s_nop 1
	v_cndmask_b32_e32 v83, v83, v85, vcc
	v_sqrt_f32_e32 v85, v83
	s_nop 0
	v_add_u32_e32 v87, -1, v85
	v_fma_f32 v89, -v87, v85, v83
	v_cmp_ge_f32_e64 s[0:1], 0, v89
	v_add_u32_e32 v89, 1, v85
	s_nop 0
	v_cndmask_b32_e64 v87, v85, v87, s[0:1]
	v_fma_f32 v85, -v89, v85, v83
	v_cmp_lt_f32_e64 s[0:1], 0, v85
	s_nop 1
	v_cndmask_b32_e64 v85, v87, v89, s[0:1]
	v_mul_f32_e32 v87, 0x37800000, v85
	v_cndmask_b32_e32 v85, v85, v87, vcc
	v_cmp_class_f32_e32 vcc, v83, v79
	s_nop 1
	v_cndmask_b32_e32 v83, v85, v83, vcc
	v_div_scale_f32 v85, s[0:1], v83, v83, 1.0
	v_rcp_f32_e32 v87, v85
	s_add_i32 s0, s4, 7
	s_cmp_gt_u32 s0, 12
	v_fma_f32 v89, -v85, v87, 1.0
	v_fmac_f32_e32 v87, v89, v87
	v_div_scale_f32 v89, vcc, 1.0, v83, 1.0
	v_mul_f32_e32 v92, v89, v87
	v_fma_f32 v93, -v85, v92, v89
	v_fmac_f32_e32 v92, v93, v87
	v_fma_f32 v85, -v85, v92, v89
	v_div_fmas_f32 v85, v85, v87, v92
	v_div_fixup_f32 v92, v85, v83, 1.0
	v_pk_mul_f32 v[90:91], v[90:91], v[92:93] op_sel_hi:[1,0]
	v_pk_mul_f32 v[80:81], v[80:81], v[92:93] op_sel_hi:[1,0]
	v_mov_b32_e32 v83, v84
	v_pk_mul_f32 v[96:97], v[98:99], v[92:93] op_sel_hi:[1,0]
	v_pk_fma_f32 v[90:91], v[6:7], v[90:91], v[14:15]
	v_pk_mul_f32 v[98:99], v[100:101], v[92:93] op_sel_hi:[1,0]
	v_pk_fma_f32 v[100:101], v[24:25], v[80:81], v[32:33]
	v_pk_mul_f32 v[80:81], v[82:83], v[92:93] op_sel_hi:[1,0]
	v_mov_b32_e32 v87, v88
	v_pk_mul_f32 v[82:83], v[86:87], v[92:93] op_sel_hi:[1,0]
	v_pk_fma_f32 v[86:87], v[18:19], v[80:81], v[26:27]
	v_pk_fma_f32 v[96:97], v[8:9], v[96:97], v[16:17]
	v_cvt_pk_bf16_f32 v80, v90, v91
	v_pk_mul_f32 v[94:95], v[94:95], v[92:93] op_sel_hi:[1,0]
	v_pk_fma_f32 v[84:85], v[20:21], v[82:83], v[28:29]
	v_pk_fma_f32 v[94:95], v[2:3], v[94:95], v[10:11]
	v_cvt_pk_bf16_f32 v81, v96, v97
	v_pk_fma_f32 v[98:99], v[4:5], v[98:99], v[12:13]
	v_cvt_pk_bf16_f32 v82, v94, v95
	v_pk_mul_f32 v[72:73], v[72:73], v[92:93] op_sel_hi:[1,0]
	v_pk_fma_f32 v[72:73], v[22:23], v[72:73], v[30:31]
	v_cvt_pk_bf16_f32 v83, v98, v99
	global_store_dwordx4 v[70:71], v[80:83], off offset:-3072
	s_nop 1
	v_cvt_pk_bf16_f32 v80, v72, v73
	v_cvt_pk_bf16_f32 v81, v100, v101
	v_cvt_pk_bf16_f32 v82, v86, v87
	v_cvt_pk_bf16_f32 v83, v84, v85
	global_store_dwordx4 v[70:71], v[80:83], off offset:-2048
	s_cbranch_scc1 .LBB0_721
	v_add3_u32 v50, v66, s4, 10
	v_ashrrev_i32_e32 v51, 31, v50
	v_lshlrev_b64 v[50:51], 11, v[50:51]
	v_lshl_add_u64 v[54:55], v[68:69], 0, v[50:51]
	global_load_dwordx4 v[50:53], v[54:55], off
	s_nop 0
	global_load_dwordx4 v[54:57], v[54:55], off offset:1024
	s_branch .LBB0_721

.LBB0_767:
	v_cvt_pk_bf16_f32 v114, v130, v131
	v_cvt_pk_bf16_f32 v115, v132, v133
	s_lshl_b32 s4, s72, 8
	v_cvt_pk_bf16_f32 v116, v134, v135
	s_ashr_i32 s5, s4, 31
	v_lshl_add_u32 v166, s73, 8, v162
	v_lshl_add_u64 v[160:161], s[4:5], 1, v[154:155]
	v_mad_i64_i32 v[118:119], s[4:5], v166, s77, v[160:161]
	v_cvt_pk_bf16_f32 v117, v136, v137
	global_store_dwordx4 v[118:119], v[114:117], off
	s_nop 1
	v_cvt_pk_bf16_f32 v114, v138, v139
	v_cvt_pk_bf16_f32 v115, v140, v141
	v_cvt_pk_bf16_f32 v116, v142, v143
	v_cvt_pk_bf16_f32 v117, v144, v145
	global_store_dwordx4 v[118:119], v[114:117], off offset:256
	s_andn2_b64 vcc, exec, s[52:53]
	s_mov_b64 s[38:39], -1
	v_cndmask_b32_e64 v114, 0, 1, s[52:53]
	v_cmp_ne_u32_e64 s[4:5], 1, v114
	s_cbranch_vccnz .LBB0_771
	v_mov_b64_e32 v[116:117], v[112:113]
	v_mov_b64_e32 v[128:129], v[100:101]
	v_mov_b64_e32 v[124:125], v[104:105]
	v_mov_b64_e32 v[120:121], v[108:109]
	s_and_b64 vcc, exec, s[2:3]
	v_mov_b64_e32 v[114:115], v[110:111]
	v_mov_b64_e32 v[126:127], v[98:99]
	v_mov_b64_e32 v[122:123], v[102:103]
	v_mov_b64_e32 v[118:119], v[106:107]
	s_cbranch_vccnz .LBB0_770
	v_pk_mul_f32 v[116:117], v[112:113], s[20:21] op_sel_hi:[1,0]
	v_pk_mul_f32 v[114:115], v[110:111], s[20:21] op_sel_hi:[1,0]
	v_pk_mul_f32 v[120:121], v[108:109], s[20:21] op_sel_hi:[1,0]
	v_pk_mul_f32 v[118:119], v[106:107], s[20:21] op_sel_hi:[1,0]
	v_pk_mul_f32 v[124:125], v[104:105], s[20:21] op_sel_hi:[1,0]
	v_pk_mul_f32 v[122:123], v[102:103], s[20:21] op_sel_hi:[1,0]
	v_pk_mul_f32 v[128:129], v[100:101], s[20:21] op_sel_hi:[1,0]
	v_pk_mul_f32 v[126:127], v[98:99], s[20:21] op_sel_hi:[1,0]

.LBB0_773:
	v_or_b32_e32 v98, 16, v166
	v_mad_i64_i32 v[102:103], s[38:39], v98, s77, v[160:161]
	v_cvt_pk_bf16_f32 v98, v114, v115
	v_cvt_pk_bf16_f32 v99, v116, v117
	v_cvt_pk_bf16_f32 v100, v118, v119
	v_cvt_pk_bf16_f32 v101, v120, v121
	global_store_dwordx4 v[102:103], v[98:101], off
	s_nop 1
	v_cvt_pk_bf16_f32 v98, v122, v123
	v_cvt_pk_bf16_f32 v99, v124, v125
	v_cvt_pk_bf16_f32 v100, v126, v127
	v_cvt_pk_bf16_f32 v101, v128, v129
	s_and_b64 vcc, exec, s[4:5]
	s_mov_b64 s[38:39], -1
	global_store_dwordx4 v[102:103], v[98:101], off offset:256
	s_cbranch_vccnz .LBB0_777
	s_nop 0
	v_mov_b64_e32 v[100:101], v[96:97]
	v_mov_b64_e32 v[112:113], v[84:85]
	v_mov_b64_e32 v[108:109], v[88:89]
	v_mov_b64_e32 v[104:105], v[92:93]
	s_and_b64 vcc, exec, s[2:3]
	v_mov_b64_e32 v[98:99], v[94:95]
	v_mov_b64_e32 v[110:111], v[82:83]
	v_mov_b64_e32 v[106:107], v[86:87]
	v_mov_b64_e32 v[102:103], v[90:91]
	s_cbranch_vccnz .LBB0_776
	v_pk_mul_f32 v[100:101], v[96:97], s[20:21] op_sel_hi:[1,0]
	v_pk_mul_f32 v[98:99], v[94:95], s[20:21] op_sel_hi:[1,0]
	v_pk_mul_f32 v[104:105], v[92:93], s[20:21] op_sel_hi:[1,0]
	v_pk_mul_f32 v[102:103], v[90:91], s[20:21] op_sel_hi:[1,0]
	v_pk_mul_f32 v[108:109], v[88:89], s[20:21] op_sel_hi:[1,0]
	v_pk_mul_f32 v[106:107], v[86:87], s[20:21] op_sel_hi:[1,0]
	v_pk_mul_f32 v[112:113], v[84:85], s[20:21] op_sel_hi:[1,0]
	v_pk_mul_f32 v[110:111], v[82:83], s[20:21] op_sel_hi:[1,0]

.LBB0_779:
	v_or_b32_e32 v82, 32, v166
	v_mad_i64_i32 v[86:87], s[38:39], v82, s77, v[160:161]
	v_cvt_pk_bf16_f32 v82, v98, v99
	v_cvt_pk_bf16_f32 v83, v100, v101
	v_cvt_pk_bf16_f32 v84, v102, v103
	v_cvt_pk_bf16_f32 v85, v104, v105
	global_store_dwordx4 v[86:87], v[82:85], off
	s_nop 1
	v_cvt_pk_bf16_f32 v82, v106, v107
	v_cvt_pk_bf16_f32 v83, v108, v109
	v_cvt_pk_bf16_f32 v84, v110, v111
	v_cvt_pk_bf16_f32 v85, v112, v113
	s_and_b64 vcc, exec, s[4:5]
	s_mov_b64 s[38:39], -1
	global_store_dwordx4 v[86:87], v[82:85], off offset:256
	s_cbranch_vccnz .LBB0_783
	s_nop 0
	v_mov_b64_e32 v[84:85], v[80:81]
	v_mov_b64_e32 v[96:97], v[68:69]
	v_mov_b64_e32 v[92:93], v[72:73]
	v_mov_b64_e32 v[88:89], v[76:77]
	s_and_b64 vcc, exec, s[2:3]
	v_mov_b64_e32 v[82:83], v[78:79]
	v_mov_b64_e32 v[94:95], v[66:67]
	v_mov_b64_e32 v[90:91], v[70:71]
	v_mov_b64_e32 v[86:87], v[74:75]
	s_cbranch_vccnz .LBB0_782
	v_pk_mul_f32 v[84:85], v[80:81], s[20:21] op_sel_hi:[1,0]
	v_pk_mul_f32 v[82:83], v[78:79], s[20:21] op_sel_hi:[1,0]
	v_pk_mul_f32 v[88:89], v[76:77], s[20:21] op_sel_hi:[1,0]
	v_pk_mul_f32 v[86:87], v[74:75], s[20:21] op_sel_hi:[1,0]
	v_pk_mul_f32 v[92:93], v[72:73], s[20:21] op_sel_hi:[1,0]
	v_pk_mul_f32 v[90:91], v[70:71], s[20:21] op_sel_hi:[1,0]
	v_pk_mul_f32 v[96:97], v[68:69], s[20:21] op_sel_hi:[1,0]
	v_pk_mul_f32 v[94:95], v[66:67], s[20:21] op_sel_hi:[1,0]

.LBB0_785:
	v_or_b32_e32 v66, 48, v166
	v_mad_i64_i32 v[70:71], s[38:39], v66, s77, v[160:161]
	v_cvt_pk_bf16_f32 v66, v82, v83
	v_cvt_pk_bf16_f32 v67, v84, v85
	v_cvt_pk_bf16_f32 v68, v86, v87
	v_cvt_pk_bf16_f32 v69, v88, v89
	global_store_dwordx4 v[70:71], v[66:69], off
	s_nop 1
	v_cvt_pk_bf16_f32 v66, v90, v91
	v_cvt_pk_bf16_f32 v67, v92, v93
	v_cvt_pk_bf16_f32 v68, v94, v95
	v_cvt_pk_bf16_f32 v69, v96, v97
	s_and_b64 vcc, exec, s[4:5]
	s_mov_b64 s[38:39], -1
	global_store_dwordx4 v[70:71], v[66:69], off offset:256
	s_cbranch_vccnz .LBB0_789
	s_nop 0
	v_mov_b64_e32 v[68:69], v[64:65]
	v_mov_b64_e32 v[80:81], v[52:53]
	v_mov_b64_e32 v[76:77], v[56:57]
	v_mov_b64_e32 v[72:73], v[60:61]
	s_and_b64 vcc, exec, s[2:3]
	v_mov_b64_e32 v[66:67], v[62:63]
	v_mov_b64_e32 v[78:79], v[50:51]
	v_mov_b64_e32 v[74:75], v[54:55]
	v_mov_b64_e32 v[70:71], v[58:59]
	s_cbranch_vccnz .LBB0_788
	v_pk_mul_f32 v[68:69], v[64:65], s[20:21] op_sel_hi:[1,0]
	v_pk_mul_f32 v[66:67], v[62:63], s[20:21] op_sel_hi:[1,0]
	v_pk_mul_f32 v[72:73], v[60:61], s[20:21] op_sel_hi:[1,0]
	v_pk_mul_f32 v[70:71], v[58:59], s[20:21] op_sel_hi:[1,0]
	v_pk_mul_f32 v[76:77], v[56:57], s[20:21] op_sel_hi:[1,0]
	v_pk_mul_f32 v[74:75], v[54:55], s[20:21] op_sel_hi:[1,0]
	v_pk_mul_f32 v[80:81], v[52:53], s[20:21] op_sel_hi:[1,0]
	v_pk_mul_f32 v[78:79], v[50:51], s[20:21] op_sel_hi:[1,0]

.LBB0_791:
	v_add_u32_e32 v50, 0x80, v166
	v_mad_i64_i32 v[54:55], s[38:39], v50, s77, v[160:161]
	v_cvt_pk_bf16_f32 v50, v66, v67
	v_cvt_pk_bf16_f32 v51, v68, v69
	v_cvt_pk_bf16_f32 v52, v70, v71
	v_cvt_pk_bf16_f32 v53, v72, v73
	global_store_dwordx4 v[54:55], v[50:53], off
	s_nop 1
	v_cvt_pk_bf16_f32 v50, v74, v75
	v_cvt_pk_bf16_f32 v51, v76, v77
	v_cvt_pk_bf16_f32 v52, v78, v79
	v_cvt_pk_bf16_f32 v53, v80, v81
	s_and_b64 vcc, exec, s[4:5]
	s_mov_b64 s[38:39], -1
	global_store_dwordx4 v[54:55], v[50:53], off offset:256
	s_cbranch_vccnz .LBB0_795
	s_nop 0
	v_mov_b64_e32 v[52:53], v[48:49]
	v_mov_b64_e32 v[64:65], v[36:37]
	v_mov_b64_e32 v[60:61], v[40:41]
	v_mov_b64_e32 v[56:57], v[44:45]
	s_and_b64 vcc, exec, s[2:3]
	v_mov_b64_e32 v[50:51], v[46:47]
	v_mov_b64_e32 v[62:63], v[34:35]
	v_mov_b64_e32 v[58:59], v[38:39]
	v_mov_b64_e32 v[54:55], v[42:43]
	s_cbranch_vccnz .LBB0_794
	v_pk_mul_f32 v[52:53], v[48:49], s[20:21] op_sel_hi:[1,0]
	v_pk_mul_f32 v[50:51], v[46:47], s[20:21] op_sel_hi:[1,0]
	v_pk_mul_f32 v[56:57], v[44:45], s[20:21] op_sel_hi:[1,0]
	v_pk_mul_f32 v[54:55], v[42:43], s[20:21] op_sel_hi:[1,0]
	v_pk_mul_f32 v[60:61], v[40:41], s[20:21] op_sel_hi:[1,0]
	v_pk_mul_f32 v[58:59], v[38:39], s[20:21] op_sel_hi:[1,0]
	v_pk_mul_f32 v[64:65], v[36:37], s[20:21] op_sel_hi:[1,0]
	v_pk_mul_f32 v[62:63], v[34:35], s[20:21] op_sel_hi:[1,0]

.LBB0_797:
	v_add_u32_e32 v34, 0x90, v166
	v_mad_i64_i32 v[38:39], s[38:39], v34, s77, v[160:161]
	v_cvt_pk_bf16_f32 v34, v50, v51
	v_cvt_pk_bf16_f32 v35, v52, v53
	v_cvt_pk_bf16_f32 v36, v54, v55
	v_cvt_pk_bf16_f32 v37, v56, v57
	global_store_dwordx4 v[38:39], v[34:37], off
	s_nop 1
	v_cvt_pk_bf16_f32 v34, v58, v59
	v_cvt_pk_bf16_f32 v35, v60, v61
	v_cvt_pk_bf16_f32 v36, v62, v63
	v_cvt_pk_bf16_f32 v37, v64, v65
	s_and_b64 vcc, exec, s[4:5]
	s_mov_b64 s[38:39], -1
	global_store_dwordx4 v[38:39], v[34:37], off offset:256
	s_cbranch_vccnz .LBB0_801
	s_nop 0
	v_mov_b64_e32 v[36:37], v[32:33]
	v_mov_b64_e32 v[48:49], v[20:21]
	v_mov_b64_e32 v[44:45], v[24:25]
	v_mov_b64_e32 v[40:41], v[28:29]
	s_and_b64 vcc, exec, s[2:3]
	v_mov_b64_e32 v[34:35], v[30:31]
	v_mov_b64_e32 v[46:47], v[18:19]
	v_mov_b64_e32 v[42:43], v[22:23]
	v_mov_b64_e32 v[38:39], v[26:27]
	s_cbranch_vccnz .LBB0_800
	v_pk_mul_f32 v[36:37], v[32:33], s[20:21] op_sel_hi:[1,0]
	v_pk_mul_f32 v[34:35], v[30:31], s[20:21] op_sel_hi:[1,0]
	v_pk_mul_f32 v[40:41], v[28:29], s[20:21] op_sel_hi:[1,0]
	v_pk_mul_f32 v[38:39], v[26:27], s[20:21] op_sel_hi:[1,0]
	v_pk_mul_f32 v[44:45], v[24:25], s[20:21] op_sel_hi:[1,0]
	v_pk_mul_f32 v[42:43], v[22:23], s[20:21] op_sel_hi:[1,0]
	v_pk_mul_f32 v[48:49], v[20:21], s[20:21] op_sel_hi:[1,0]
	v_pk_mul_f32 v[46:47], v[18:19], s[20:21] op_sel_hi:[1,0]

.LBB0_803:
	v_add_u32_e32 v18, 0xa0, v166
	v_mad_i64_i32 v[22:23], s[38:39], v18, s77, v[160:161]
	v_cvt_pk_bf16_f32 v18, v34, v35
	v_cvt_pk_bf16_f32 v19, v36, v37
	v_cvt_pk_bf16_f32 v20, v38, v39
	v_cvt_pk_bf16_f32 v21, v40, v41
	global_store_dwordx4 v[22:23], v[18:21], off
	s_nop 1
	v_cvt_pk_bf16_f32 v18, v42, v43
	v_cvt_pk_bf16_f32 v19, v44, v45
	v_cvt_pk_bf16_f32 v20, v46, v47
	v_cvt_pk_bf16_f32 v21, v48, v49
	s_and_b64 vcc, exec, s[4:5]
	s_mov_b64 s[4:5], -1
	global_store_dwordx4 v[22:23], v[18:21], off offset:256
	s_cbranch_vccnz .LBB0_807
	s_nop 0
	v_mov_b64_e32 v[20:21], v[16:17]
	v_mov_b64_e32 v[32:33], v[4:5]
	v_mov_b64_e32 v[28:29], v[8:9]
	v_mov_b64_e32 v[24:25], v[12:13]
	s_and_b64 vcc, exec, s[2:3]
	v_mov_b64_e32 v[18:19], v[14:15]
	v_mov_b64_e32 v[30:31], v[2:3]
	v_mov_b64_e32 v[26:27], v[6:7]
	v_mov_b64_e32 v[22:23], v[10:11]
	s_cbranch_vccnz .LBB0_806
	v_pk_mul_f32 v[20:21], v[16:17], s[20:21] op_sel_hi:[1,0]
	v_pk_mul_f32 v[18:19], v[14:15], s[20:21] op_sel_hi:[1,0]
	v_pk_mul_f32 v[24:25], v[12:13], s[20:21] op_sel_hi:[1,0]
	v_pk_mul_f32 v[22:23], v[10:11], s[20:21] op_sel_hi:[1,0]
	v_pk_mul_f32 v[28:29], v[8:9], s[20:21] op_sel_hi:[1,0]
	v_pk_mul_f32 v[26:27], v[6:7], s[20:21] op_sel_hi:[1,0]
	v_pk_mul_f32 v[32:33], v[4:5], s[20:21] op_sel_hi:[1,0]
	v_pk_mul_f32 v[30:31], v[2:3], s[20:21] op_sel_hi:[1,0]

.LBB0_809:
	v_add_u32_e32 v2, 0xb0, v166
	v_mad_i64_i32 v[6:7], s[2:3], v2, s77, v[160:161]
	v_cvt_pk_bf16_f32 v2, v18, v19
	v_cvt_pk_bf16_f32 v3, v20, v21
	v_cvt_pk_bf16_f32 v4, v22, v23
	v_cvt_pk_bf16_f32 v5, v24, v25
	global_store_dwordx4 v[6:7], v[2:5], off
	s_nop 1
	v_cvt_pk_bf16_f32 v2, v26, v27
	v_cvt_pk_bf16_f32 v3, v28, v29
	v_cvt_pk_bf16_f32 v4, v30, v31
	v_cvt_pk_bf16_f32 v5, v32, v33
	s_mov_b64 s[2:3], -1
	s_and_b64 vcc, exec, s[44:45]
	global_store_dwordx4 v[6:7], v[2:5], off offset:256
	s_cbranch_vccz .LBB0_754
	s_and_b64 vcc, exec, s[6:7]
	s_cbranch_vccz .LBB0_753
	s_barrier
	s_branch .LBB0_753

.LBB0_955:
	s_cmp_lg_u32 0, -1
	s_cselect_b32 s0, 0, 0
	s_addk_i32 s0, 0x6000
	v_add3_u32 v8, v237, s0, v233
	s_add_i32 s0, s43, 0x4000
	v_add_f32_e32 v2, v243, v2
	s_and_b32 s0, s0, 0xffff
	v_add3_u32 v16, v8, v236, s0
	ds_read_b64_tr_b16 v[8:9],v16 offset:0
	ds_read_b64_tr_b16 v[10:11],v16 offset:512
	ds_read_b64_tr_b16 v[12:13],v16 offset:1024
	ds_read_b64_tr_b16 v[14:15],v16 offset:1536
	ds_read_b64_tr_b16 v[82:83],v16 offset:2048
	ds_read_b64_tr_b16 v[84:85],v16 offset:2560
	ds_read_b64_tr_b16 v[86:87],v16 offset:3072
	ds_read_b64_tr_b16 v[88:89],v16 offset:3584
	s_waitcnt lgkmcnt(0)
	s_nop 0
	v_mfma_f32_32x32x16_bf16 v[66:81], v[138:141], v[8:11], v[66:81]
	ds_read_b64_tr_b16 v[8:9],v16 offset:4096
	ds_read_b64_tr_b16 v[10:11],v16 offset:4608
	v_mfma_f32_32x32x16_bf16 v[66:81], v[134:137], v[12:15], v[66:81]
	ds_read_b64_tr_b16 v[12:13],v16 offset:5120
	ds_read_b64_tr_b16 v[14:15],v16 offset:5632
	v_mfma_f32_32x32x16_bf16 v[66:81], v[130:133], v[82:85], v[66:81]
	ds_read_b64_tr_b16 v[82:83],v16 offset:6144
	ds_read_b64_tr_b16 v[84:85],v16 offset:6656
	ds_read_b64_tr_b16 v[90:91],v16 offset:7168
	ds_read_b64_tr_b16 v[92:93],v16 offset:7680
	s_waitcnt lgkmcnt(0)
	v_mfma_f32_32x32x16_bf16 v[66:81], v[4:7], v[86:89], v[66:81]
	v_mfma_f32_32x32x16_bf16 v[50:65], v[138:141], v[8:11], v[50:65]
	v_add_u32_e32 v16, 0x2000, v16
	ds_read_b64_tr_b16 v[8:9],v16 offset:0
	ds_read_b64_tr_b16 v[10:11],v16 offset:512
	v_mfma_f32_32x32x16_bf16 v[50:65], v[134:137], v[12:15], v[50:65]
	ds_read_b64_tr_b16 v[12:13],v16 offset:1024
	ds_read_b64_tr_b16 v[14:15],v16 offset:1536
	v_mfma_f32_32x32x16_bf16 v[50:65], v[130:133], v[82:85], v[50:65]
	ds_read_b64_tr_b16 v[82:83],v16 offset:2048
	ds_read_b64_tr_b16 v[84:85],v16 offset:2560
	ds_read_b64_tr_b16 v[86:87],v16 offset:3072
	ds_read_b64_tr_b16 v[88:89],v16 offset:3584
	s_waitcnt lgkmcnt(0)
	v_mfma_f32_32x32x16_bf16 v[50:65], v[4:7], v[90:93], v[50:65]
	v_mfma_f32_32x32x16_bf16 v[34:49], v[138:141], v[8:11], v[34:49]
	ds_read_b64_tr_b16 v[8:9],v16 offset:4096
	ds_read_b64_tr_b16 v[10:11],v16 offset:4608
	v_mfma_f32_32x32x16_bf16 v[34:49], v[134:137], v[12:15], v[34:49]
	ds_read_b64_tr_b16 v[12:13],v16 offset:5120
	ds_read_b64_tr_b16 v[14:15],v16 offset:5632
	v_mfma_f32_32x32x16_bf16 v[34:49], v[130:133], v[82:85], v[34:49]
	ds_read_b64_tr_b16 v[82:83],v16 offset:6144
	ds_read_b64_tr_b16 v[84:85],v16 offset:6656
	ds_read_b64_tr_b16 v[90:91],v16 offset:7168
	ds_read_b64_tr_b16 v[92:93],v16 offset:7680
	s_waitcnt lgkmcnt(0)
	v_mfma_f32_32x32x16_bf16 v[34:49], v[4:7], v[86:89], v[34:49]
	v_mfma_f32_32x32x16_bf16 v[18:33], v[138:141], v[8:11], v[18:33]
	v_mov_b32_e32 v8, v2
	s_nop 1
	v_permlane32_swap_b32_e32 v2, v8
	v_cmp_gt_u32_e32 vcc, 32, v230
	v_mfma_f32_32x32x16_bf16 v[18:33], v[134:137], v[12:15], v[18:33]
	v_mfma_f32_32x32x16_bf16 v[18:33], v[130:133], v[82:85], v[18:33]
	v_mfma_f32_32x32x16_bf16 v[18:33], v[4:7], v[90:93], v[18:33]
	s_and_saveexec_b64 s[0:1], vcc
	v_add_f32_e32 v2, v2, v8
	ds_write_b32 v235, v2 offset:128
	s_or_b64 exec, exec, s[0:1]
	s_waitcnt lgkmcnt(0)
	ds_read_b128 v[4:7], v234 offset:128
	ds_read_b128 v[8:11], v234 offset:160
	s_lshl_b32 s0, s42, 8
	s_add_u32 s2, s6, s0
	s_addc_u32 s3, s7, 0
	s_waitcnt lgkmcnt(1)
	v_rcp_f32_e32 v14, v4
	v_rcp_f32_e32 v15, v5
	v_rcp_f32_e32 v16, v6
	v_rcp_f32_e32 v17, v7
	ds_read_b128 v[4:7], v234 offset:192
	s_lshl_b64 s[0:1], s[26:27], 11
	s_add_u32 s0, s2, s0
	s_addc_u32 s1, s3, s1
	s_lshl_b32 s2, s33, 12
	s_add_i32 s2, s2, 0
	v_lshlrev_b32_e32 v2, 1, v232
	s_add_i32 s2, s2, 0x16800
	v_and_b32_e32 v2, 0x70, v2
	s_waitcnt lgkmcnt(1)
	v_rcp_f32_e32 v82, v8
	v_rcp_f32_e32 v83, v9
	v_rcp_f32_e32 v84, v10
	v_rcp_f32_e32 v85, v11
	ds_read_b128 v[8:11], v234 offset:224
	s_waitcnt lgkmcnt(1)
	v_rcp_f32_e32 v86, v4
	v_lshlrev_b32_e32 v4, 1, v231
	v_add_u32_e32 v95, s2, v2
	v_lshl_add_u64 v[12:13], s[0:1], 0, v[2:3]
	v_lshlrev_b32_e32 v2, 9, v229
	v_add3_u32 v97, s2, v4, v2
	v_mul_f32_e32 v2, v66, v14
	v_cvt_pk_bf16_f32 v2, v2, s0
	ds_write_b16 v97, v2
	v_mul_f32_e32 v2, v50, v14
	v_cvt_pk_bf16_f32 v2, v2, s0
	ds_write_b16 v97, v2 offset:64
	v_mul_f32_e32 v2, v67, v15
	v_cvt_pk_bf16_f32 v2, v2, s0
	ds_write_b16 v97, v2 offset:128
	v_mul_f32_e32 v2, v51, v15
	v_cvt_pk_bf16_f32 v2, v2, s0
	ds_write_b16 v97, v2 offset:192
	v_mul_f32_e32 v2, v68, v16
	v_cvt_pk_bf16_f32 v2, v2, s0
	ds_write_b16 v97, v2 offset:256
	v_mul_f32_e32 v2, v52, v16
	v_cvt_pk_bf16_f32 v2, v2, s0
	ds_write_b16 v97, v2 offset:320
	v_mul_f32_e32 v2, v69, v17
	v_cvt_pk_bf16_f32 v2, v2, s0
	ds_write_b16 v97, v2 offset:384
	v_mul_f32_e32 v2, v53, v17
	v_cvt_pk_bf16_f32 v2, v2, s0
	ds_write_b16 v97, v2 offset:448
	v_mul_f32_e32 v2, v70, v82
	v_cvt_pk_bf16_f32 v2, v2, s0
	ds_write_b16 v97, v2 offset:1024
	v_mul_f32_e32 v2, v54, v82
	v_cvt_pk_bf16_f32 v2, v2, s0
	ds_write_b16 v97, v2 offset:1088
	v_mul_f32_e32 v2, v71, v83
	v_cvt_pk_bf16_f32 v2, v2, s0
	ds_write_b16 v97, v2 offset:1152
	v_mul_f32_e32 v2, v55, v83
	v_cvt_pk_bf16_f32 v2, v2, s0
	ds_write_b16 v97, v2 offset:1216
	v_mul_f32_e32 v2, v72, v84
	v_cvt_pk_bf16_f32 v2, v2, s0
	ds_write_b16 v97, v2 offset:1280
	v_mul_f32_e32 v2, v56, v84
	v_cvt_pk_bf16_f32 v2, v2, s0
	ds_write_b16 v97, v2 offset:1344
	v_mul_f32_e32 v2, v73, v85
	v_cvt_pk_bf16_f32 v2, v2, s0
	ds_write_b16 v97, v2 offset:1408
	v_mul_f32_e32 v2, v57, v85
	v_cvt_pk_bf16_f32 v2, v2, s0
	v_rcp_f32_e32 v87, v5
	ds_write_b16 v97, v2 offset:1472
	v_mul_f32_e32 v2, v74, v86
	v_cvt_pk_bf16_f32 v2, v2, s0
	ds_write_b16 v97, v2 offset:2048
	v_mul_f32_e32 v2, v58, v86
	v_cvt_pk_bf16_f32 v2, v2, s0
	v_rcp_f32_e32 v88, v6
	ds_write_b16 v97, v2 offset:2112
	v_mul_f32_e32 v2, v75, v87
	v_cvt_pk_bf16_f32 v2, v2, s0
	ds_write_b16 v97, v2 offset:2176
	v_mul_f32_e32 v2, v59, v87
	v_cvt_pk_bf16_f32 v2, v2, s0
	v_rcp_f32_e32 v89, v7
	ds_write_b16 v97, v2 offset:2240
	v_mul_f32_e32 v2, v76, v88
	v_cvt_pk_bf16_f32 v2, v2, s0
	ds_write_b16 v97, v2 offset:2304
	v_mul_f32_e32 v2, v60, v88
	v_cvt_pk_bf16_f32 v2, v2, s0
	s_waitcnt lgkmcnt(14)
	v_rcp_f32_e32 v90, v8
	ds_write_b16 v97, v2 offset:2368
	v_mul_f32_e32 v2, v77, v89
	v_cvt_pk_bf16_f32 v2, v2, s0
	ds_write_b16 v97, v2 offset:2432
	v_mul_f32_e32 v2, v61, v89
	v_cvt_pk_bf16_f32 v2, v2, s0
	v_rcp_f32_e32 v91, v9
	ds_write_b16 v97, v2 offset:2496
	v_mul_f32_e32 v2, v78, v90
	v_cvt_pk_bf16_f32 v2, v2, s0
	ds_write_b16 v97, v2 offset:3072
	v_mul_f32_e32 v2, v62, v90
	v_cvt_pk_bf16_f32 v2, v2, s0
	v_rcp_f32_e32 v92, v10
	ds_write_b16 v97, v2 offset:3136
	v_mul_f32_e32 v2, v79, v91
	v_cvt_pk_bf16_f32 v2, v2, s0
	ds_write_b16 v97, v2 offset:3200
	v_mul_f32_e32 v2, v63, v91
	v_cvt_pk_bf16_f32 v2, v2, s0
	v_rcp_f32_e32 v93, v11
	ds_write_b16 v97, v2 offset:3264
	v_mul_f32_e32 v2, v80, v92
	v_cvt_pk_bf16_f32 v2, v2, s0
	ds_write_b16 v97, v2 offset:3328
	v_mul_f32_e32 v2, v64, v92
	v_cvt_pk_bf16_f32 v2, v2, s0
	ds_write_b16 v97, v2 offset:3392
	v_mul_f32_e32 v2, v81, v93
	v_cvt_pk_bf16_f32 v2, v2, s0
	ds_write_b16 v97, v2 offset:3456
	v_mul_f32_e32 v2, v65, v93
	v_lshrrev_b32_e32 v94, 3, v230
	v_cvt_pk_bf16_f32 v2, v2, s0
	ds_write_b16 v97, v2 offset:3520
	v_or_b32_e32 v52, 8, v94
	v_lshl_add_u32 v96, v94, 7, v95
	s_waitcnt lgkmcnt(0)
	v_lshl_add_u32 v58, v52, 7, v95
	ds_read_b128 v[4:7], v96
	ds_read_b128 v[8:11], v58
	v_lshlrev_b32_e32 v2, 11, v94
	v_lshl_add_u64 v[50:51], v[12:13], 0, v[2:3]
	v_lshlrev_b32_e32 v2, 11, v52
	v_lshl_add_u64 v[52:53], v[12:13], 0, v[2:3]
	v_or_b32_e32 v2, 16, v94
	v_or_b32_e32 v56, 24, v94
	v_lshl_add_u32 v59, v2, 7, v95
	v_lshl_add_u32 v60, v56, 7, v95
	s_waitcnt lgkmcnt(1)
	global_store_dwordx4 v[50:51], v[4:7], off
	ds_read_b128 v[4:7], v59
	s_waitcnt lgkmcnt(1)
	global_store_dwordx4 v[52:53], v[8:11], off
	ds_read_b128 v[8:11], v60
	v_lshlrev_b32_e32 v2, 11, v2
	v_lshl_add_u64 v[54:55], v[12:13], 0, v[2:3]
	v_lshlrev_b32_e32 v2, 11, v56
	v_lshl_add_u64 v[56:57], v[12:13], 0, v[2:3]
	v_mul_f32_e32 v2, v34, v14
	s_waitcnt lgkmcnt(1)
	global_store_dwordx4 v[54:55], v[4:7], off
	s_waitcnt lgkmcnt(0)
	global_store_dwordx4 v[56:57], v[8:11], off
	v_cvt_pk_bf16_f32 v2, v2, s0
	s_waitcnt lgkmcnt(0)
	ds_write_b16 v97, v2
	v_mul_f32_e32 v2, v18, v14
	v_cvt_pk_bf16_f32 v2, v2, s0
	ds_write_b16 v97, v2 offset:64
	v_mul_f32_e32 v2, v35, v15
	v_cvt_pk_bf16_f32 v2, v2, s0
	ds_write_b16 v97, v2 offset:128
	v_mul_f32_e32 v2, v19, v15
	v_cvt_pk_bf16_f32 v2, v2, s0
	ds_write_b16 v97, v2 offset:192
	v_mul_f32_e32 v2, v36, v16
	v_cvt_pk_bf16_f32 v2, v2, s0
	ds_write_b16 v97, v2 offset:256
	v_mul_f32_e32 v2, v20, v16
	v_cvt_pk_bf16_f32 v2, v2, s0
	ds_write_b16 v97, v2 offset:320
	v_mul_f32_e32 v2, v37, v17
	v_cvt_pk_bf16_f32 v2, v2, s0
	ds_write_b16 v97, v2 offset:384
	v_mul_f32_e32 v2, v21, v17
	v_cvt_pk_bf16_f32 v2, v2, s0
	ds_write_b16 v97, v2 offset:448
	v_mul_f32_e32 v2, v38, v82
	v_cvt_pk_bf16_f32 v2, v2, s0
	ds_write_b16 v97, v2 offset:1024
	v_mul_f32_e32 v2, v22, v82
	v_cvt_pk_bf16_f32 v2, v2, s0
	ds_write_b16 v97, v2 offset:1088
	v_mul_f32_e32 v2, v39, v83
	v_cvt_pk_bf16_f32 v2, v2, s0
	ds_write_b16 v97, v2 offset:1152
	v_mul_f32_e32 v2, v23, v83
	v_cvt_pk_bf16_f32 v2, v2, s0
	ds_write_b16 v97, v2 offset:1216
	v_mul_f32_e32 v2, v40, v84
	v_cvt_pk_bf16_f32 v2, v2, s0
	ds_write_b16 v97, v2 offset:1280
	v_mul_f32_e32 v2, v24, v84
	v_cvt_pk_bf16_f32 v2, v2, s0
	ds_write_b16 v97, v2 offset:1344
	v_mul_f32_e32 v2, v41, v85
	v_cvt_pk_bf16_f32 v2, v2, s0
	ds_write_b16 v97, v2 offset:1408
	v_mul_f32_e32 v2, v25, v85
	v_cvt_pk_bf16_f32 v2, v2, s0
	ds_write_b16 v97, v2 offset:1472
	v_mul_f32_e32 v2, v42, v86
	v_cvt_pk_bf16_f32 v2, v2, s0
	ds_write_b16 v97, v2 offset:2048
	v_mul_f32_e32 v2, v26, v86
	v_cvt_pk_bf16_f32 v2, v2, s0
	ds_write_b16 v97, v2 offset:2112
	v_mul_f32_e32 v2, v43, v87
	v_cvt_pk_bf16_f32 v2, v2, s0
	ds_write_b16 v97, v2 offset:2176
	v_mul_f32_e32 v2, v27, v87
	v_cvt_pk_bf16_f32 v2, v2, s0
	ds_write_b16 v97, v2 offset:2240
	v_mul_f32_e32 v2, v44, v88
	v_cvt_pk_bf16_f32 v2, v2, s0
	ds_write_b16 v97, v2 offset:2304
	v_mul_f32_e32 v2, v28, v88
	v_cvt_pk_bf16_f32 v2, v2, s0
	ds_write_b16 v97, v2 offset:2368
	v_mul_f32_e32 v2, v45, v89
	v_cvt_pk_bf16_f32 v2, v2, s0
	ds_write_b16 v97, v2 offset:2432
	v_mul_f32_e32 v2, v29, v89
	v_cvt_pk_bf16_f32 v2, v2, s0
	ds_write_b16 v97, v2 offset:2496
	v_mul_f32_e32 v2, v46, v90
	v_cvt_pk_bf16_f32 v2, v2, s0
	ds_write_b16 v97, v2 offset:3072
	v_mul_f32_e32 v2, v30, v90
	v_cvt_pk_bf16_f32 v2, v2, s0
	ds_write_b16 v97, v2 offset:3136
	v_mul_f32_e32 v2, v47, v91
	v_cvt_pk_bf16_f32 v2, v2, s0
	ds_write_b16 v97, v2 offset:3200
	v_mul_f32_e32 v2, v31, v91
	v_cvt_pk_bf16_f32 v2, v2, s0
	ds_write_b16 v97, v2 offset:3264
	v_mul_f32_e32 v2, v48, v92
	v_cvt_pk_bf16_f32 v2, v2, s0
	ds_write_b16 v97, v2 offset:3328
	v_mul_f32_e32 v2, v32, v92
	v_cvt_pk_bf16_f32 v2, v2, s0
	ds_write_b16 v97, v2 offset:3392
	v_mul_f32_e32 v2, v49, v93
	v_cvt_pk_bf16_f32 v2, v2, s0
	ds_write_b16 v97, v2 offset:3456
	v_mul_f32_e32 v2, v33, v93
	v_cvt_pk_bf16_f32 v2, v2, s0
	ds_write_b16 v97, v2 offset:3520
	s_waitcnt lgkmcnt(0)
	ds_read_b128 v[4:7], v96
	ds_read_b128 v[8:11], v58
	ds_read_b128 v[12:15], v59
	ds_read_b128 v[16:19], v60
	s_waitcnt lgkmcnt(3)
	global_store_dwordx4 v[50:51], v[4:7], off offset:128
	s_waitcnt lgkmcnt(2)
	global_store_dwordx4 v[52:53], v[8:11], off offset:128
	s_waitcnt lgkmcnt(1)
	global_store_dwordx4 v[54:55], v[12:15], off offset:128
	s_waitcnt lgkmcnt(0)
	global_store_dwordx4 v[56:57], v[16:19], off offset:128
	s_waitcnt lgkmcnt(0)
	s_waitcnt lgkmcnt(0)
	s_barrier
	s_cmp_lt_u32 s21, 2
	s_cbranch_scc1 .LBB0_872
	v_mov_b32_e32 v6, v0
	s_lshl_b32 s0, s63, 8
	v_ashrrev_i32_e32 v4, 1, v6
	s_or_b32 s0, s8, s0
	s_mov_b32 s1, s9
	v_ashrrev_i32_e32 v5, 31, v4
	v_lshl_add_u64 v[12:13], s[0:1], 0, v[4:5]
	v_lshlrev_b32_e32 v2, 6, v6
	v_lshlrev_b64 v[4:5], 11, v[12:13]
	v_and_b32_e32 v7, 64, v2
	v_lshl_add_u64 v[4:5], s[6:7], 0, v[4:5]
	v_lshlrev_b32_e32 v2, 1, v7
	v_lshl_add_u64 v[4:5], v[4:5], 0, v[2:3]
	s_waitcnt vmcnt(0)
	s_barrier
	global_load_dwordx2 v[16:17], v[4:5], off sc1
	global_load_dwordx2 v[18:19], v[4:5], off offset:256 sc1
	global_load_dwordx2 v[24:25], v[4:5], off offset:8 sc1
	global_load_dwordx2 v[26:27], v[4:5], off offset:264 sc1
	global_load_dwordx2 v[30:31], v[4:5], off offset:16 sc1
	global_load_dwordx2 v[34:35], v[4:5], off offset:272 sc1
	global_load_dwordx2 v[42:43], v[4:5], off offset:24 sc1
	global_load_dwordx2 v[50:51], v[4:5], off offset:280 sc1
	v_lshlrev_b32_e32 v6, 2, v6
	v_bitop3_b32 v83, v6, 4, v228 bitop3:0x6c
	v_lshlrev_b32_e32 v82, 2, v7
	global_load_dwordx2 v[54:55], v[4:5], off offset:32 sc1
	global_load_dwordx2 v[60:61], v[4:5], off offset:288 sc1
	global_load_dwordx2 v[74:75], v[4:5], off offset:40 sc1
	global_load_dwordx2 v[84:85], v[4:5], off offset:296 sc1
	global_load_dwordx2 v[86:87], v[4:5], off offset:48 sc1
	global_load_dwordx2 v[88:89], v[4:5], off offset:304 sc1
	global_load_dwordx2 v[90:91], v[4:5], off offset:56 sc1
	global_load_dwordx2 v[28:29], v[4:5], off offset:312 sc1
	global_load_dwordx2 v[58:59], v[4:5], off offset:64 sc1
	global_load_dwordx2 v[36:37], v[4:5], off offset:320 sc1
	global_load_dwordx2 v[66:67], v[4:5], off offset:72 sc1
	global_load_dwordx2 v[44:45], v[4:5], off offset:328 sc1
	global_load_dwordx2 v[62:63], v[4:5], off offset:80 sc1
	global_load_dwordx2 v[52:53], v[4:5], off offset:336 sc1
	global_load_dwordx2 v[76:77], v[4:5], off offset:88 sc1
	global_load_dwordx2 v[32:33], v[4:5], off offset:344 sc1
	global_load_dwordx2 v[68:69], v[4:5], off offset:96 sc1
	global_load_dwordx2 v[38:39], v[4:5], off offset:352 sc1
	global_load_dwordx2 v[80:81], v[4:5], off offset:104 sc1
	global_load_dwordx2 v[20:21], v[4:5], off offset:360 sc1
	global_load_dwordx2 v[46:47], v[4:5], off offset:112 sc1
	global_load_dwordx2 v[22:23], v[4:5], off offset:368 sc1
	global_load_dwordx2 v[56:57], v[4:5], off offset:120 sc1
	global_load_dwordx2 v[48:49], v[4:5], off offset:376 sc1
	s_nop 0
	global_load_dwordx4 v[4:7], v82, s[58:59] offset:528
	global_load_dwordx4 v[8:11], v82, s[58:59] offset:512
	v_mov_b64_e32 v[14:15], s[16:17]
	v_mad_u64_u32 v[14:15], s[0:1], v12, s5, v[14:15]
	v_mad_i32_i24 v15, v13, s5, v15
	v_lshl_add_u64 v[12:13], v[14:15], 0, v[2:3]
	s_mov_b32 s0, 0xf800000
	s_waitcnt vmcnt(33)
	v_lshlrev_b32_e32 v41, 16, v17
	v_lshlrev_b32_e32 v40, 16, v16
	s_waitcnt vmcnt(32)
	v_lshlrev_b32_e32 v65, 16, v19
	v_lshlrev_b32_e32 v64, 16, v18
	v_and_b32_e32 v17, 0xffff0000, v17
	v_and_b32_e32 v16, 0xffff0000, v16
	v_and_b32_e32 v19, 0xffff0000, v19
	v_and_b32_e32 v18, 0xffff0000, v18
	s_waitcnt vmcnt(29)
	v_lshlrev_b32_e32 v95, 16, v31
	v_lshlrev_b32_e32 v94, 16, v30
	s_waitcnt vmcnt(28)
	v_lshlrev_b32_e32 v97, 16, v35
	v_lshlrev_b32_e32 v96, 16, v34
	v_and_b32_e32 v31, 0xffff0000, v31
	v_and_b32_e32 v30, 0xffff0000, v30
	v_and_b32_e32 v35, 0xffff0000, v35
	v_and_b32_e32 v34, 0xffff0000, v34
	v_pk_fma_f32 v[72:73], v[214:215], v[18:19], v[16:17] neg_lo:[1,0,0] neg_hi:[1,0,0]
	v_pk_fma_f32 v[18:19], v[214:215], v[96:97], v[94:95] neg_lo:[1,0,0] neg_hi:[1,0,0]
	v_pk_fma_f32 v[16:17], v[214:215], v[34:35], v[30:31] neg_lo:[1,0,0] neg_hi:[1,0,0]
	v_lshlrev_b32_e32 v71, 16, v25
	v_lshlrev_b32_e32 v70, 16, v24
	v_lshlrev_b32_e32 v93, 16, v27
	v_lshlrev_b32_e32 v92, 16, v26
	v_and_b32_e32 v25, 0xffff0000, v25
	v_and_b32_e32 v24, 0xffff0000, v24
	v_and_b32_e32 v27, 0xffff0000, v27
	v_and_b32_e32 v26, 0xffff0000, v26
	v_mov_b32_e32 v30, v18
	v_mov_b32_e32 v31, v16
	v_mul_f32_e32 v34, v16, v16
	v_pk_fma_f32 v[78:79], v[214:215], v[64:65], v[40:41] neg_lo:[1,0,0] neg_hi:[1,0,0]
	v_pk_fma_f32 v[64:65], v[214:215], v[26:27], v[24:25] neg_lo:[1,0,0] neg_hi:[1,0,0]
	v_pk_fma_f32 v[30:31], v[30:31], v[30:31], v[34:35] op_sel_hi:[1,1,0]
	v_mov_b32_e32 v34, v19
	v_mov_b32_e32 v35, v17
	v_mul_f32_e32 v40, v17, v17
	v_pk_fma_f32 v[70:71], v[214:215], v[92:93], v[70:71] neg_lo:[1,0,0] neg_hi:[1,0,0]
	v_pk_mul_f32 v[24:25], v[72:73], v[72:73]
	v_pk_mul_f32 v[26:27], v[64:65], v[64:65]
	v_pk_fma_f32 v[34:35], v[34:35], v[34:35], v[40:41] op_sel_hi:[1,1,0]
	s_waitcnt vmcnt(27)
	v_lshlrev_b32_e32 v41, 16, v43
	v_lshlrev_b32_e32 v40, 16, v42
	s_waitcnt vmcnt(26)
	v_lshlrev_b32_e32 v93, 16, v51
	v_lshlrev_b32_e32 v92, 16, v50
	v_and_b32_e32 v43, 0xffff0000, v43
	v_and_b32_e32 v42, 0xffff0000, v42
	v_and_b32_e32 v51, 0xffff0000, v51
	v_and_b32_e32 v50, 0xffff0000, v50
	v_pk_fma_f32 v[24:25], v[78:79], v[78:79], v[24:25]
	v_pk_fma_f32 v[26:27], v[70:71], v[70:71], v[26:27]
	v_pk_fma_f32 v[40:41], v[214:215], v[92:93], v[40:41] neg_lo:[1,0,0] neg_hi:[1,0,0]
	v_pk_fma_f32 v[50:51], v[214:215], v[50:51], v[42:43] neg_lo:[1,0,0] neg_hi:[1,0,0]
	v_pk_add_f32 v[24:25], v[24:25], v[24:25] op_sel:[0,1] op_sel_hi:[1,0]
	v_pk_add_f32 v[26:27], v[26:27], v[26:27] op_sel:[0,1] op_sel_hi:[1,0]
	v_pk_mul_f32 v[42:43], v[40:41], v[40:41]
	v_pk_mul_f32 v[92:93], v[50:51], v[50:51]
	v_mov_b32_e32 v25, v42
	v_mov_b32_e32 v27, v92
	v_mov_b32_e32 v31, v43
	v_mov_b32_e32 v35, v93
	v_pk_add_f32 v[24:25], v[24:25], v[26:27]
	v_pk_add_f32 v[26:27], v[30:31], v[34:35]
	s_waitcnt vmcnt(24)
	v_and_b32_e32 v31, 0xffff0000, v61
	v_pk_add_f32 v[24:25], v[24:25], v[26:27]
	v_lshlrev_b32_e32 v27, 16, v61
	v_pk_add_f32 v[92:93], v[24:25], v[24:25] op_sel:[0,1] op_sel_hi:[1,0]
	v_lshlrev_b32_e32 v25, 16, v55
	v_lshlrev_b32_e32 v24, 16, v54
	v_lshlrev_b32_e32 v26, 16, v60
	v_pk_fma_f32 v[26:27], v[214:215], v[26:27], v[24:25] neg_lo:[1,0,0] neg_hi:[1,0,0]
	v_and_b32_e32 v25, 0xffff0000, v55
	v_and_b32_e32 v24, 0xffff0000, v54
	v_and_b32_e32 v30, 0xffff0000, v60
	v_pk_fma_f32 v[34:35], v[214:215], v[30:31], v[24:25] neg_lo:[1,0,0] neg_hi:[1,0,0]
	s_waitcnt vmcnt(22)
	v_lshlrev_b32_e32 v31, 16, v85
	v_pk_mul_f32 v[24:25], v[34:35], v[34:35]
	v_lshlrev_b32_e32 v30, 16, v84
	v_pk_fma_f32 v[24:25], v[26:27], v[26:27], v[24:25]
	s_waitcnt vmcnt(0)
	v_mov_b32_e32 v15, v10
	v_pk_add_f32 v[60:61], v[24:25], v[24:25] op_sel:[0,1] op_sel_hi:[1,0]
	v_lshlrev_b32_e32 v25, 16, v75
	v_lshlrev_b32_e32 v24, 16, v74
	v_pk_fma_f32 v[42:43], v[214:215], v[30:31], v[24:25] neg_lo:[1,0,0] neg_hi:[1,0,0]
	v_and_b32_e32 v25, 0xffff0000, v75
	v_and_b32_e32 v24, 0xffff0000, v74
	v_and_b32_e32 v31, 0xffff0000, v85
	v_and_b32_e32 v30, 0xffff0000, v84
	v_pk_fma_f32 v[54:55], v[214:215], v[30:31], v[24:25] neg_lo:[1,0,0] neg_hi:[1,0,0]
	v_mov_b32_e32 v24, v42
	v_mov_b32_e32 v25, v54
	v_mul_f32_e32 v30, v54, v54
	v_pk_fma_f32 v[74:75], v[24:25], v[24:25], v[30:31] op_sel_hi:[1,1,0]
	v_mov_b32_e32 v24, v43
	v_mov_b32_e32 v25, v55
	v_mul_f32_e32 v30, v55, v55
	v_pk_fma_f32 v[84:85], v[24:25], v[24:25], v[30:31] op_sel_hi:[1,1,0]
	v_lshlrev_b32_e32 v25, 16, v87
	v_lshlrev_b32_e32 v24, 16, v86
	v_lshlrev_b32_e32 v31, 16, v89
	v_lshlrev_b32_e32 v30, 16, v88
	v_pk_fma_f32 v[24:25], v[214:215], v[30:31], v[24:25] neg_lo:[1,0,0] neg_hi:[1,0,0]
	v_and_b32_e32 v31, 0xffff0000, v87
	v_and_b32_e32 v30, 0xffff0000, v86
	v_and_b32_e32 v87, 0xffff0000, v89
	v_and_b32_e32 v86, 0xffff0000, v88
	v_pk_fma_f32 v[30:31], v[214:215], v[86:87], v[30:31] neg_lo:[1,0,0] neg_hi:[1,0,0]
	v_pk_mul_f32 v[86:87], v[24:25], v[24:25]
	v_pk_mul_f32 v[88:89], v[30:31], v[30:31]
	v_mov_b32_e32 v93, v86
	v_mov_b32_e32 v61, v88
	v_mov_b32_e32 v75, v87
	v_mov_b32_e32 v85, v89
	v_pk_add_f32 v[60:61], v[92:93], v[60:61]
	v_pk_add_f32 v[74:75], v[74:75], v[84:85]
	v_lshlrev_b32_e32 v89, 16, v37
	v_pk_add_f32 v[60:61], v[60:61], v[74:75]
	v_lshlrev_b32_e32 v75, 16, v29
	v_pk_add_f32 v[84:85], v[60:61], v[60:61] op_sel:[0,1] op_sel_hi:[1,0]
	v_lshlrev_b32_e32 v61, 16, v91
	v_lshlrev_b32_e32 v60, 16, v90
	v_lshlrev_b32_e32 v74, 16, v28
	v_pk_fma_f32 v[60:61], v[214:215], v[74:75], v[60:61] neg_lo:[1,0,0] neg_hi:[1,0,0]
	v_and_b32_e32 v75, 0xffff0000, v91
	v_and_b32_e32 v74, 0xffff0000, v90
	v_and_b32_e32 v29, 0xffff0000, v29
	v_and_b32_e32 v28, 0xffff0000, v28
	v_pk_fma_f32 v[74:75], v[214:215], v[28:29], v[74:75] neg_lo:[1,0,0] neg_hi:[1,0,0]
	v_lshlrev_b32_e32 v88, 16, v36
	v_pk_mul_f32 v[28:29], v[74:75], v[74:75]
	v_and_b32_e32 v37, 0xffff0000, v37
	v_pk_fma_f32 v[28:29], v[60:61], v[60:61], v[28:29]
	v_and_b32_e32 v36, 0xffff0000, v36
	v_pk_add_f32 v[86:87], v[28:29], v[28:29] op_sel:[0,1] op_sel_hi:[1,0]
	v_lshlrev_b32_e32 v29, 16, v59
	v_lshlrev_b32_e32 v28, 16, v58
	v_and_b32_e32 v59, 0xffff0000, v59
	v_and_b32_e32 v58, 0xffff0000, v58
	v_pk_fma_f32 v[28:29], v[214:215], v[88:89], v[28:29] neg_lo:[1,0,0] neg_hi:[1,0,0]
	v_pk_fma_f32 v[36:37], v[214:215], v[36:37], v[58:59] neg_lo:[1,0,0] neg_hi:[1,0,0]
	v_mov_b32_e32 v58, v28
	v_mov_b32_e32 v59, v36
	v_mul_f32_e32 v88, v36, v36
	v_pk_fma_f32 v[88:89], v[58:59], v[58:59], v[88:89] op_sel_hi:[1,1,0]
	v_mov_b32_e32 v58, v29
	v_mov_b32_e32 v59, v37
	v_mul_f32_e32 v90, v37, v37
	v_pk_fma_f32 v[90:91], v[58:59], v[58:59], v[90:91] op_sel_hi:[1,1,0]
	v_lshlrev_b32_e32 v59, 16, v67
	v_lshlrev_b32_e32 v58, 16, v66
	v_lshlrev_b32_e32 v93, 16, v45
	v_lshlrev_b32_e32 v92, 16, v44
	v_and_b32_e32 v67, 0xffff0000, v67
	v_and_b32_e32 v66, 0xffff0000, v66
	v_and_b32_e32 v45, 0xffff0000, v45
	v_and_b32_e32 v44, 0xffff0000, v44
	v_pk_fma_f32 v[58:59], v[214:215], v[92:93], v[58:59] neg_lo:[1,0,0] neg_hi:[1,0,0]
	v_pk_fma_f32 v[66:67], v[214:215], v[44:45], v[66:67] neg_lo:[1,0,0] neg_hi:[1,0,0]
	v_pk_mul_f32 v[44:45], v[58:59], v[58:59]
	v_pk_mul_f32 v[92:93], v[66:67], v[66:67]
	v_mov_b32_e32 v85, v44
	v_mov_b32_e32 v87, v92
	v_mov_b32_e32 v89, v45
	v_mov_b32_e32 v91, v93
	v_pk_add_f32 v[84:85], v[84:85], v[86:87]
	v_pk_add_f32 v[44:45], v[88:89], v[90:91]
	v_lshlrev_b32_e32 v87, 16, v53
	v_pk_add_f32 v[44:45], v[84:85], v[44:45]
	v_lshlrev_b32_e32 v86, 16, v52
	v_pk_add_f32 v[84:85], v[44:45], v[44:45] op_sel:[0,1] op_sel_hi:[1,0]
	v_lshlrev_b32_e32 v45, 16, v63
	v_lshlrev_b32_e32 v44, 16, v62
	v_and_b32_e32 v63, 0xffff0000, v63
	v_and_b32_e32 v62, 0xffff0000, v62
	v_and_b32_e32 v53, 0xffff0000, v53
	v_and_b32_e32 v52, 0xffff0000, v52
	v_pk_fma_f32 v[52:53], v[214:215], v[52:53], v[62:63] neg_lo:[1,0,0] neg_hi:[1,0,0]
	v_pk_fma_f32 v[44:45], v[214:215], v[86:87], v[44:45] neg_lo:[1,0,0] neg_hi:[1,0,0]
	v_pk_mul_f32 v[62:63], v[52:53], v[52:53]
	v_lshlrev_b32_e32 v89, 16, v33
	v_pk_fma_f32 v[62:63], v[44:45], v[44:45], v[62:63]
	v_lshlrev_b32_e32 v88, 16, v32
	v_pk_add_f32 v[86:87], v[62:63], v[62:63] op_sel:[0,1] op_sel_hi:[1,0]
	v_lshlrev_b32_e32 v63, 16, v77
	v_lshlrev_b32_e32 v62, 16, v76
	v_and_b32_e32 v77, 0xffff0000, v77
	v_and_b32_e32 v76, 0xffff0000, v76
	v_and_b32_e32 v33, 0xffff0000, v33
	v_and_b32_e32 v32, 0xffff0000, v32
	v_pk_fma_f32 v[62:63], v[214:215], v[88:89], v[62:63] neg_lo:[1,0,0] neg_hi:[1,0,0]
	v_pk_fma_f32 v[76:77], v[214:215], v[32:33], v[76:77] neg_lo:[1,0,0] neg_hi:[1,0,0]
	v_mov_b32_e32 v32, v62
	v_mov_b32_e32 v33, v76
	v_mul_f32_e32 v88, v76, v76
	v_pk_fma_f32 v[88:89], v[32:33], v[32:33], v[88:89] op_sel_hi:[1,1,0]
	v_mov_b32_e32 v32, v63
	v_mov_b32_e32 v33, v77
	v_mul_f32_e32 v90, v77, v77
	v_pk_fma_f32 v[90:91], v[32:33], v[32:33], v[90:91] op_sel_hi:[1,1,0]
	v_lshlrev_b32_e32 v33, 16, v69
	v_lshlrev_b32_e32 v32, 16, v68
	v_lshlrev_b32_e32 v93, 16, v39
	v_lshlrev_b32_e32 v92, 16, v38
	v_and_b32_e32 v69, 0xffff0000, v69
	v_and_b32_e32 v68, 0xffff0000, v68
	v_and_b32_e32 v39, 0xffff0000, v39
	v_and_b32_e32 v38, 0xffff0000, v38
	v_pk_fma_f32 v[32:33], v[214:215], v[92:93], v[32:33] neg_lo:[1,0,0] neg_hi:[1,0,0]
	v_pk_fma_f32 v[38:39], v[214:215], v[38:39], v[68:69] neg_lo:[1,0,0] neg_hi:[1,0,0]
	v_pk_mul_f32 v[68:69], v[32:33], v[32:33]
	v_pk_mul_f32 v[92:93], v[38:39], v[38:39]
	v_mov_b32_e32 v85, v68
	v_mov_b32_e32 v87, v92
	v_mov_b32_e32 v89, v69
	v_mov_b32_e32 v91, v93
	v_pk_add_f32 v[84:85], v[84:85], v[86:87]
	v_pk_add_f32 v[68:69], v[88:89], v[90:91]
	v_lshlrev_b32_e32 v87, 16, v21
	v_pk_add_f32 v[68:69], v[84:85], v[68:69]
	v_lshlrev_b32_e32 v86, 16, v20
	v_pk_add_f32 v[84:85], v[68:69], v[68:69] op_sel:[0,1] op_sel_hi:[1,0]
	v_lshlrev_b32_e32 v69, 16, v81
	v_lshlrev_b32_e32 v68, 16, v80
	v_and_b32_e32 v81, 0xffff0000, v81
	v_and_b32_e32 v80, 0xffff0000, v80
	v_and_b32_e32 v21, 0xffff0000, v21
	v_and_b32_e32 v20, 0xffff0000, v20
	v_pk_fma_f32 v[80:81], v[214:215], v[20:21], v[80:81] neg_lo:[1,0,0] neg_hi:[1,0,0]
	v_pk_fma_f32 v[68:69], v[214:215], v[86:87], v[68:69] neg_lo:[1,0,0] neg_hi:[1,0,0]
	v_pk_mul_f32 v[20:21], v[80:81], v[80:81]
	v_lshlrev_b32_e32 v89, 16, v23
	v_pk_fma_f32 v[20:21], v[68:69], v[68:69], v[20:21]
	v_lshlrev_b32_e32 v88, 16, v22
	v_pk_add_f32 v[86:87], v[20:21], v[20:21] op_sel:[0,1] op_sel_hi:[1,0]
	v_lshlrev_b32_e32 v21, 16, v47
	v_lshlrev_b32_e32 v20, 16, v46
	v_and_b32_e32 v47, 0xffff0000, v47
	v_and_b32_e32 v46, 0xffff0000, v46
	v_and_b32_e32 v23, 0xffff0000, v23
	v_and_b32_e32 v22, 0xffff0000, v22
	v_pk_fma_f32 v[20:21], v[214:215], v[88:89], v[20:21] neg_lo:[1,0,0] neg_hi:[1,0,0]
	v_pk_fma_f32 v[22:23], v[214:215], v[22:23], v[46:47] neg_lo:[1,0,0] neg_hi:[1,0,0]
	v_mov_b32_e32 v46, v20
	v_mov_b32_e32 v47, v22
	v_mul_f32_e32 v88, v22, v22
	v_pk_fma_f32 v[88:89], v[46:47], v[46:47], v[88:89] op_sel_hi:[1,1,0]
	v_mov_b32_e32 v46, v21
	v_mov_b32_e32 v47, v23
	v_mul_f32_e32 v90, v23, v23
	v_pk_fma_f32 v[90:91], v[46:47], v[46:47], v[90:91] op_sel_hi:[1,1,0]
	v_lshlrev_b32_e32 v47, 16, v57
	v_lshlrev_b32_e32 v46, 16, v56
	v_lshlrev_b32_e32 v93, 16, v49
	v_lshlrev_b32_e32 v92, 16, v48
	v_and_b32_e32 v57, 0xffff0000, v57
	v_and_b32_e32 v56, 0xffff0000, v56
	v_and_b32_e32 v49, 0xffff0000, v49
	v_and_b32_e32 v48, 0xffff0000, v48
	v_pk_fma_f32 v[46:47], v[214:215], v[92:93], v[46:47] neg_lo:[1,0,0] neg_hi:[1,0,0]
	v_pk_fma_f32 v[48:49], v[214:215], v[48:49], v[56:57] neg_lo:[1,0,0] neg_hi:[1,0,0]
	v_pk_mul_f32 v[56:57], v[46:47], v[46:47]
	v_pk_mul_f32 v[92:93], v[48:49], v[48:49]
	v_mov_b32_e32 v85, v56
	v_mov_b32_e32 v87, v92
	v_mov_b32_e32 v89, v57
	v_mov_b32_e32 v91, v93
	v_pk_add_f32 v[84:85], v[84:85], v[86:87]
	v_pk_add_f32 v[56:57], v[88:89], v[90:91]
	v_mov_b32_e32 v10, v9
	v_pk_add_f32 v[56:57], v[84:85], v[56:57]
	s_nop 0
	v_add_f32_e32 v56, v56, v57
	ds_bpermute_b32 v57, v83, v56
	s_waitcnt lgkmcnt(0)
	v_add_f32_e32 v2, v56, v57
	v_fmamk_f32 v2, v2, 0x3c000000, v1
	v_mul_f32_e32 v14, 0x4f800000, v2
	v_cmp_gt_f32_e32 vcc, s0, v2
	s_nop 1
	v_cndmask_b32_e32 v2, v2, v14, vcc
	v_sqrt_f32_e32 v56, v2
	v_mov_b32_e32 v14, v8
	v_add_u32_e32 v8, -1, v56
	v_fma_f32 v9, -v8, v56, v2
	v_cmp_ge_f32_e64 s[0:1], 0, v9
	v_add_u32_e32 v9, 1, v56
	s_nop 0
	v_cndmask_b32_e64 v8, v56, v8, s[0:1]
	v_fma_f32 v56, -v9, v56, v2
	v_cmp_lt_f32_e64 s[0:1], 0, v56
	s_nop 1
	v_cndmask_b32_e64 v8, v8, v9, s[0:1]
	v_mul_f32_e32 v9, 0x37800000, v8
	v_cndmask_b32_e32 v8, v8, v9, vcc
	v_cmp_class_f32_e32 vcc, v2, v226
	v_mov_b32_e32 v9, v6
	v_mov_b32_e32 v6, v5
	v_cndmask_b32_e32 v2, v8, v2, vcc
	v_div_scale_f32 v56, s[0:1], v2, v2, 1.0
	v_rcp_f32_e32 v57, v56
	v_mov_b32_e32 v8, v4
	v_fma_f32 v4, -v56, v57, 1.0
	v_fmac_f32_e32 v57, v4, v57
	v_div_scale_f32 v4, vcc, 1.0, v2, 1.0
	v_mul_f32_e32 v5, v4, v57
	v_fma_f32 v83, -v56, v5, v4
	v_fmac_f32_e32 v5, v83, v57
	v_fma_f32 v4, -v56, v5, v4
	v_div_fmas_f32 v4, v4, v57, v5
	v_div_fixup_f32 v2, v4, v2, 1.0
	v_mul_f32_e32 v2, 0x3f24fd5c, v2
	v_pk_mul_f32 v[4:5], v[78:79], v[2:3] op_sel_hi:[1,0]
	v_pk_mul_f32 v[16:17], v[16:17], v[2:3] op_sel_hi:[1,0]
	v_pk_mul_f32 v[4:5], v[14:15], v[4:5]
	v_pk_mul_f32 v[14:15], v[72:73], v[2:3] op_sel_hi:[1,0]
	s_nop 0
	v_pk_mul_f32 v[10:11], v[10:11], v[14:15]
	v_pk_mul_f32 v[14:15], v[70:71], v[2:3] op_sel_hi:[1,0]
	v_pk_mul_f32 v[8:9], v[8:9], v[14:15]
	v_pk_mul_f32 v[14:15], v[64:65], v[2:3] op_sel_hi:[1,0]
	v_pk_mul_f32 v[6:7], v[6:7], v[14:15]
	v_cvt_pk_bf16_f32 v7, v9, v7
	v_cvt_pk_bf16_f32 v6, v8, v6
	v_cvt_pk_bf16_f32 v5, v5, v11
	v_cvt_pk_bf16_f32 v4, v4, v10
	global_store_dwordx4 v[12:13], v[4:7], off offset:1024
	global_load_dwordx4 v[4:7], v82, s[58:59] offset:544
	s_nop 0
	global_load_dwordx4 v[8:11], v82, s[58:59] offset:560
	v_pk_mul_f32 v[14:15], v[18:19], v[2:3] op_sel_hi:[1,0]
	s_waitcnt vmcnt(1)
	v_mov_b32_e32 v19, v6
	v_mov_b32_e32 v6, v5
	v_mov_b32_e32 v18, v4
	v_pk_mul_f32 v[4:5], v[6:7], v[16:17]
	v_pk_mul_f32 v[6:7], v[40:41], v[2:3] op_sel_hi:[1,0]
	s_waitcnt vmcnt(0)
	v_mov_b32_e32 v16, v8
	v_mov_b32_e32 v17, v10
	v_pk_mul_f32 v[6:7], v[16:17], v[6:7]
	v_pk_mul_f32 v[16:17], v[50:51], v[2:3] op_sel_hi:[1,0]
	v_mov_b32_e32 v10, v9
	v_pk_mul_f32 v[8:9], v[10:11], v[16:17]
	v_pk_mul_f32 v[14:15], v[18:19], v[14:15]
	v_bfe_u32 v10, v9, 16, 1
	v_bfe_u32 v11, v8, 16, 1
	v_add3_u32 v8, v8, v11, s62
	v_add3_u32 v9, v9, v10, s62
	v_bfe_u32 v16, v6, 16, 1
	v_bfe_u32 v17, v7, 16, 1
	v_add3_u32 v7, v7, v17, s62
	v_add3_u32 v6, v6, v16, s62
	v_lshrrev_b32_e32 v6, 16, v6
	v_lshrrev_b32_e32 v7, 16, v7
	v_and_or_b32 v7, v9, s61, v7
	v_and_or_b32 v6, v8, s61, v6
	v_cvt_pk_bf16_f32 v5, v15, v5
	v_cvt_pk_bf16_f32 v4, v14, v4
	global_store_dwordx4 v[12:13], v[4:7], off offset:1040
	global_load_dwordx4 v[4:7], v82, s[58:59] offset:576
	s_nop 0
	global_load_dwordx4 v[8:11], v82, s[58:59] offset:592
	v_pk_mul_f32 v[14:15], v[26:27], v[2:3] op_sel_hi:[1,0]
	v_pk_mul_f32 v[18:19], v[62:63], v[2:3] op_sel_hi:[1,0]
	s_waitcnt vmcnt(1)
	v_mov_b32_e32 v16, v4
	v_mov_b32_e32 v17, v6
	v_pk_mul_f32 v[14:15], v[14:15], v[16:17]
	v_pk_mul_f32 v[16:17], v[34:35], v[2:3] op_sel_hi:[1,0]
	v_mov_b32_e32 v6, v5
	v_pk_mul_f32 v[4:5], v[16:17], v[6:7]
	v_pk_mul_f32 v[6:7], v[42:43], v[2:3] op_sel_hi:[1,0]
	s_waitcnt vmcnt(0)
	v_mov_b32_e32 v16, v8
	v_mov_b32_e32 v17, v10
	v_pk_mul_f32 v[6:7], v[6:7], v[16:17]
	v_pk_mul_f32 v[16:17], v[54:55], v[2:3] op_sel_hi:[1,0]
	v_mov_b32_e32 v10, v9
	v_pk_mul_f32 v[8:9], v[16:17], v[10:11]
	v_bfe_u32 v10, v9, 16, 1
	v_bfe_u32 v11, v8, 16, 1
	v_add3_u32 v8, v8, v11, s62
	v_add3_u32 v9, v9, v10, s62
	v_bfe_u32 v16, v6, 16, 1
	v_bfe_u32 v17, v7, 16, 1
	v_add3_u32 v7, v7, v17, s62
	v_add3_u32 v6, v6, v16, s62
	v_lshrrev_b32_e32 v6, 16, v6
	v_lshrrev_b32_e32 v7, 16, v7
	v_and_or_b32 v7, v9, s61, v7
	v_and_or_b32 v6, v8, s61, v6
	v_cvt_pk_bf16_f32 v5, v15, v5
	v_cvt_pk_bf16_f32 v4, v14, v4
	global_store_dwordx4 v[12:13], v[4:7], off offset:1056
	global_load_dwordx4 v[4:7], v82, s[58:59] offset:608
	s_nop 0
	global_load_dwordx4 v[8:11], v82, s[58:59] offset:624
	v_pk_mul_f32 v[14:15], v[24:25], v[2:3] op_sel_hi:[1,0]
	v_pk_mul_f32 v[24:25], v[76:77], v[2:3] op_sel_hi:[1,0]
	s_waitcnt vmcnt(1)
	v_mov_b32_e32 v16, v4
	v_mov_b32_e32 v17, v6
	v_pk_mul_f32 v[14:15], v[14:15], v[16:17]
	v_pk_mul_f32 v[16:17], v[30:31], v[2:3] op_sel_hi:[1,0]
	v_mov_b32_e32 v6, v5
	v_pk_mul_f32 v[4:5], v[16:17], v[6:7]
	v_pk_mul_f32 v[6:7], v[60:61], v[2:3] op_sel_hi:[1,0]
	s_waitcnt vmcnt(0)
	v_mov_b32_e32 v16, v8
	v_mov_b32_e32 v17, v10
	v_pk_mul_f32 v[6:7], v[6:7], v[16:17]
	v_pk_mul_f32 v[16:17], v[74:75], v[2:3] op_sel_hi:[1,0]
	v_mov_b32_e32 v10, v9
	v_pk_mul_f32 v[8:9], v[16:17], v[10:11]
	v_bfe_u32 v10, v9, 16, 1
	v_bfe_u32 v11, v8, 16, 1
	v_add3_u32 v8, v8, v11, s62
	v_add3_u32 v9, v9, v10, s62
	v_bfe_u32 v16, v6, 16, 1
	v_bfe_u32 v17, v7, 16, 1
	v_add3_u32 v7, v7, v17, s62
	v_add3_u32 v6, v6, v16, s62
	v_lshrrev_b32_e32 v6, 16, v6
	v_lshrrev_b32_e32 v7, 16, v7
	v_and_or_b32 v7, v9, s61, v7
	v_and_or_b32 v6, v8, s61, v6
	v_cvt_pk_bf16_f32 v5, v15, v5
	v_cvt_pk_bf16_f32 v4, v14, v4
	global_store_dwordx4 v[12:13], v[4:7], off offset:1072
	global_load_dwordx4 v[4:7], v82, s[58:59] offset:640
	s_nop 0
	global_load_dwordx4 v[8:11], v82, s[58:59] offset:656
	v_pk_mul_f32 v[14:15], v[28:29], v[2:3] op_sel_hi:[1,0]
	s_waitcnt vmcnt(1)
	v_mov_b32_e32 v16, v4
	v_mov_b32_e32 v17, v6
	v_pk_mul_f32 v[14:15], v[14:15], v[16:17]
	v_pk_mul_f32 v[16:17], v[36:37], v[2:3] op_sel_hi:[1,0]
	v_mov_b32_e32 v6, v5
	v_pk_mul_f32 v[4:5], v[16:17], v[6:7]
	v_pk_mul_f32 v[6:7], v[58:59], v[2:3] op_sel_hi:[1,0]
	s_waitcnt vmcnt(0)
	v_mov_b32_e32 v16, v8
	v_mov_b32_e32 v17, v10
	v_pk_mul_f32 v[6:7], v[6:7], v[16:17]
	v_pk_mul_f32 v[16:17], v[66:67], v[2:3] op_sel_hi:[1,0]
	v_mov_b32_e32 v10, v9
	v_pk_mul_f32 v[8:9], v[16:17], v[10:11]
	v_bfe_u32 v10, v9, 16, 1
	v_bfe_u32 v11, v8, 16, 1
	v_add3_u32 v8, v8, v11, s62
	v_add3_u32 v9, v9, v10, s62
	v_bfe_u32 v16, v6, 16, 1
	v_bfe_u32 v17, v7, 16, 1
	v_add3_u32 v7, v7, v17, s62
	v_add3_u32 v6, v6, v16, s62
	v_lshrrev_b32_e32 v6, 16, v6
	v_lshrrev_b32_e32 v7, 16, v7
	v_and_or_b32 v7, v9, s61, v7
	v_and_or_b32 v6, v8, s61, v6
	v_cvt_pk_bf16_f32 v5, v15, v5
	v_cvt_pk_bf16_f32 v4, v14, v4
	global_store_dwordx4 v[12:13], v[4:7], off offset:1088
	global_load_dwordx4 v[4:7], v82, s[58:59] offset:672
	s_nop 0
	global_load_dwordx4 v[8:11], v82, s[58:59] offset:688
	v_pk_mul_f32 v[16:17], v[52:53], v[2:3] op_sel_hi:[1,0]
	v_pk_mul_f32 v[14:15], v[44:45], v[2:3] op_sel_hi:[1,0]
	s_waitcnt vmcnt(1)
	v_mov_b32_e32 v27, v6
	v_mov_b32_e32 v6, v5
	s_waitcnt vmcnt(0)
	v_mov_b32_e32 v5, v10
	v_mov_b32_e32 v10, v9
	v_mov_b32_e32 v26, v4
	v_mov_b32_e32 v4, v8
	v_pk_mul_f32 v[6:7], v[16:17], v[6:7]
	v_pk_mul_f32 v[10:11], v[24:25], v[10:11]
	v_pk_mul_f32 v[8:9], v[14:15], v[26:27]
	v_pk_mul_f32 v[4:5], v[18:19], v[4:5]
	v_bfe_u32 v14, v11, 16, 1
	v_bfe_u32 v15, v10, 16, 1
	v_bfe_u32 v16, v7, 16, 1
	v_bfe_u32 v17, v6, 16, 1
	v_add3_u32 v17, v6, v17, s62
	v_add3_u32 v16, v7, v16, s62
	v_add3_u32 v6, v10, v15, s62
	v_add3_u32 v7, v11, v14, s62
	v_bfe_u32 v10, v8, 16, 1
	v_bfe_u32 v11, v9, 16, 1
	v_bfe_u32 v14, v4, 16, 1
	v_bfe_u32 v15, v5, 16, 1
	v_add3_u32 v5, v5, v15, s62
	v_add3_u32 v4, v4, v14, s62
	v_add3_u32 v9, v9, v11, s62
	v_add3_u32 v8, v8, v10, s62
	v_lshrrev_b32_e32 v8, 16, v8
	v_lshrrev_b32_e32 v9, 16, v9
	v_lshrrev_b32_e32 v4, 16, v4
	v_lshrrev_b32_e32 v5, 16, v5
	v_and_or_b32 v7, v7, s61, v5
	v_and_or_b32 v6, v6, s61, v4
	v_and_or_b32 v5, v16, s61, v9
	v_and_or_b32 v4, v17, s61, v8
	global_store_dwordx4 v[12:13], v[4:7], off offset:1104
	global_load_dwordx4 v[4:7], v82, s[58:59] offset:704
	s_nop 0
	global_load_dwordx4 v[8:11], v82, s[58:59] offset:720
	v_pk_mul_f32 v[14:15], v[32:33], v[2:3] op_sel_hi:[1,0]
	v_pk_mul_f32 v[18:19], v[68:69], v[2:3] op_sel_hi:[1,0]
	v_pk_mul_f32 v[16:17], v[38:39], v[2:3] op_sel_hi:[1,0]
	v_pk_mul_f32 v[24:25], v[80:81], v[2:3] op_sel_hi:[1,0]
	s_waitcnt vmcnt(1)
	v_mov_b32_e32 v26, v4
	v_mov_b32_e32 v27, v6
	v_mov_b32_e32 v6, v5
	s_waitcnt vmcnt(0)
	v_mov_b32_e32 v4, v8
	v_mov_b32_e32 v5, v10
	v_mov_b32_e32 v10, v9
	v_pk_mul_f32 v[8:9], v[14:15], v[26:27]
	v_pk_mul_f32 v[4:5], v[18:19], v[4:5]
	v_pk_mul_f32 v[6:7], v[16:17], v[6:7]
	v_pk_mul_f32 v[10:11], v[24:25], v[10:11]
	v_bfe_u32 v18, v8, 16, 1
	v_bfe_u32 v19, v9, 16, 1
	v_bfe_u32 v16, v7, 16, 1
	v_bfe_u32 v17, v6, 16, 1
	v_add3_u32 v9, v9, v19, s62
	v_add3_u32 v8, v8, v18, s62
	v_add3_u32 v17, v6, v17, s62
	v_add3_u32 v16, v7, v16, s62
	v_lshrrev_b32_e32 v8, 16, v8
	v_lshrrev_b32_e32 v9, 16, v9
	v_cvt_pk_bf16_f32 v7, v5, v11
	v_cvt_pk_bf16_f32 v6, v4, v10
	v_and_or_b32 v5, v16, s61, v9
	v_and_or_b32 v4, v17, s61, v8
	global_store_dwordx4 v[12:13], v[4:7], off offset:1120
	global_load_dwordx4 v[4:7], v82, s[58:59] offset:736
	s_nop 0
	global_load_dwordx4 v[8:11], v82, s[58:59] offset:752
	v_pk_mul_f32 v[14:15], v[20:21], v[2:3] op_sel_hi:[1,0]
	v_pk_mul_f32 v[16:17], v[22:23], v[2:3] op_sel_hi:[1,0]
	v_pk_mul_f32 v[18:19], v[46:47], v[2:3] op_sel_hi:[1,0]
	v_pk_mul_f32 v[20:21], v[48:49], v[2:3] op_sel_hi:[1,0]
	s_waitcnt vmcnt(1)
	v_mov_b32_e32 v22, v4
	v_mov_b32_e32 v23, v6
	v_mov_b32_e32 v6, v5
	s_waitcnt vmcnt(0)
	v_mov_b32_e32 v4, v8
	v_mov_b32_e32 v5, v10
	v_mov_b32_e32 v10, v9
	v_pk_mul_f32 v[8:9], v[14:15], v[22:23]
	v_pk_mul_f32 v[6:7], v[16:17], v[6:7]
	v_pk_mul_f32 v[4:5], v[18:19], v[4:5]
	v_pk_mul_f32 v[10:11], v[20:21], v[10:11]
	v_bfe_u32 v15, v7, 16, 1
	v_bfe_u32 v17, v8, 16, 1
	v_bfe_u32 v18, v9, 16, 1
	v_bfe_u32 v19, v4, 16, 1
	v_bfe_u32 v14, v10, 16, 1
	v_bfe_u32 v16, v6, 16, 1
	v_add3_u32 v15, v7, v15, s62
	v_add3_u32 v4, v4, v19, s62
	v_add3_u32 v7, v9, v18, s62
	v_add3_u32 v8, v8, v17, s62
	v_add3_u32 v16, v6, v16, s62
	v_add3_u32 v6, v10, v14, s62
	v_lshrrev_b32_e32 v8, 16, v8
	v_lshrrev_b32_e32 v9, 16, v7
	v_lshrrev_b32_e32 v4, 16, v4
	v_cvt_pk_bf16_f32 v7, v5, v11
	v_and_or_b32 v6, v6, s61, v4
	v_and_or_b32 v5, v15, s61, v9
	v_and_or_b32 v4, v16, s61, v8
	global_store_dwordx4 v[12:13], v[4:7], off offset:1136
	s_branch .LBB0_872

.LBB0_1145:
	s_or_b64 exec, exec, s[0:1]
	ds_read_b128 v[44:47], v53 offset:3888
	v_mov_b32_e32 v48, v34
	v_mov_b32_e32 v49, v34
	s_movk_i32 s0, 0x7fff
	s_mov_b32 s1, 0xffff0000
	s_waitcnt lgkmcnt(0)
	v_pk_fma_f32 v[34:35], v[34:35], v[36:37], v[44:45] neg_lo:[0,0,1] neg_hi:[0,0,1]
	v_xor_b32_e32 v47, 0x80000000, v47
	v_xor_b32_e32 v46, 0x80000000, v46
	v_pk_fma_f32 v[36:37], v[48:49], v[42:43], v[46:47]
	v_cvt_pk_bf16_f32 v34, v34, v35
	v_cvt_pk_bf16_f32 v35, v36, v37
	ds_write_b64 v51, v[34:35] offset:40984
	s_waitcnt lgkmcnt(0)
	s_barrier
	ds_read_b128 v[34:37], v55 offset:40960
	ds_read_b128 v[42:45], v55 offset:41024
	s_waitcnt vmcnt(11) lgkmcnt(1)
	v_mfma_f32_16x16x32_bf16 v[18:21], v[18:21], v[34:37], 0
	s_mov_b32 s3, 0
	s_waitcnt vmcnt(9)
	v_mfma_f32_16x16x32_bf16 v[22:25], v[22:25], v[34:37], 0
	s_waitcnt vmcnt(7)
	v_mfma_f32_16x16x32_bf16 v[26:29], v[26:29], v[34:37], 0
	s_waitcnt vmcnt(5)
	v_mfma_f32_16x16x32_bf16 v[30:33], v[30:33], v[34:37], 0
	s_waitcnt lgkmcnt(0)
	v_mfma_f32_16x16x32_bf16 v[14:17], v[14:17], v[42:45], v[18:21]
	v_mfma_f32_16x16x32_bf16 v[10:13], v[10:13], v[42:45], v[22:25]
	v_mfma_f32_16x16x32_bf16 v[6:9], v[6:9], v[42:45], v[26:29]
	s_waitcnt vmcnt(0)
	s_nop 4
	v_pk_mul_f32 v[16:17], v[16:17], v[102:103]
	v_pk_mul_f32 v[14:15], v[14:15], v[100:101]
	v_bfe_u32 v19, v16, 16, 1
	v_bfe_u32 v1, v14, 16, 1
	v_bfe_u32 v18, v15, 16, 1
	v_bfe_u32 v20, v17, 16, 1
	v_add3_u32 v1, v14, v1, s0
	v_add3_u32 v14, v15, v18, s0
	v_add3_u32 v15, v16, v19, s0
	v_add3_u32 v16, v17, v20, s0
	v_lshrrev_b32_e32 v1, 16, v1
	v_lshrrev_b32_e32 v15, 16, v15
	v_and_or_b32 v14, v14, s1, v1
	v_and_or_b32 v15, v16, s1, v15
	global_store_dwordx2 v[38:39], v[14:15], off offset:896
	v_mfma_f32_16x16x32_bf16 v[2:5], v[2:5], v[42:45], v[30:33]
	v_pk_mul_f32 v[12:13], v[12:13], v[106:107]
	v_pk_mul_f32 v[10:11], v[10:11], v[104:105]
	v_bfe_u32 v1, v10, 16, 1
	v_bfe_u32 v14, v11, 16, 1
	v_add3_u32 v1, v10, v1, s0
	v_add3_u32 v10, v11, v14, s0
	v_lshrrev_b32_e32 v1, 16, v1
	v_and_or_b32 v10, v10, s1, v1
	v_cvt_pk_bf16_f32 v11, v12, v13
	global_store_dwordx2 v[38:39], v[10:11], off offset:928
	v_pk_mul_f32 v[8:9], v[8:9], v[110:111]
	v_pk_mul_f32 v[6:7], v[6:7], v[108:109]
	v_bfe_u32 v1, v6, 16, 1
	v_bfe_u32 v10, v7, 16, 1
	v_add3_u32 v1, v6, v1, s0
	v_add3_u32 v6, v7, v10, s0
	v_lshrrev_b32_e32 v1, 16, v1
	v_and_or_b32 v6, v6, s1, v1
	v_cvt_pk_bf16_f32 v7, v8, v9
	global_store_dwordx2 v[38:39], v[6:7], off offset:960
	v_pk_mul_f32 v[4:5], v[4:5], v[114:115]
	v_pk_mul_f32 v[2:3], v[2:3], v[112:113]
	v_bfe_u32 v1, v2, 16, 1
	v_bfe_u32 v6, v3, 16, 1
	v_add3_u32 v1, v2, v1, s0
	v_add3_u32 v2, v3, v6, s0
	v_lshrrev_b32_e32 v1, 16, v1
	v_and_or_b32 v2, v2, s1, v1
	v_cvt_pk_bf16_f32 v3, v4, v5
	global_store_dwordx2 v[38:39], v[2:3], off offset:992
	s_barrier
	s_waitcnt vmcnt(0)
	s_barrier
	s_mov_b64 s[0:1], exec
	v_readlane_b32 s4, v254, 2
	v_readlane_b32 s5, v254, 3
	s_and_b64 s[4:5], s[0:1], s[4:5]
	s_mov_b64 exec, s[4:5]
	s_cbranch_execz .LBB0_1197
	s_mov_b32 s2, 0
	s_lshl_b64 s[2:3], s[2:3], 2
	v_readlane_b32 s4, v254, 0
	v_readlane_b32 s5, v254, 1
	s_add_u32 s2, s4, s2
	s_addc_u32 s3, s5, s3
	s_add_i32 s4, 0, 0x20160
	v_mov_b32_e32 v1, s4
	s_waitcnt vmcnt(0) expcnt(0) lgkmcnt(0)
	ds_read_b32 v3, v1
	s_add_i32 s4, 0, 0x20164
	v_mov_b32_e32 v1, s4
	ds_read_b32 v1, v1
	s_waitcnt lgkmcnt(1)
	v_cmp_ne_u32_e32 vcc, 0, v3
	s_cbranch_vccnz .LBB0_1161
	v_readlane_b32 s8, v254, 20
	v_readlane_b32 s9, v254, 21
	s_load_dword s6, s[8:9], 0x14
	s_load_dwordx2 s[4:5], s[8:9], 0x4
	s_mov_b32 s19, 1
	v_mov_b32_e32 v17, 0
	s_waitcnt lgkmcnt(0)
	s_lshr_b32 s8, s6, 16
	s_and_b32 s6, s6, 0xffff
	s_cmp_lg_u32 s6, 0
	s_cselect_b64 s[6:7], -1, 0
	s_cmp_lg_u64 s[6:7], 0
	s_addc_u32 s4, s4, 0
	v_readlane_b32 s6, v254, 22
	s_cmp_lg_u32 s8, 0
	s_mul_i32 s18, s4, s6
	s_cselect_b64 s[6:7], -1, 0
	s_cmp_lg_u64 s[6:7], 0
	s_addc_u32 s4, s5, 0
	s_mul_i32 s18, s18, s4
	s_add_u32 s4, s2, 0x1000
	s_addc_u32 s5, s3, 0
	s_add_u32 s6, s2, 0x1100
	s_addc_u32 s7, s3, 0
	s_add_u32 s8, s2, 0x1200
	s_addc_u32 s9, s3, 0
	s_add_u32 s10, s2, 0x1300
	s_addc_u32 s11, s3, 0
	s_branch .LBB0_1149

.LBB0_1233:
	s_waitcnt vmcnt(5)
	v_lshlrev_b32_e32 v217, 16, v163
	s_waitcnt lgkmcnt(2)
	v_lshlrev_b32_e32 v216, 16, v162
	v_and_b32_e32 v187, 0xffff0000, v163
	v_and_b32_e32 v186, 0xffff0000, v162
	v_pk_add_f32 v[188:189], v[216:217], v[186:187]
	v_lshlrev_b32_e32 v235, 16, v165
	v_add_f32_e32 v188, v188, v189
	v_add_f32_e32 v233, 0, v188
	v_lshlrev_b32_e32 v234, 16, v164
	v_and_b32_e32 v189, 0xffff0000, v165
	v_and_b32_e32 v188, 0xffff0000, v164
	v_pk_add_f32 v[190:191], v[234:235], v[188:189]
	s_waitcnt vmcnt(4)
	v_lshlrev_b32_e32 v194, 16, v166
	v_and_b32_e32 v195, 0xffff0000, v166
	v_lshlrev_b32_e32 v196, 16, v167
	v_and_b32_e32 v197, 0xffff0000, v167
	v_pk_add_f32 v[190:191], v[190:191], v[190:191] op_sel_hi:[0,1]
	v_lshlrev_b32_e32 v212, 16, v168
	v_and_b32_e32 v214, 0xffff0000, v168
	s_waitcnt lgkmcnt(1)
	v_lshlrev_b32_e32 v218, 16, v169
	s_waitcnt lgkmcnt(0)
	v_and_b32_e32 v232, 0xffff0000, v169
	v_add_f32_e32 v213, v194, v195
	v_add_f32_e32 v215, v196, v197
	v_mov_b32_e32 v219, v191
	v_pk_add_f32 v[192:193], v[212:213], v[214:215]
	v_pk_add_f32 v[190:191], v[218:219], v[232:233]
	s_nop 0
	v_pk_add_f32 v[190:191], v[192:193], v[190:191]
	s_nop 0
	v_add_f32_e32 v190, v190, v191
	s_waitcnt lgkmcnt(0)
	s_nop 1
	v_add_f32_dpp v190, v190, v190 quad_perm:[1,0,3,2] row_mask:0xf bank_mask:0xf
	s_nop 1
	v_add_f32_dpp v190, v190, v190 quad_perm:[2,3,0,1] row_mask:0xf bank_mask:0xf
	s_nop 1
	v_add_f32_dpp v190, v190, v190 row_half_mirror row_mask:0xf bank_mask:0xf
	s_nop 1
	v_add_f32_dpp v190, v190, v190 row_mirror row_mask:0xf bank_mask:0xf
	v_mov_b32_e32 v191, v190
	s_nop 1
	v_permlane16_swap_b32_e32 v190, v191
	v_add_f32_e32 v190, v190, v191
	v_mov_b32_e32 v191, v190
	s_nop 1
	v_permlane32_swap_b32_e32 v190, v191
	v_add_f32_e32 v210, v190, v191
	v_fmac_f32_e32 v186, 0xba800000, v210
	v_fmac_f32_e32 v187, 0xba800000, v210
	v_fmac_f32_e32 v217, 0xba800000, v210
	v_fmac_f32_e32 v216, 0xba800000, v210
	v_mov_b32_e32 v236, v217
	v_mov_b32_e32 v237, v187
	v_mov_b32_e32 v217, v186
	v_pk_mul_f32 v[190:191], v[236:237], v[236:237]
	v_pk_mul_f32 v[186:187], v[216:217], v[216:217]
	v_fmac_f32_e32 v188, 0xba800000, v210
	v_pk_mov_b32 v[192:193], v[186:187], v[190:191] op_sel:[1,0]
	v_mov_b32_e32 v187, v191
	v_fmac_f32_e32 v189, 0xba800000, v210
	v_fmac_f32_e32 v235, 0xba800000, v210
	v_pk_add_f32 v[186:187], v[192:193], v[186:187]
	v_fmac_f32_e32 v234, 0xba800000, v210
	v_mov_b32_e32 v238, v235
	v_mov_b32_e32 v239, v189
	v_mov_b32_e32 v235, v188
	v_pk_add_f32 v[186:187], v[186:187], v[186:187] op_sel_hi:[0,1]
	v_pk_mul_f32 v[190:191], v[238:239], v[238:239]
	v_pk_mul_f32 v[188:189], v[234:235], v[234:235]
	v_fmac_f32_e32 v194, 0xba800000, v210
	v_pk_mov_b32 v[192:193], v[188:189], v[190:191] op_sel:[1,0]
	v_mov_b32_e32 v189, v191
	v_fmac_f32_e32 v195, 0xba800000, v210
	v_fmac_f32_e32 v196, 0xba800000, v210
	v_mul_f32_e32 v186, v194, v194
	v_pk_add_f32 v[188:189], v[192:193], v[188:189]
	v_fmac_f32_e32 v197, 0xba800000, v210
	v_pk_fma_f32 v[190:191], v[194:195], v[194:195], v[186:187] op_sel_hi:[1,1,0]
	v_mul_f32_e32 v186, v196, v196
	v_pk_add_f32 v[188:189], v[188:189], v[188:189] op_sel_hi:[0,1]
	v_pk_fma_f32 v[192:193], v[196:197], v[196:197], v[186:187] op_sel_hi:[1,1,0]
	v_fmac_f32_e32 v232, 0xba800000, v210
	v_fmac_f32_e32 v218, 0xba800000, v210
	v_fmac_f32_e32 v214, 0xba800000, v210
	v_fmac_f32_e32 v212, 0xba800000, v210
	v_mul_f32_e32 v190, v212, v212
	v_mul_f32_e32 v192, v214, v214
	v_mul_f32_e32 v186, v218, v218
	v_mul_f32_e32 v188, v232, v232
	v_pk_add_f32 v[190:191], v[190:191], v[192:193]
	v_pk_add_f32 v[186:187], v[186:187], v[188:189]
	v_lshl_add_u64 v[210:211], s[94:95], 0, v[208:209]
	v_pk_add_f32 v[186:187], v[190:191], v[186:187]
	v_add_co_u32_e32 v190, vcc, 0xca01000, v210
	v_add_f32_e32 v186, v186, v187
	s_waitcnt lgkmcnt(0)
	v_addc_co_u32_e32 v191, vcc, 0, v211, vcc
	s_nop 1
	v_add_f32_dpp v186, v186, v186 quad_perm:[1,0,3,2] row_mask:0xf bank_mask:0xf
	s_nop 1
	v_add_f32_dpp v186, v186, v186 quad_perm:[2,3,0,1] row_mask:0xf bank_mask:0xf
	s_nop 1
	v_add_f32_dpp v186, v186, v186 row_half_mirror row_mask:0xf bank_mask:0xf
	s_nop 1
	v_add_f32_dpp v186, v186, v186 row_mirror row_mask:0xf bank_mask:0xf
	v_mov_b32_e32 v187, v186
	s_nop 1
	v_permlane16_swap_b32_e32 v186, v187
	v_add_f32_e32 v186, v186, v187
	v_mov_b32_e32 v187, v186
	s_nop 1
	v_permlane32_swap_b32_e32 v186, v187
	v_add_f32_e32 v186, v186, v187
	v_fmamk_f32 v186, v186, 0x3a800000, v228
	v_mul_f32_e32 v187, 0x4f800000, v186
	v_cmp_gt_f32_e64 s[0:1], s30, v186
	s_nop 1
	v_cndmask_b32_e64 v186, v186, v187, s[0:1]
	v_sqrt_f32_e32 v187, v186
	s_nop 0
	v_add_u32_e32 v188, -1, v187
	v_fma_f32 v189, -v188, v187, v186
	v_cmp_ge_f32_e64 s[4:5], 0, v189
	v_add_u32_e32 v189, 1, v187
	s_nop 0
	v_cndmask_b32_e64 v188, v187, v188, s[4:5]
	v_fma_f32 v187, -v189, v187, v186
	v_cmp_lt_f32_e64 s[4:5], 0, v187
	s_nop 1
	v_cndmask_b32_e64 v187, v188, v189, s[4:5]
	v_mul_f32_e32 v188, 0x37800000, v187
	v_cndmask_b32_e64 v187, v187, v188, s[0:1]
	v_cmp_class_f32_e64 s[0:1], v186, v229
	s_nop 1
	v_cndmask_b32_e64 v213, v187, v186, s[0:1]
	v_div_scale_f32 v215, s[0:1], v213, v213, 1.0
	v_rcp_f32_e32 v219, v215
	global_load_dwordx4 v[186:189], v[190:191], off offset:2048
	s_nop 0
	global_load_dwordx4 v[190:193], v[190:191], off offset:3072
	v_fma_f32 v233, -v215, v219, 1.0
	v_fmac_f32_e32 v219, v233, v219
	v_div_scale_f32 v233, vcc, 1.0, v213, 1.0
	v_mul_f32_e32 v240, v233, v219
	v_fma_f32 v241, -v215, v240, v233
	v_fmac_f32_e32 v240, v241, v219
	v_fma_f32 v215, -v215, v240, v233
	v_div_fmas_f32 v215, v215, v219, v240
	v_div_fixup_f32 v240, v215, v213, 1.0
	v_pk_mul_f32 v[216:217], v[216:217], v[240:241] op_sel_hi:[1,0]
	v_pk_mul_f32 v[194:195], v[194:195], v[240:241] op_sel_hi:[1,0]
	v_mov_b32_e32 v213, v214
	v_pk_fma_f32 v[242:243], v[2:3], v[216:217], v[6:7]
	v_pk_mul_f32 v[216:217], v[234:235], v[240:241] op_sel_hi:[1,0]
	v_pk_mul_f32 v[196:197], v[196:197], v[240:241] op_sel_hi:[1,0]
	v_pk_fma_f32 v[244:245], v[18:19], v[194:195], v[30:31]
	v_pk_mul_f32 v[194:195], v[212:213], v[240:241] op_sel_hi:[1,0]
	v_mov_b32_e32 v219, v232
	v_pk_mul_f32 v[234:235], v[238:239], v[240:241] op_sel_hi:[1,0]
	v_pk_fma_f32 v[238:239], v[14:15], v[216:217], v[26:27]
	v_pk_fma_f32 v[216:217], v[20:21], v[196:197], v[32:33]
	v_pk_mul_f32 v[196:197], v[218:219], v[240:241] op_sel_hi:[1,0]
	v_pk_fma_f32 v[218:219], v[10:11], v[194:195], v[22:23]
	v_pk_mul_f32 v[236:237], v[236:237], v[240:241] op_sel_hi:[1,0]
	v_pk_fma_f32 v[236:237], v[4:5], v[236:237], v[8:9]
	v_cvt_pk_bf16_f32 v194, v242, v243
	v_pk_fma_f32 v[214:215], v[12:13], v[196:197], v[24:25]
	v_cvt_pk_bf16_f32 v195, v236, v237
	v_fma_f32 v240, v36, v242, 0
	v_fma_f32 v241, v37, v242, 0
	v_fma_f32 v246, v38, v242, 0
	v_fma_f32 v247, v39, v242, 0
	v_fma_f32 v248, v40, v242, 0
	v_fma_f32 v249, v41, v242, 0
	v_pk_fma_f32 v[232:233], v[34:35], v[242:243], 0 op_sel_hi:[1,0,0]
	v_pk_fma_f32 v[234:235], v[16:17], v[234:235], v[28:29]
	v_fmac_f32_e32 v240, v44, v243
	v_fmac_f32_e32 v241, v45, v243
	v_fmac_f32_e32 v246, v46, v243
	v_fmac_f32_e32 v247, v47, v243
	v_fmac_f32_e32 v248, v48, v243
	v_fmac_f32_e32 v249, v49, v243
	v_pk_fma_f32 v[232:233], v[42:43], v[242:243], v[232:233] op_sel:[0,1,0]
	v_cvt_pk_bf16_f32 v196, v238, v239
	v_fmac_f32_e32 v240, v52, v236
	v_fmac_f32_e32 v241, v53, v236
	v_fmac_f32_e32 v246, v54, v236
	v_fmac_f32_e32 v247, v55, v236
	v_fmac_f32_e32 v248, v56, v236
	v_fmac_f32_e32 v249, v57, v236
	v_pk_fma_f32 v[232:233], v[50:51], v[236:237], v[232:233] op_sel_hi:[1,0,1]
	v_fmac_f32_e32 v240, v60, v237
	v_fmac_f32_e32 v241, v61, v237
	v_fmac_f32_e32 v246, v62, v237
	v_fmac_f32_e32 v247, v63, v237
	v_fmac_f32_e32 v248, v64, v237
	v_fmac_f32_e32 v249, v65, v237
	v_pk_fma_f32 v[232:233], v[58:59], v[236:237], v[232:233] op_sel:[0,1,0]
	v_fmac_f32_e32 v240, v68, v238
	v_fmac_f32_e32 v241, v69, v238
	v_fmac_f32_e32 v246, v70, v238
	v_fmac_f32_e32 v247, v71, v238
	v_fmac_f32_e32 v248, v72, v238
	v_fmac_f32_e32 v249, v73, v238
	v_pk_fma_f32 v[232:233], v[66:67], v[238:239], v[232:233] op_sel_hi:[1,0,1]
	v_cvt_pk_bf16_f32 v197, v234, v235
	v_add_co_u32_e32 v212, vcc, s33, v210
	v_fmac_f32_e32 v240, v76, v239
	v_fmac_f32_e32 v241, v77, v239
	v_fmac_f32_e32 v246, v78, v239
	v_fmac_f32_e32 v247, v79, v239
	v_fmac_f32_e32 v248, v80, v239
	v_fmac_f32_e32 v249, v81, v239
	v_pk_fma_f32 v[232:233], v[74:75], v[238:239], v[232:233] op_sel:[0,1,0]
	v_addc_co_u32_e32 v213, vcc, 0, v211, vcc
	v_fmac_f32_e32 v240, v84, v234
	v_fmac_f32_e32 v241, v85, v234
	v_fmac_f32_e32 v246, v86, v234
	v_fmac_f32_e32 v247, v87, v234
	v_fmac_f32_e32 v248, v88, v234
	v_fmac_f32_e32 v249, v89, v234
	v_pk_fma_f32 v[232:233], v[82:83], v[234:235], v[232:233] op_sel_hi:[1,0,1]
	global_store_dwordx4 v[212:213], v[194:197], off
	v_fmac_f32_e32 v240, v92, v235
	v_fmac_f32_e32 v241, v93, v235
	v_fmac_f32_e32 v246, v94, v235
	v_fmac_f32_e32 v247, v95, v235
	v_fmac_f32_e32 v248, v96, v235
	v_fmac_f32_e32 v249, v97, v235
	v_pk_fma_f32 v[232:233], v[90:91], v[234:235], v[232:233] op_sel:[0,1,0]
	v_fmac_f32_e32 v240, v108, v244
	v_fmac_f32_e32 v241, v109, v244
	v_fmac_f32_e32 v246, v98, v244
	v_fmac_f32_e32 v247, v99, v244
	v_fmac_f32_e32 v248, v100, v244
	v_fmac_f32_e32 v249, v101, v244
	v_pk_fma_f32 v[232:233], v[106:107], v[244:245], v[232:233] op_sel_hi:[1,0,1]
	v_pk_fma_f32 v[232:233], v[102:103], v[244:245], v[232:233] op_sel:[0,1,0]
	v_fmac_f32_e32 v240, v104, v245
	v_fmac_f32_e32 v241, v105, v245
	v_fmac_f32_e32 v246, v110, v245
	v_fmac_f32_e32 v247, v111, v245
	v_fmac_f32_e32 v248, v112, v245
	v_fmac_f32_e32 v249, v113, v245
	v_cvt_pk_bf16_f32 v194, v244, v245
	v_bfe_u32 v195, v216, 16, 1
	v_bfe_u32 v196, v217, 16, 1
	v_fmac_f32_e32 v240, v124, v216
	v_fmac_f32_e32 v241, v125, v216
	v_fmac_f32_e32 v246, v138, v216
	v_fmac_f32_e32 v247, v139, v216
	v_fmac_f32_e32 v248, v140, v216
	v_fmac_f32_e32 v249, v141, v216
	v_pk_fma_f32 v[232:233], v[122:123], v[216:217], v[232:233] op_sel_hi:[1,0,1]
	v_add3_u32 v195, v216, v195, s31
	v_add3_u32 v196, v217, v196, s31
	v_fmac_f32_e32 v240, v116, v217
	v_fmac_f32_e32 v241, v117, v217
	v_fmac_f32_e32 v246, v118, v217
	v_fmac_f32_e32 v247, v119, v217
	v_fmac_f32_e32 v248, v120, v217
	v_fmac_f32_e32 v249, v121, v217
	v_pk_fma_f32 v[216:217], v[114:115], v[216:217], v[232:233] op_sel:[0,1,0]
	v_lshrrev_b32_e32 v195, 16, v195
	v_pk_fma_f32 v[216:217], v[126:127], v[218:219], v[216:217] op_sel_hi:[1,0,1]
	v_and_or_b32 v195, v196, s29, v195
	v_pk_fma_f32 v[216:217], v[134:135], v[218:219], v[216:217] op_sel:[0,1,0]
	v_bfe_u32 v196, v218, 16, 1
	v_pk_fma_f32 v[216:217], v[142:143], v[214:215], v[216:217] op_sel_hi:[1,0,1]
	v_bfe_u32 v197, v219, 16, 1
	v_pk_fma_f32 v[216:217], v[154:155], v[214:215], v[216:217] op_sel:[0,1,0]
	ds_bpermute_b32 v232, v220, v216
	ds_bpermute_b32 v233, v220, v217
	v_fmac_f32_e32 v240, v128, v218
	v_fmac_f32_e32 v241, v129, v218
	v_fmac_f32_e32 v246, v130, v218
	v_fmac_f32_e32 v247, v131, v218
	v_fmac_f32_e32 v248, v132, v218
	v_fmac_f32_e32 v249, v133, v218
	s_waitcnt lgkmcnt(0)
	v_pk_add_f32 v[216:217], v[216:217], v[232:233]
	v_add3_u32 v196, v218, v196, s31
	v_add3_u32 v197, v219, v197, s31
	v_fmac_f32_e32 v240, v136, v219
	v_fmac_f32_e32 v241, v137, v219
	v_fmac_f32_e32 v246, v146, v219
	v_fmac_f32_e32 v247, v147, v219
	v_fmac_f32_e32 v248, v148, v219
	v_fmac_f32_e32 v249, v149, v219
	ds_bpermute_b32 v218, v221, v216
	ds_bpermute_b32 v219, v221, v217
	v_lshrrev_b32_e32 v196, 16, v196
	v_fmac_f32_e32 v240, v144, v214
	v_and_or_b32 v196, v197, s29, v196
	v_bfe_u32 v197, v214, 16, 1
	s_waitcnt lgkmcnt(0)
	v_pk_add_f32 v[216:217], v[216:217], v[218:219]
	v_fmac_f32_e32 v240, v156, v215
	v_add3_u32 v197, v214, v197, s31
	v_fmac_f32_e32 v241, v145, v214
	v_fmac_f32_e32 v246, v150, v214
	v_fmac_f32_e32 v247, v151, v214
	v_fmac_f32_e32 v248, v152, v214
	v_fmac_f32_e32 v249, v153, v214
	ds_bpermute_b32 v218, v222, v216
	ds_bpermute_b32 v219, v222, v217
	ds_bpermute_b32 v214, v220, v240
	v_fmac_f32_e32 v241, v157, v215
	v_fmac_f32_e32 v246, v158, v215
	ds_bpermute_b32 v233, v220, v241
	s_waitcnt lgkmcnt(2)
	v_pk_add_f32 v[216:217], v[216:217], v[218:219]
	s_waitcnt lgkmcnt(1)
	v_add_f32_e32 v214, v240, v214
	ds_bpermute_b32 v218, v223, v216
	ds_bpermute_b32 v219, v223, v217
	ds_bpermute_b32 v232, v221, v214
	ds_bpermute_b32 v234, v220, v246
	v_fmac_f32_e32 v247, v159, v215
	v_fmac_f32_e32 v248, v160, v215
	s_waitcnt lgkmcnt(2)
	v_pk_add_f32 v[216:217], v[216:217], v[218:219]
	s_waitcnt lgkmcnt(1)
	v_add_f32_e32 v214, v214, v232
	ds_bpermute_b32 v218, v224, v216
	ds_bpermute_b32 v219, v224, v217
	ds_bpermute_b32 v232, v222, v214
	v_fmac_f32_e32 v249, v161, v215
	ds_bpermute_b32 v238, v220, v247
	ds_bpermute_b32 v239, v220, v249
	s_waitcnt lgkmcnt(3)
	v_pk_add_f32 v[216:217], v[216:217], v[218:219]
	v_add_f32_e32 v218, v241, v233
	s_waitcnt lgkmcnt(2)
	v_add_f32_e32 v214, v214, v232
	v_add_f32_e32 v232, v246, v234
	ds_bpermute_b32 v219, v221, v218
	ds_bpermute_b32 v233, v221, v232
	ds_bpermute_b32 v234, v223, v214
	s_waitcnt lgkmcnt(4)
	v_add_f32_e32 v238, v247, v238
	s_waitcnt lgkmcnt(3)
	v_add_f32_e32 v239, v249, v239
	s_waitcnt lgkmcnt(2)
	v_add_f32_e32 v219, v218, v219
	s_waitcnt lgkmcnt(1)
	v_add_f32_e32 v232, v232, v233
	ds_bpermute_b32 v235, v222, v219
	ds_bpermute_b32 v233, v222, v232
	s_waitcnt lgkmcnt(2)
	v_add_f32_e32 v214, v214, v234
	ds_bpermute_b32 v236, v224, v214
	ds_bpermute_b32 v240, v221, v238
	s_waitcnt lgkmcnt(3)
	v_add_f32_e32 v234, v219, v235
	s_waitcnt lgkmcnt(2)
	v_add_f32_e32 v232, v232, v233
	ds_bpermute_b32 v235, v223, v234
	ds_bpermute_b32 v233, v223, v232
	s_waitcnt lgkmcnt(3)
	v_add_f32_e32 v214, v214, v236
	ds_bpermute_b32 v242, v221, v239
	s_waitcnt lgkmcnt(3)
	v_add_f32_e32 v238, v238, v240
	s_waitcnt lgkmcnt(2)
	v_add_f32_e32 v234, v234, v235
	s_waitcnt lgkmcnt(1)
	v_add_f32_e32 v236, v232, v233
	ds_bpermute_b32 v235, v224, v234
	ds_bpermute_b32 v237, v224, v236
	s_waitcnt lgkmcnt(2)
	v_add_f32_e32 v239, v239, v242
	ds_bpermute_b32 v240, v222, v238
	ds_bpermute_b32 v242, v222, v239
	s_waitcnt lgkmcnt(3)
	v_add_f32_e32 v233, v234, v235
	s_waitcnt lgkmcnt(2)
	v_add_f32_e32 v235, v236, v237
	ds_bpermute_b32 v237, v220, v248
	s_waitcnt lgkmcnt(2)
	v_add_f32_e32 v238, v238, v240
	s_waitcnt lgkmcnt(1)
	v_add_f32_e32 v239, v239, v242
	ds_bpermute_b32 v240, v223, v238
	ds_bpermute_b32 v242, v223, v239
	s_waitcnt lgkmcnt(2)
	v_add_f32_e32 v237, v248, v237
	ds_bpermute_b32 v241, v221, v237
	ds_bpermute_b32 v218, v225, v216
	s_waitcnt lgkmcnt(3)
	v_add_f32_e32 v238, v238, v240
	s_waitcnt lgkmcnt(2)
	v_add_f32_e32 v242, v239, v242
	ds_bpermute_b32 v240, v224, v238
	s_waitcnt lgkmcnt(2)
	v_add_f32_e32 v237, v237, v241
	ds_bpermute_b32 v241, v222, v237
	ds_bpermute_b32 v244, v224, v242
	ds_bpermute_b32 v219, v225, v217
	ds_bpermute_b32 v232, v225, v214
	ds_bpermute_b32 v234, v225, v233
	s_waitcnt lgkmcnt(4)
	v_add_f32_e32 v237, v237, v241
	ds_bpermute_b32 v241, v223, v237
	ds_bpermute_b32 v236, v225, v235
	v_lshrrev_b32_e32 v197, 16, v197
	s_waitcnt lgkmcnt(1)
	v_add_f32_e32 v241, v237, v241
	ds_bpermute_b32 v243, v224, v241
	v_add_f32_e32 v237, v238, v240
	ds_bpermute_b32 v238, v225, v237
	s_waitcnt lgkmcnt(1)
	v_add_f32_e32 v239, v241, v243
	v_add_f32_e32 v241, v242, v244
	ds_bpermute_b32 v240, v225, v239
	ds_bpermute_b32 v242, v225, v241
	v_bfe_u32 v243, v215, 16, 1
	v_add3_u32 v215, v215, v243, s31
	v_and_or_b32 v197, v215, s29, v197
	global_store_dwordx4 v[212:213], v[194:197], off offset:1024
	s_and_saveexec_b64 s[24:25], s[2:3]
	s_cbranch_execz .LBB0_1235
	v_pk_add_f32 v[196:197], v[216:217], v[218:219]
	v_add_f32_e32 v214, v214, v232
	v_cmp_gt_f32_e32 vcc, v197, v196
	v_add_f32_e32 v233, v233, v234
	v_add_f32_e32 v235, v235, v236
	v_cndmask_b32_e32 v194, v196, v197, vcc
	v_cmp_gt_f32_e64 s[0:1], v214, v194
	s_waitcnt lgkmcnt(2)
	v_add_f32_e32 v237, v237, v238
	s_waitcnt lgkmcnt(1)
	v_add_f32_e32 v215, v239, v240
	v_cndmask_b32_e64 v194, v194, v214, s[0:1]
	v_cmp_gt_f32_e64 s[4:5], v233, v194
	s_waitcnt lgkmcnt(0)
	v_add_f32_e32 v195, v241, v242
	v_cmp_nlg_f32_e64 s[14:15], s34, v196
	v_cndmask_b32_e64 v194, v194, v233, s[4:5]
	v_cmp_gt_f32_e64 s[6:7], v235, v194
	s_nop 1
	v_cndmask_b32_e64 v194, v194, v235, s[6:7]
	v_cmp_gt_f32_e64 s[8:9], v237, v194
	s_nop 1
	v_cndmask_b32_e64 v194, v194, v237, s[8:9]
	v_cmp_gt_f32_e64 s[10:11], v215, v194
	s_nop 1
	v_cndmask_b32_e64 v216, v194, v215, s[10:11]
	v_cndmask_b32_e64 v194, 0, 1, vcc
	v_cndmask_b32_e64 v194, v194, 2, s[0:1]
	v_cndmask_b32_e64 v194, v194, 3, s[4:5]
	v_cndmask_b32_e64 v194, v194, 4, s[6:7]
	v_cndmask_b32_e64 v194, v194, 5, s[8:9]
	v_cndmask_b32_e64 v194, v194, 6, s[10:11]
	v_cmp_ngt_f32_e32 vcc, v195, v216
	s_and_b64 s[16:17], s[10:11], vcc
	s_nop 0
	v_cndmask_b32_e32 v194, 7, v194, vcc
	v_cmp_eq_u32_e64 s[12:13], 0, v194
	s_or_b64 s[12:13], s[12:13], s[14:15]
	v_cmp_ne_u32_e64 s[10:11], 1, v194
	v_cndmask_b32_e64 v196, v196, v231, s[12:13]
	v_cmp_gt_f32_e64 s[14:15], v197, v196
	s_and_b64 s[10:11], s[10:11], s[14:15]
	v_cndmask_b32_e64 v196, v196, v197, s[10:11]
	v_cmp_ne_u32_e64 s[8:9], 2, v194
	v_cmp_gt_f32_e64 s[14:15], v214, v196
	s_and_b64 s[8:9], s[8:9], s[14:15]
	v_cndmask_b32_e64 v196, v196, v214, s[8:9]
	v_cmp_ne_u32_e64 s[6:7], 3, v194
	v_cmp_gt_f32_e64 s[14:15], v233, v196
	s_and_b64 s[6:7], s[6:7], s[14:15]
	v_cndmask_b32_e64 v196, v196, v233, s[6:7]
	v_cmp_ne_u32_e64 s[4:5], 4, v194
	v_cmp_gt_f32_e64 s[14:15], v235, v196
	s_and_b64 s[4:5], s[4:5], s[14:15]
	v_cndmask_b32_e64 v196, v196, v235, s[4:5]
	v_cmp_ne_u32_e64 s[0:1], 5, v194
	v_cmp_gt_f32_e64 s[14:15], v237, v196
	s_and_b64 s[0:1], s[0:1], s[14:15]
	v_cndmask_b32_e64 v196, v196, v237, s[0:1]
	v_cmp_ngt_f32_e64 s[14:15], v215, v196
	s_or_b64 s[14:15], s[16:17], s[14:15]
	v_cndmask_b32_e64 v197, 0, -1, s[12:13]
	v_cndmask_b32_e64 v196, v215, v196, s[14:15]
	v_cmp_gt_f32_e64 s[16:17], v195, v196
	s_and_b64 s[16:17], vcc, s[16:17]
	v_cndmask_b32_e64 v197, v197, 1, s[10:11]
	v_cndmask_b32_e64 v196, v196, v195, s[16:17]
	v_cndmask_b32_e32 v195, v195, v216, vcc
	v_sub_f32_e32 v195, v196, v195
	v_mul_f32_e32 v195, 0x3fb8aa3b, v195
	v_exp_f32_e32 v215, v195
	v_cndmask_b32_e64 v195, v197, 2, s[8:9]
	v_cndmask_b32_e64 v195, v195, 3, s[6:7]
	v_cndmask_b32_e64 v195, v195, 4, s[4:5]
	v_add_f32_e32 v214, 1.0, v215
	v_div_scale_f32 v196, s[4:5], v214, v214, 1.0
	v_rcp_f32_e32 v216, v196
	v_cndmask_b32_e64 v195, v195, 5, s[0:1]
	v_cndmask_b32_e64 v195, 6, v195, s[14:15]
	v_cndmask_b32_e64 v195, v195, 7, s[16:17]
	v_fma_f32 v197, -v196, v216, 1.0
	v_fmac_f32_e32 v216, v197, v216
	v_div_scale_f32 v197, vcc, 1.0, v214, 1.0
	v_mul_f32_e32 v217, v197, v216
	v_fma_f32 v218, -v196, v217, v197
	v_fmac_f32_e32 v217, v218, v216
	v_fma_f32 v218, -v196, v217, v197
	v_lshl_add_u32 v196, v194, 2, 0
	ds_add_rtn_u32 v196, v196, v230
	v_lshl_add_u32 v197, v195, 2, 0
	ds_add_rtn_u32 v197, v197, v230
	v_div_fmas_f32 v216, v218, v216, v217
	v_div_fixup_f32 v214, v216, v214, 1.0
	v_mul_f32_e32 v215, v215, v214
	s_waitcnt lgkmcnt(0)
	ds_write_b128 v226, v[194:197]
	v_lshl_add_u64 v[194:195], s[94:95], 0, v[206:207]
	v_add_co_u32_e32 v194, vcc, 0x280000, v194
	s_nop 1
	v_addc_co_u32_e32 v195, vcc, 0, v195, vcc
	global_store_dwordx2 v[194:195], v[214:215], off

.LBB0_1237:
	s_waitcnt vmcnt(7)
	v_lshlrev_b32_e32 v217, 16, v171
	v_lshlrev_b32_e32 v216, 16, v170
	v_and_b32_e32 v237, 0xffff0000, v171
	v_and_b32_e32 v236, 0xffff0000, v170
	s_waitcnt lgkmcnt(2)
	v_pk_add_f32 v[238:239], v[216:217], v[236:237]
	v_and_b32_e32 v241, 0xffff0000, v173
	v_add_f32_e32 v215, v238, v239
	v_lshlrev_b32_e32 v239, 16, v173
	v_lshlrev_b32_e32 v238, 16, v172
	s_waitcnt lgkmcnt(1)
	v_and_b32_e32 v240, 0xffff0000, v172
	s_waitcnt lgkmcnt(0)
	v_pk_add_f32 v[242:243], v[238:239], v[240:241]
	s_waitcnt vmcnt(6)
	v_lshlrev_b32_e32 v194, 16, v174
	v_and_b32_e32 v195, 0xffff0000, v174
	v_lshlrev_b32_e32 v196, 16, v175
	v_and_b32_e32 v197, 0xffff0000, v175
	v_pk_add_f32 v[242:243], v[242:243], v[242:243] op_sel_hi:[0,1]
	v_lshlrev_b32_e32 v214, 16, v176
	v_and_b32_e32 v218, 0xffff0000, v176
	v_lshlrev_b32_e32 v232, 16, v177
	v_and_b32_e32 v234, 0xffff0000, v177
	v_add_f32_e32 v235, 0, v215
	v_add_f32_e32 v215, v194, v195
	v_add_f32_e32 v219, v196, v197
	v_mov_b32_e32 v233, v243
	v_pk_add_f32 v[244:245], v[214:215], v[218:219]
	v_pk_add_f32 v[242:243], v[232:233], v[234:235]
	s_nop 0
	v_pk_add_f32 v[242:243], v[244:245], v[242:243]
	s_nop 0
	v_add_f32_e32 v215, v242, v243
	s_waitcnt lgkmcnt(0)
	s_nop 1
	v_add_f32_dpp v215, v215, v215 quad_perm:[1,0,3,2] row_mask:0xf bank_mask:0xf
	s_nop 1
	v_add_f32_dpp v215, v215, v215 quad_perm:[2,3,0,1] row_mask:0xf bank_mask:0xf
	s_nop 1
	v_add_f32_dpp v215, v215, v215 row_half_mirror row_mask:0xf bank_mask:0xf
	s_nop 1
	v_add_f32_dpp v215, v215, v215 row_mirror row_mask:0xf bank_mask:0xf
	v_mov_b32_e32 v219, v215
	s_nop 1
	v_permlane16_swap_b32_e32 v215, v219
	v_add_f32_e32 v215, v215, v219
	v_mov_b32_e32 v219, v215
	s_nop 1
	v_permlane32_swap_b32_e32 v215, v219
	v_add_f32_e32 v215, v215, v219
	v_fmac_f32_e32 v236, 0xba800000, v215
	v_fmac_f32_e32 v237, 0xba800000, v215
	v_fmac_f32_e32 v217, 0xba800000, v215
	v_fmac_f32_e32 v216, 0xba800000, v215
	v_mov_b32_e32 v242, v217
	v_mov_b32_e32 v243, v237
	v_mov_b32_e32 v217, v236
	v_pk_mul_f32 v[244:245], v[242:243], v[242:243]
	v_pk_mul_f32 v[236:237], v[216:217], v[216:217]
	v_fmac_f32_e32 v240, 0xba800000, v215
	v_pk_mov_b32 v[246:247], v[236:237], v[244:245] op_sel:[1,0]
	v_mov_b32_e32 v237, v245
	v_fmac_f32_e32 v241, 0xba800000, v215
	v_fmac_f32_e32 v239, 0xba800000, v215
	v_pk_add_f32 v[236:237], v[246:247], v[236:237]
	v_fmac_f32_e32 v238, 0xba800000, v215
	v_mov_b32_e32 v244, v239
	v_mov_b32_e32 v245, v241
	v_mov_b32_e32 v239, v240
	v_pk_add_f32 v[236:237], v[236:237], v[236:237] op_sel_hi:[0,1]
	v_pk_mul_f32 v[246:247], v[244:245], v[244:245]
	v_pk_mul_f32 v[240:241], v[238:239], v[238:239]
	v_fmac_f32_e32 v194, 0xba800000, v215
	v_pk_mov_b32 v[248:249], v[240:241], v[246:247] op_sel:[1,0]
	v_mov_b32_e32 v241, v247
	v_fmac_f32_e32 v195, 0xba800000, v215
	v_fmac_f32_e32 v196, 0xba800000, v215
	v_mul_f32_e32 v236, v194, v194
	v_pk_add_f32 v[240:241], v[248:249], v[240:241]
	v_fmac_f32_e32 v197, 0xba800000, v215
	v_pk_fma_f32 v[246:247], v[194:195], v[194:195], v[236:237] op_sel_hi:[1,1,0]
	v_mul_f32_e32 v236, v196, v196
	v_pk_add_f32 v[240:241], v[240:241], v[240:241] op_sel_hi:[0,1]
	v_pk_fma_f32 v[248:249], v[196:197], v[196:197], v[236:237] op_sel_hi:[1,1,0]
	v_fmac_f32_e32 v234, 0xba800000, v215
	v_fmac_f32_e32 v232, 0xba800000, v215
	v_fmac_f32_e32 v218, 0xba800000, v215
	v_fmac_f32_e32 v214, 0xba800000, v215
	v_mul_f32_e32 v246, v214, v214
	v_mul_f32_e32 v248, v218, v218
	v_mul_f32_e32 v236, v232, v232
	v_mul_f32_e32 v240, v234, v234
	v_pk_add_f32 v[246:247], v[246:247], v[248:249]
	v_pk_add_f32 v[236:237], v[236:237], v[240:241]
	s_nop 0
	v_pk_add_f32 v[236:237], v[246:247], v[236:237]
	s_nop 0
	v_add_f32_e32 v215, v236, v237
	s_waitcnt lgkmcnt(0)
	s_nop 1
	v_add_f32_dpp v215, v215, v215 quad_perm:[1,0,3,2] row_mask:0xf bank_mask:0xf
	s_nop 1
	v_add_f32_dpp v215, v215, v215 quad_perm:[2,3,0,1] row_mask:0xf bank_mask:0xf
	s_nop 1
	v_add_f32_dpp v215, v215, v215 row_half_mirror row_mask:0xf bank_mask:0xf
	s_nop 1
	v_add_f32_dpp v215, v215, v215 row_mirror row_mask:0xf bank_mask:0xf
	v_mov_b32_e32 v219, v215
	s_nop 1
	v_permlane16_swap_b32_e32 v215, v219
	v_add_f32_e32 v215, v215, v219
	v_mov_b32_e32 v219, v215
	s_nop 1
	v_permlane32_swap_b32_e32 v215, v219
	v_add_f32_e32 v215, v215, v219
	v_fmamk_f32 v215, v215, 0x3a800000, v228
	v_mul_f32_e32 v219, 0x4f800000, v215
	v_cmp_gt_f32_e32 vcc, s30, v215
	s_nop 1
	v_cndmask_b32_e32 v215, v215, v219, vcc
	v_sqrt_f32_e32 v219, v215
	s_nop 0
	v_add_u32_e32 v233, -1, v219
	v_fma_f32 v235, -v233, v219, v215
	v_cmp_ge_f32_e64 s[0:1], 0, v235
	v_add_u32_e32 v235, 1, v219
	s_nop 0
	v_cndmask_b32_e64 v233, v219, v233, s[0:1]
	v_fma_f32 v219, -v235, v219, v215
	v_cmp_lt_f32_e64 s[0:1], 0, v219
	s_nop 1
	v_cndmask_b32_e64 v219, v233, v235, s[0:1]
	v_mul_f32_e32 v233, 0x37800000, v219
	v_cndmask_b32_e32 v219, v219, v233, vcc
	v_cmp_class_f32_e32 vcc, v215, v229
	s_nop 1
	v_cndmask_b32_e32 v215, v219, v215, vcc
	v_div_scale_f32 v219, s[0:1], v215, v215, 1.0
	v_rcp_f32_e32 v233, v219
	s_nop 0
	v_fma_f32 v235, -v219, v233, 1.0
	v_fmac_f32_e32 v233, v235, v233
	v_div_scale_f32 v235, vcc, 1.0, v215, 1.0
	v_mul_f32_e32 v236, v235, v233
	v_fma_f32 v237, -v219, v236, v235
	v_fmac_f32_e32 v236, v237, v233
	v_fma_f32 v219, -v219, v236, v235
	v_div_fmas_f32 v219, v219, v233, v236
	v_div_fixup_f32 v236, v219, v215, 1.0
	v_pk_mul_f32 v[216:217], v[216:217], v[236:237] op_sel_hi:[1,0]
	v_pk_mul_f32 v[194:195], v[194:195], v[236:237] op_sel_hi:[1,0]
	v_mov_b32_e32 v215, v218
	v_pk_mul_f32 v[240:241], v[242:243], v[236:237] op_sel_hi:[1,0]
	v_pk_fma_f32 v[242:243], v[2:3], v[216:217], v[6:7]
	v_pk_fma_f32 v[246:247], v[18:19], v[194:195], v[30:31]
	v_pk_mul_f32 v[194:195], v[214:215], v[236:237] op_sel_hi:[1,0]
	v_pk_fma_f32 v[240:241], v[4:5], v[240:241], v[8:9]
	v_pk_fma_f32 v[218:219], v[10:11], v[194:195], v[22:23]
	v_pk_mul_f32 v[216:217], v[238:239], v[236:237] op_sel_hi:[1,0]
	v_pk_mul_f32 v[196:197], v[196:197], v[236:237] op_sel_hi:[1,0]
	v_mov_b32_e32 v233, v234
	v_pk_mul_f32 v[238:239], v[244:245], v[236:237] op_sel_hi:[1,0]
	v_pk_fma_f32 v[244:245], v[14:15], v[216:217], v[26:27]
	v_pk_fma_f32 v[216:217], v[20:21], v[196:197], v[32:33]
	v_pk_mul_f32 v[196:197], v[232:233], v[236:237] op_sel_hi:[1,0]
	v_cvt_pk_bf16_f32 v194, v242, v243
	v_pk_fma_f32 v[214:215], v[12:13], v[196:197], v[24:25]
	v_cvt_pk_bf16_f32 v195, v240, v241
	v_pk_fma_f32 v[238:239], v[16:17], v[238:239], v[28:29]
	v_cvt_pk_bf16_f32 v196, v244, v245
	v_cvt_pk_bf16_f32 v197, v238, v239
	v_fma_f32 v234, v36, v242, 0
	v_fma_f32 v235, v37, v242, 0
	v_fma_f32 v236, v38, v242, 0
	v_fma_f32 v237, v39, v242, 0
	v_fma_f32 v248, v40, v242, 0
	v_fma_f32 v249, v41, v242, 0
	v_pk_fma_f32 v[232:233], v[34:35], v[242:243], 0 op_sel_hi:[1,0,0]
	v_fmac_f32_e32 v234, v44, v243
	v_fmac_f32_e32 v235, v45, v243
	v_fmac_f32_e32 v236, v46, v243
	v_fmac_f32_e32 v237, v47, v243
	v_fmac_f32_e32 v248, v48, v243
	v_fmac_f32_e32 v249, v49, v243
	v_pk_fma_f32 v[232:233], v[42:43], v[242:243], v[232:233] op_sel:[0,1,0]
	v_fmac_f32_e32 v234, v52, v240
	v_fmac_f32_e32 v235, v53, v240
	v_fmac_f32_e32 v236, v54, v240
	v_fmac_f32_e32 v237, v55, v240
	v_fmac_f32_e32 v248, v56, v240
	v_fmac_f32_e32 v249, v57, v240
	v_pk_fma_f32 v[232:233], v[50:51], v[240:241], v[232:233] op_sel_hi:[1,0,1]
	v_fmac_f32_e32 v234, v60, v241
	v_fmac_f32_e32 v235, v61, v241
	v_fmac_f32_e32 v236, v62, v241
	v_fmac_f32_e32 v237, v63, v241
	v_fmac_f32_e32 v248, v64, v241
	v_fmac_f32_e32 v249, v65, v241
	v_pk_fma_f32 v[232:233], v[58:59], v[240:241], v[232:233] op_sel:[0,1,0]
	v_fmac_f32_e32 v234, v68, v244
	v_fmac_f32_e32 v235, v69, v244
	v_fmac_f32_e32 v236, v70, v244
	v_fmac_f32_e32 v237, v71, v244
	v_fmac_f32_e32 v248, v72, v244
	v_fmac_f32_e32 v249, v73, v244
	v_pk_fma_f32 v[232:233], v[66:67], v[244:245], v[232:233] op_sel_hi:[1,0,1]
	v_fmac_f32_e32 v234, v76, v245
	v_fmac_f32_e32 v235, v77, v245
	v_fmac_f32_e32 v236, v78, v245
	v_fmac_f32_e32 v237, v79, v245
	v_fmac_f32_e32 v248, v80, v245
	v_fmac_f32_e32 v249, v81, v245
	v_pk_fma_f32 v[232:233], v[74:75], v[244:245], v[232:233] op_sel:[0,1,0]
	v_fmac_f32_e32 v234, v84, v238
	v_fmac_f32_e32 v235, v85, v238
	v_fmac_f32_e32 v236, v86, v238
	v_fmac_f32_e32 v237, v87, v238
	v_fmac_f32_e32 v248, v88, v238
	v_fmac_f32_e32 v249, v89, v238
	v_pk_fma_f32 v[232:233], v[82:83], v[238:239], v[232:233] op_sel_hi:[1,0,1]
	global_store_dwordx4 v[212:213], v[194:197], off offset:2048
	v_fmac_f32_e32 v234, v92, v239
	v_fmac_f32_e32 v235, v93, v239
	v_fmac_f32_e32 v236, v94, v239
	v_fmac_f32_e32 v237, v95, v239
	v_fmac_f32_e32 v248, v96, v239
	v_fmac_f32_e32 v249, v97, v239
	v_pk_fma_f32 v[232:233], v[90:91], v[238:239], v[232:233] op_sel:[0,1,0]
	v_fmac_f32_e32 v234, v108, v246
	v_fmac_f32_e32 v235, v109, v246
	v_fmac_f32_e32 v236, v98, v246
	v_fmac_f32_e32 v237, v99, v246
	v_fmac_f32_e32 v248, v100, v246
	v_fmac_f32_e32 v249, v101, v246
	v_pk_fma_f32 v[232:233], v[106:107], v[246:247], v[232:233] op_sel_hi:[1,0,1]
	v_pk_fma_f32 v[232:233], v[102:103], v[246:247], v[232:233] op_sel:[0,1,0]
	v_fmac_f32_e32 v234, v104, v247
	v_fmac_f32_e32 v235, v105, v247
	v_fmac_f32_e32 v236, v110, v247
	v_fmac_f32_e32 v237, v111, v247
	v_fmac_f32_e32 v248, v112, v247
	v_fmac_f32_e32 v249, v113, v247
	v_cvt_pk_bf16_f32 v194, v246, v247
	v_bfe_u32 v195, v216, 16, 1
	v_bfe_u32 v196, v217, 16, 1
	v_fmac_f32_e32 v234, v124, v216
	v_fmac_f32_e32 v235, v125, v216
	v_fmac_f32_e32 v236, v138, v216
	v_fmac_f32_e32 v237, v139, v216
	v_fmac_f32_e32 v248, v140, v216
	v_fmac_f32_e32 v249, v141, v216
	v_pk_fma_f32 v[232:233], v[122:123], v[216:217], v[232:233] op_sel_hi:[1,0,1]
	v_add3_u32 v195, v216, v195, s31
	v_add3_u32 v196, v217, v196, s31
	v_fmac_f32_e32 v234, v116, v217
	v_fmac_f32_e32 v235, v117, v217
	v_fmac_f32_e32 v236, v118, v217
	v_fmac_f32_e32 v237, v119, v217
	v_fmac_f32_e32 v248, v120, v217
	v_fmac_f32_e32 v249, v121, v217
	v_pk_fma_f32 v[216:217], v[114:115], v[216:217], v[232:233] op_sel:[0,1,0]
	v_lshrrev_b32_e32 v195, 16, v195
	v_pk_fma_f32 v[216:217], v[126:127], v[218:219], v[216:217] op_sel_hi:[1,0,1]
	v_and_or_b32 v195, v196, s29, v195
	v_pk_fma_f32 v[216:217], v[134:135], v[218:219], v[216:217] op_sel:[0,1,0]
	v_bfe_u32 v196, v218, 16, 1
	v_pk_fma_f32 v[216:217], v[142:143], v[214:215], v[216:217] op_sel_hi:[1,0,1]
	v_bfe_u32 v197, v219, 16, 1
	v_pk_fma_f32 v[216:217], v[154:155], v[214:215], v[216:217] op_sel:[0,1,0]
	ds_bpermute_b32 v232, v220, v216
	ds_bpermute_b32 v233, v220, v217
	v_fmac_f32_e32 v234, v128, v218
	v_fmac_f32_e32 v235, v129, v218
	v_fmac_f32_e32 v236, v130, v218
	v_fmac_f32_e32 v237, v131, v218
	v_fmac_f32_e32 v248, v132, v218
	v_fmac_f32_e32 v249, v133, v218
	s_waitcnt lgkmcnt(0)
	v_pk_add_f32 v[216:217], v[216:217], v[232:233]
	v_add3_u32 v196, v218, v196, s31
	v_add3_u32 v197, v219, v197, s31
	v_fmac_f32_e32 v234, v136, v219
	v_fmac_f32_e32 v235, v137, v219
	v_fmac_f32_e32 v236, v146, v219
	v_fmac_f32_e32 v237, v147, v219
	v_fmac_f32_e32 v248, v148, v219
	v_fmac_f32_e32 v249, v149, v219
	ds_bpermute_b32 v218, v221, v216
	ds_bpermute_b32 v219, v221, v217
	v_lshrrev_b32_e32 v196, 16, v196
	v_fmac_f32_e32 v234, v144, v214
	v_and_or_b32 v196, v197, s29, v196
	v_bfe_u32 v197, v214, 16, 1
	s_waitcnt lgkmcnt(0)
	v_pk_add_f32 v[216:217], v[216:217], v[218:219]
	v_fmac_f32_e32 v234, v156, v215
	v_add3_u32 v197, v214, v197, s31
	v_fmac_f32_e32 v235, v145, v214
	v_fmac_f32_e32 v236, v150, v214
	v_fmac_f32_e32 v237, v151, v214
	v_fmac_f32_e32 v248, v152, v214
	v_fmac_f32_e32 v249, v153, v214
	ds_bpermute_b32 v218, v222, v216
	ds_bpermute_b32 v219, v222, v217
	ds_bpermute_b32 v214, v220, v234
	v_fmac_f32_e32 v235, v157, v215
	v_fmac_f32_e32 v236, v158, v215
	ds_bpermute_b32 v233, v220, v235
	s_waitcnt lgkmcnt(2)
	v_pk_add_f32 v[216:217], v[216:217], v[218:219]
	s_waitcnt lgkmcnt(1)
	v_add_f32_e32 v214, v234, v214
	ds_bpermute_b32 v218, v223, v216
	ds_bpermute_b32 v219, v223, v217
	ds_bpermute_b32 v232, v221, v214
	ds_bpermute_b32 v234, v220, v236
	v_fmac_f32_e32 v237, v159, v215
	v_fmac_f32_e32 v248, v160, v215
	s_waitcnt lgkmcnt(2)
	v_pk_add_f32 v[216:217], v[216:217], v[218:219]
	s_waitcnt lgkmcnt(1)
	v_add_f32_e32 v214, v214, v232
	ds_bpermute_b32 v218, v224, v216
	ds_bpermute_b32 v219, v224, v217
	ds_bpermute_b32 v232, v222, v214
	v_fmac_f32_e32 v249, v161, v215
	ds_bpermute_b32 v239, v220, v237
	ds_bpermute_b32 v240, v220, v249
	s_waitcnt lgkmcnt(3)
	v_pk_add_f32 v[216:217], v[216:217], v[218:219]
	v_add_f32_e32 v218, v235, v233
	s_waitcnt lgkmcnt(2)
	v_add_f32_e32 v214, v214, v232
	v_add_f32_e32 v232, v236, v234
	ds_bpermute_b32 v219, v221, v218
	ds_bpermute_b32 v233, v221, v232
	ds_bpermute_b32 v234, v223, v214
	s_waitcnt lgkmcnt(4)
	v_add_f32_e32 v237, v237, v239
	s_waitcnt lgkmcnt(3)
	v_add_f32_e32 v240, v249, v240
	s_waitcnt lgkmcnt(2)
	v_add_f32_e32 v219, v218, v219
	s_waitcnt lgkmcnt(1)
	v_add_f32_e32 v232, v232, v233
	ds_bpermute_b32 v235, v222, v219
	ds_bpermute_b32 v233, v222, v232
	s_waitcnt lgkmcnt(2)
	v_add_f32_e32 v214, v214, v234
	ds_bpermute_b32 v236, v224, v214
	ds_bpermute_b32 v239, v221, v237
	s_waitcnt lgkmcnt(3)
	v_add_f32_e32 v234, v219, v235
	s_waitcnt lgkmcnt(2)
	v_add_f32_e32 v232, v232, v233
	ds_bpermute_b32 v235, v223, v234
	ds_bpermute_b32 v233, v223, v232
	s_waitcnt lgkmcnt(3)
	v_add_f32_e32 v214, v214, v236
	ds_bpermute_b32 v242, v221, v240
	s_waitcnt lgkmcnt(3)
	v_add_f32_e32 v237, v237, v239
	s_waitcnt lgkmcnt(2)
	v_add_f32_e32 v234, v234, v235
	s_waitcnt lgkmcnt(1)
	v_add_f32_e32 v236, v232, v233
	ds_bpermute_b32 v235, v224, v234
	ds_bpermute_b32 v238, v224, v236
	s_waitcnt lgkmcnt(2)
	v_add_f32_e32 v240, v240, v242
	ds_bpermute_b32 v239, v222, v237
	ds_bpermute_b32 v242, v222, v240
	s_waitcnt lgkmcnt(3)
	v_add_f32_e32 v233, v234, v235
	s_waitcnt lgkmcnt(2)
	v_add_f32_e32 v235, v236, v238
	ds_bpermute_b32 v238, v220, v248
	s_waitcnt lgkmcnt(2)
	v_add_f32_e32 v237, v237, v239
	s_waitcnt lgkmcnt(1)
	v_add_f32_e32 v240, v240, v242
	ds_bpermute_b32 v239, v223, v237
	ds_bpermute_b32 v242, v223, v240
	s_waitcnt lgkmcnt(2)
	v_add_f32_e32 v238, v248, v238
	ds_bpermute_b32 v241, v221, v238
	ds_bpermute_b32 v218, v225, v216
	s_waitcnt lgkmcnt(3)
	v_add_f32_e32 v237, v237, v239
	s_waitcnt lgkmcnt(2)
	v_add_f32_e32 v242, v240, v242
	ds_bpermute_b32 v239, v224, v237
	s_waitcnt lgkmcnt(2)
	v_add_f32_e32 v238, v238, v241
	ds_bpermute_b32 v241, v222, v238
	ds_bpermute_b32 v244, v224, v242
	ds_bpermute_b32 v219, v225, v217
	s_waitcnt lgkmcnt(3)
	v_add_f32_e32 v237, v237, v239
	ds_bpermute_b32 v232, v225, v214
	s_waitcnt lgkmcnt(3)
	v_add_f32_e32 v238, v238, v241
	ds_bpermute_b32 v241, v223, v238
	ds_bpermute_b32 v234, v225, v233
	ds_bpermute_b32 v236, v225, v235
	v_lshrrev_b32_e32 v197, 16, v197
	s_waitcnt lgkmcnt(2)
	v_add_f32_e32 v241, v238, v241
	ds_bpermute_b32 v243, v224, v241
	ds_bpermute_b32 v238, v225, v237
	s_waitcnt lgkmcnt(1)
	v_add_f32_e32 v239, v241, v243
	v_add_f32_e32 v241, v242, v244
	ds_bpermute_b32 v240, v225, v239
	ds_bpermute_b32 v242, v225, v241
	v_bfe_u32 v243, v215, 16, 1
	v_add3_u32 v215, v215, v243, s31
	v_and_or_b32 v197, v215, s29, v197
	global_store_dwordx4 v[212:213], v[194:197], off offset:3072
	s_and_saveexec_b64 s[24:25], s[2:3]
	s_cbranch_execz .LBB0_1239
	v_pk_add_f32 v[196:197], v[216:217], v[218:219]
	v_add_f32_e32 v214, v214, v232
	v_cmp_gt_f32_e32 vcc, v197, v196
	v_add_f32_e32 v233, v233, v234
	v_add_f32_e32 v215, v235, v236
	v_cndmask_b32_e32 v194, v196, v197, vcc
	v_cmp_gt_f32_e64 s[0:1], v214, v194
	s_waitcnt lgkmcnt(2)
	v_add_f32_e32 v213, v237, v238
	s_waitcnt lgkmcnt(1)
	v_add_f32_e32 v212, v239, v240
	v_cndmask_b32_e64 v194, v194, v214, s[0:1]
	v_cmp_gt_f32_e64 s[4:5], v233, v194
	s_waitcnt lgkmcnt(0)
	v_add_f32_e32 v195, v241, v242
	v_cmp_nlg_f32_e64 s[14:15], s34, v196
	v_cndmask_b32_e64 v194, v194, v233, s[4:5]
	v_cmp_gt_f32_e64 s[6:7], v215, v194
	s_nop 1
	v_cndmask_b32_e64 v194, v194, v215, s[6:7]
	v_cmp_gt_f32_e64 s[8:9], v213, v194
	s_nop 1
	v_cndmask_b32_e64 v194, v194, v213, s[8:9]
	v_cmp_gt_f32_e64 s[10:11], v212, v194
	s_nop 1
	v_cndmask_b32_e64 v216, v194, v212, s[10:11]
	v_cndmask_b32_e64 v194, 0, 1, vcc
	v_cndmask_b32_e64 v194, v194, 2, s[0:1]
	v_cndmask_b32_e64 v194, v194, 3, s[4:5]
	v_cndmask_b32_e64 v194, v194, 4, s[6:7]
	v_cndmask_b32_e64 v194, v194, 5, s[8:9]
	v_cndmask_b32_e64 v194, v194, 6, s[10:11]
	v_cmp_ngt_f32_e32 vcc, v195, v216
	s_and_b64 s[16:17], s[10:11], vcc
	s_nop 0
	v_cndmask_b32_e32 v194, 7, v194, vcc
	v_cmp_eq_u32_e64 s[12:13], 0, v194
	s_or_b64 s[12:13], s[12:13], s[14:15]
	v_cmp_ne_u32_e64 s[10:11], 1, v194
	v_cndmask_b32_e64 v196, v196, v231, s[12:13]
	v_cmp_gt_f32_e64 s[14:15], v197, v196
	s_and_b64 s[10:11], s[10:11], s[14:15]
	v_cndmask_b32_e64 v196, v196, v197, s[10:11]
	v_cmp_ne_u32_e64 s[8:9], 2, v194
	v_cmp_gt_f32_e64 s[14:15], v214, v196
	s_and_b64 s[8:9], s[8:9], s[14:15]
	v_cndmask_b32_e64 v196, v196, v214, s[8:9]
	v_cmp_ne_u32_e64 s[6:7], 3, v194
	v_cmp_gt_f32_e64 s[14:15], v233, v196
	s_and_b64 s[6:7], s[6:7], s[14:15]
	v_cndmask_b32_e64 v196, v196, v233, s[6:7]
	v_cmp_ne_u32_e64 s[4:5], 4, v194
	v_cmp_gt_f32_e64 s[14:15], v215, v196
	s_and_b64 s[4:5], s[4:5], s[14:15]
	v_cndmask_b32_e64 v196, v196, v215, s[4:5]
	v_cmp_ne_u32_e64 s[0:1], 5, v194
	v_cmp_gt_f32_e64 s[14:15], v213, v196
	s_and_b64 s[0:1], s[0:1], s[14:15]
	v_cndmask_b32_e64 v196, v196, v213, s[0:1]
	v_cmp_ngt_f32_e64 s[14:15], v212, v196
	s_or_b64 s[14:15], s[16:17], s[14:15]
	v_cndmask_b32_e64 v197, 0, -1, s[12:13]
	v_cndmask_b32_e64 v196, v212, v196, s[14:15]
	v_cmp_gt_f32_e64 s[16:17], v195, v196
	s_and_b64 s[16:17], vcc, s[16:17]
	v_cndmask_b32_e64 v197, v197, 1, s[10:11]
	v_cndmask_b32_e64 v196, v196, v195, s[16:17]
	v_cndmask_b32_e32 v195, v195, v216, vcc
	v_sub_f32_e32 v195, v196, v195
	v_mul_f32_e32 v195, 0x3fb8aa3b, v195
	v_exp_f32_e32 v213, v195
	v_cndmask_b32_e64 v195, v197, 2, s[8:9]
	v_cndmask_b32_e64 v195, v195, 3, s[6:7]
	v_cndmask_b32_e64 v195, v195, 4, s[4:5]
	v_add_f32_e32 v212, 1.0, v213
	v_div_scale_f32 v196, s[4:5], v212, v212, 1.0
	v_rcp_f32_e32 v214, v196
	v_cndmask_b32_e64 v195, v195, 5, s[0:1]
	v_cndmask_b32_e64 v195, 6, v195, s[14:15]
	v_cndmask_b32_e64 v195, v195, 7, s[16:17]
	v_fma_f32 v197, -v196, v214, 1.0
	v_fmac_f32_e32 v214, v197, v214
	v_div_scale_f32 v197, vcc, 1.0, v212, 1.0
	v_mul_f32_e32 v215, v197, v214
	v_fma_f32 v216, -v196, v215, v197
	v_fmac_f32_e32 v215, v216, v214
	v_fma_f32 v216, -v196, v215, v197
	v_lshl_add_u32 v196, v194, 2, 0
	ds_add_rtn_u32 v196, v196, v230
	v_lshl_add_u32 v197, v195, 2, 0
	ds_add_rtn_u32 v197, v197, v230
	v_div_fmas_f32 v214, v216, v214, v215
	v_div_fixup_f32 v212, v214, v212, 1.0
	v_mul_f32_e32 v213, v213, v212
	s_waitcnt lgkmcnt(0)
	ds_write_b128 v226, v[194:197] offset:16
	v_add_u32_e32 v194, 2, v227
	v_ashrrev_i32_e32 v195, 31, v194
	v_lshl_add_u64 v[194:195], v[194:195], 2, s[36:37]
	global_store_dwordx2 v[194:195], v[212:213], off

.LBB0_1241:
	s_waitcnt vmcnt(7)
	v_lshlrev_b32_e32 v217, 16, v179
	v_lshlrev_b32_e32 v216, 16, v178
	v_and_b32_e32 v235, 0xffff0000, v179
	v_and_b32_e32 v234, 0xffff0000, v178
	v_pk_add_f32 v[236:237], v[216:217], v[234:235]
	v_and_b32_e32 v239, 0xffff0000, v181
	v_add_f32_e32 v213, v236, v237
	v_lshlrev_b32_e32 v237, 16, v181
	v_lshlrev_b32_e32 v236, 16, v180
	s_waitcnt lgkmcnt(2)
	v_and_b32_e32 v238, 0xffff0000, v180
	s_waitcnt lgkmcnt(1)
	v_pk_add_f32 v[240:241], v[236:237], v[238:239]
	s_waitcnt vmcnt(6)
	v_lshlrev_b32_e32 v194, 16, v182
	v_and_b32_e32 v195, 0xffff0000, v182
	v_lshlrev_b32_e32 v196, 16, v183
	v_and_b32_e32 v197, 0xffff0000, v183
	v_pk_add_f32 v[240:241], v[240:241], v[240:241] op_sel_hi:[0,1]
	v_lshlrev_b32_e32 v212, 16, v184
	v_and_b32_e32 v214, 0xffff0000, v184
	v_lshlrev_b32_e32 v218, 16, v185
	v_and_b32_e32 v232, 0xffff0000, v185
	v_add_f32_e32 v233, 0, v213
	v_add_f32_e32 v213, v194, v195
	v_add_f32_e32 v215, v196, v197
	v_mov_b32_e32 v219, v241
	s_waitcnt lgkmcnt(0)
	v_pk_add_f32 v[242:243], v[212:213], v[214:215]
	v_pk_add_f32 v[240:241], v[218:219], v[232:233]
	s_nop 0
	v_pk_add_f32 v[240:241], v[242:243], v[240:241]
	s_nop 0
	v_add_f32_e32 v213, v240, v241
	s_waitcnt lgkmcnt(0)
	s_nop 1
	v_add_f32_dpp v213, v213, v213 quad_perm:[1,0,3,2] row_mask:0xf bank_mask:0xf
	s_nop 1
	v_add_f32_dpp v213, v213, v213 quad_perm:[2,3,0,1] row_mask:0xf bank_mask:0xf
	s_nop 1
	v_add_f32_dpp v213, v213, v213 row_half_mirror row_mask:0xf bank_mask:0xf
	s_nop 1
	v_add_f32_dpp v213, v213, v213 row_mirror row_mask:0xf bank_mask:0xf
	v_mov_b32_e32 v215, v213
	s_nop 1
	v_permlane16_swap_b32_e32 v213, v215
	v_add_f32_e32 v213, v213, v215
	v_mov_b32_e32 v215, v213
	s_nop 1
	v_permlane32_swap_b32_e32 v213, v215
	v_add_f32_e32 v213, v213, v215
	v_fmac_f32_e32 v234, 0xba800000, v213
	v_fmac_f32_e32 v235, 0xba800000, v213
	v_fmac_f32_e32 v217, 0xba800000, v213
	v_fmac_f32_e32 v216, 0xba800000, v213
	v_mov_b32_e32 v240, v217
	v_mov_b32_e32 v241, v235
	v_mov_b32_e32 v217, v234
	v_pk_mul_f32 v[242:243], v[240:241], v[240:241]
	v_pk_mul_f32 v[234:235], v[216:217], v[216:217]
	v_fmac_f32_e32 v238, 0xba800000, v213
	v_pk_mov_b32 v[244:245], v[234:235], v[242:243] op_sel:[1,0]
	v_mov_b32_e32 v235, v243
	v_fmac_f32_e32 v239, 0xba800000, v213
	v_fmac_f32_e32 v237, 0xba800000, v213
	v_pk_add_f32 v[234:235], v[244:245], v[234:235]
	v_fmac_f32_e32 v236, 0xba800000, v213
	v_mov_b32_e32 v242, v237
	v_mov_b32_e32 v243, v239
	v_mov_b32_e32 v237, v238
	v_pk_add_f32 v[234:235], v[234:235], v[234:235] op_sel_hi:[0,1]
	v_pk_mul_f32 v[244:245], v[242:243], v[242:243]
	v_pk_mul_f32 v[238:239], v[236:237], v[236:237]
	v_fmac_f32_e32 v194, 0xba800000, v213
	v_pk_mov_b32 v[246:247], v[238:239], v[244:245] op_sel:[1,0]
	v_mov_b32_e32 v239, v245
	v_fmac_f32_e32 v195, 0xba800000, v213
	v_fmac_f32_e32 v196, 0xba800000, v213
	v_mul_f32_e32 v234, v194, v194
	v_pk_add_f32 v[238:239], v[246:247], v[238:239]
	v_fmac_f32_e32 v197, 0xba800000, v213
	v_pk_fma_f32 v[244:245], v[194:195], v[194:195], v[234:235] op_sel_hi:[1,1,0]
	v_mul_f32_e32 v234, v196, v196
	v_pk_add_f32 v[238:239], v[238:239], v[238:239] op_sel_hi:[0,1]
	v_pk_fma_f32 v[246:247], v[196:197], v[196:197], v[234:235] op_sel_hi:[1,1,0]
	v_fmac_f32_e32 v232, 0xba800000, v213
	v_fmac_f32_e32 v218, 0xba800000, v213
	v_fmac_f32_e32 v214, 0xba800000, v213
	v_fmac_f32_e32 v212, 0xba800000, v213
	v_mul_f32_e32 v244, v212, v212
	v_mul_f32_e32 v246, v214, v214
	v_mul_f32_e32 v234, v218, v218
	v_mul_f32_e32 v238, v232, v232
	v_pk_add_f32 v[244:245], v[244:245], v[246:247]
	v_pk_add_f32 v[234:235], v[234:235], v[238:239]
	s_nop 0
	v_pk_add_f32 v[234:235], v[244:245], v[234:235]
	s_nop 0
	v_add_f32_e32 v213, v234, v235
	s_waitcnt lgkmcnt(0)
	s_nop 1
	v_add_f32_dpp v213, v213, v213 quad_perm:[1,0,3,2] row_mask:0xf bank_mask:0xf
	s_nop 1
	v_add_f32_dpp v213, v213, v213 quad_perm:[2,3,0,1] row_mask:0xf bank_mask:0xf
	s_nop 1
	v_add_f32_dpp v213, v213, v213 row_half_mirror row_mask:0xf bank_mask:0xf
	s_nop 1
	v_add_f32_dpp v213, v213, v213 row_mirror row_mask:0xf bank_mask:0xf
	v_mov_b32_e32 v215, v213
	s_nop 1
	v_permlane16_swap_b32_e32 v213, v215
	v_add_f32_e32 v213, v213, v215
	v_mov_b32_e32 v215, v213
	s_nop 1
	v_permlane32_swap_b32_e32 v213, v215
	v_add_f32_e32 v213, v213, v215
	v_fmamk_f32 v213, v213, 0x3a800000, v228
	v_mul_f32_e32 v215, 0x4f800000, v213
	v_cmp_gt_f32_e32 vcc, s30, v213
	s_nop 1
	v_cndmask_b32_e32 v213, v213, v215, vcc
	v_sqrt_f32_e32 v215, v213
	s_nop 0
	v_add_u32_e32 v219, -1, v215
	v_fma_f32 v233, -v219, v215, v213
	v_cmp_ge_f32_e64 s[0:1], 0, v233
	v_add_u32_e32 v233, 1, v215
	s_nop 0
	v_cndmask_b32_e64 v219, v215, v219, s[0:1]
	v_fma_f32 v215, -v233, v215, v213
	v_cmp_lt_f32_e64 s[0:1], 0, v215
	s_nop 1
	v_cndmask_b32_e64 v215, v219, v233, s[0:1]
	v_mul_f32_e32 v219, 0x37800000, v215
	v_cndmask_b32_e32 v215, v215, v219, vcc
	v_cmp_class_f32_e32 vcc, v213, v229
	s_nop 1
	v_cndmask_b32_e32 v213, v215, v213, vcc
	v_div_scale_f32 v215, s[0:1], v213, v213, 1.0
	v_rcp_f32_e32 v219, v215
	s_nop 0
	v_fma_f32 v233, -v215, v219, 1.0
	v_fmac_f32_e32 v219, v233, v219
	v_div_scale_f32 v233, vcc, 1.0, v213, 1.0
	v_mul_f32_e32 v234, v233, v219
	v_fma_f32 v235, -v215, v234, v233
	v_fmac_f32_e32 v234, v235, v219
	v_fma_f32 v215, -v215, v234, v233
	v_div_fmas_f32 v215, v215, v219, v234
	v_div_fixup_f32 v234, v215, v213, 1.0
	v_pk_mul_f32 v[216:217], v[216:217], v[234:235] op_sel_hi:[1,0]
	v_pk_mul_f32 v[194:195], v[194:195], v[234:235] op_sel_hi:[1,0]
	v_mov_b32_e32 v213, v214
	v_pk_mul_f32 v[238:239], v[240:241], v[234:235] op_sel_hi:[1,0]
	v_pk_fma_f32 v[240:241], v[2:3], v[216:217], v[6:7]
	v_pk_mul_f32 v[216:217], v[236:237], v[234:235] op_sel_hi:[1,0]
	v_pk_mul_f32 v[196:197], v[196:197], v[234:235] op_sel_hi:[1,0]
	v_pk_fma_f32 v[244:245], v[18:19], v[194:195], v[30:31]
	v_pk_mul_f32 v[194:195], v[212:213], v[234:235] op_sel_hi:[1,0]
	v_mov_b32_e32 v219, v232
	v_pk_mul_f32 v[236:237], v[242:243], v[234:235] op_sel_hi:[1,0]
	v_pk_fma_f32 v[242:243], v[14:15], v[216:217], v[26:27]
	v_pk_fma_f32 v[216:217], v[20:21], v[196:197], v[32:33]
	v_pk_mul_f32 v[196:197], v[218:219], v[234:235] op_sel_hi:[1,0]
	v_pk_fma_f32 v[218:219], v[10:11], v[194:195], v[22:23]
	v_pk_fma_f32 v[238:239], v[4:5], v[238:239], v[8:9]
	v_cvt_pk_bf16_f32 v194, v240, v241
	v_pk_fma_f32 v[212:213], v[12:13], v[196:197], v[24:25]
	v_cvt_pk_bf16_f32 v195, v238, v239
	v_fma_f32 v234, v36, v240, 0
	v_fma_f32 v235, v37, v240, 0
	v_fma_f32 v246, v38, v240, 0
	v_fma_f32 v247, v39, v240, 0
	v_fma_f32 v248, v40, v240, 0
	v_fma_f32 v249, v41, v240, 0
	v_pk_fma_f32 v[232:233], v[34:35], v[240:241], 0 op_sel_hi:[1,0,0]
	v_pk_fma_f32 v[236:237], v[16:17], v[236:237], v[28:29]
	v_fmac_f32_e32 v234, v44, v241
	v_fmac_f32_e32 v235, v45, v241
	v_fmac_f32_e32 v246, v46, v241
	v_fmac_f32_e32 v247, v47, v241
	v_fmac_f32_e32 v248, v48, v241
	v_fmac_f32_e32 v249, v49, v241
	v_pk_fma_f32 v[232:233], v[42:43], v[240:241], v[232:233] op_sel:[0,1,0]
	v_cvt_pk_bf16_f32 v196, v242, v243
	v_fmac_f32_e32 v234, v52, v238
	v_fmac_f32_e32 v235, v53, v238
	v_fmac_f32_e32 v246, v54, v238
	v_fmac_f32_e32 v247, v55, v238
	v_fmac_f32_e32 v248, v56, v238
	v_fmac_f32_e32 v249, v57, v238
	v_pk_fma_f32 v[232:233], v[50:51], v[238:239], v[232:233] op_sel_hi:[1,0,1]
	v_fmac_f32_e32 v234, v60, v239
	v_fmac_f32_e32 v235, v61, v239
	v_fmac_f32_e32 v246, v62, v239
	v_fmac_f32_e32 v247, v63, v239
	v_fmac_f32_e32 v248, v64, v239
	v_fmac_f32_e32 v249, v65, v239
	v_pk_fma_f32 v[232:233], v[58:59], v[238:239], v[232:233] op_sel:[0,1,0]
	v_fmac_f32_e32 v234, v68, v242
	v_fmac_f32_e32 v235, v69, v242
	v_fmac_f32_e32 v246, v70, v242
	v_fmac_f32_e32 v247, v71, v242
	v_fmac_f32_e32 v248, v72, v242
	v_fmac_f32_e32 v249, v73, v242
	v_pk_fma_f32 v[232:233], v[66:67], v[242:243], v[232:233] op_sel_hi:[1,0,1]
	v_cvt_pk_bf16_f32 v197, v236, v237
	v_add_co_u32_e32 v214, vcc, s28, v210
	v_fmac_f32_e32 v234, v76, v243
	v_fmac_f32_e32 v235, v77, v243
	v_fmac_f32_e32 v246, v78, v243
	v_fmac_f32_e32 v247, v79, v243
	v_fmac_f32_e32 v248, v80, v243
	v_fmac_f32_e32 v249, v81, v243
	v_pk_fma_f32 v[232:233], v[74:75], v[242:243], v[232:233] op_sel:[0,1,0]
	v_addc_co_u32_e32 v215, vcc, 0, v211, vcc
	v_fmac_f32_e32 v234, v84, v236
	v_fmac_f32_e32 v235, v85, v236
	v_fmac_f32_e32 v246, v86, v236
	v_fmac_f32_e32 v247, v87, v236
	v_fmac_f32_e32 v248, v88, v236
	v_fmac_f32_e32 v249, v89, v236
	v_pk_fma_f32 v[232:233], v[82:83], v[236:237], v[232:233] op_sel_hi:[1,0,1]
	global_store_dwordx4 v[214:215], v[194:197], off
	v_fmac_f32_e32 v234, v92, v237
	v_fmac_f32_e32 v235, v93, v237
	v_fmac_f32_e32 v246, v94, v237
	v_fmac_f32_e32 v247, v95, v237
	v_fmac_f32_e32 v248, v96, v237
	v_fmac_f32_e32 v249, v97, v237
	v_pk_fma_f32 v[232:233], v[90:91], v[236:237], v[232:233] op_sel:[0,1,0]
	v_fmac_f32_e32 v234, v108, v244
	v_fmac_f32_e32 v235, v109, v244
	v_fmac_f32_e32 v246, v98, v244
	v_fmac_f32_e32 v247, v99, v244
	v_fmac_f32_e32 v248, v100, v244
	v_fmac_f32_e32 v249, v101, v244
	v_pk_fma_f32 v[232:233], v[106:107], v[244:245], v[232:233] op_sel_hi:[1,0,1]
	v_pk_fma_f32 v[232:233], v[102:103], v[244:245], v[232:233] op_sel:[0,1,0]
	v_fmac_f32_e32 v234, v104, v245
	v_fmac_f32_e32 v235, v105, v245
	v_fmac_f32_e32 v246, v110, v245
	v_fmac_f32_e32 v247, v111, v245
	v_fmac_f32_e32 v248, v112, v245
	v_fmac_f32_e32 v249, v113, v245
	v_cvt_pk_bf16_f32 v194, v244, v245
	v_bfe_u32 v195, v216, 16, 1
	v_bfe_u32 v196, v217, 16, 1
	v_fmac_f32_e32 v234, v124, v216
	v_fmac_f32_e32 v235, v125, v216
	v_fmac_f32_e32 v246, v138, v216
	v_fmac_f32_e32 v247, v139, v216
	v_fmac_f32_e32 v248, v140, v216
	v_fmac_f32_e32 v249, v141, v216
	v_pk_fma_f32 v[232:233], v[122:123], v[216:217], v[232:233] op_sel_hi:[1,0,1]
	v_add3_u32 v195, v216, v195, s31
	v_add3_u32 v196, v217, v196, s31
	v_fmac_f32_e32 v234, v116, v217
	v_fmac_f32_e32 v235, v117, v217
	v_fmac_f32_e32 v246, v118, v217
	v_fmac_f32_e32 v247, v119, v217
	v_fmac_f32_e32 v248, v120, v217
	v_fmac_f32_e32 v249, v121, v217
	v_pk_fma_f32 v[216:217], v[114:115], v[216:217], v[232:233] op_sel:[0,1,0]
	v_lshrrev_b32_e32 v195, 16, v195
	v_pk_fma_f32 v[216:217], v[126:127], v[218:219], v[216:217] op_sel_hi:[1,0,1]
	v_and_or_b32 v195, v196, s29, v195
	v_pk_fma_f32 v[216:217], v[134:135], v[218:219], v[216:217] op_sel:[0,1,0]
	v_bfe_u32 v196, v218, 16, 1
	v_pk_fma_f32 v[216:217], v[142:143], v[212:213], v[216:217] op_sel_hi:[1,0,1]
	v_bfe_u32 v197, v219, 16, 1
	v_pk_fma_f32 v[216:217], v[154:155], v[212:213], v[216:217] op_sel:[0,1,0]
	ds_bpermute_b32 v232, v220, v216
	ds_bpermute_b32 v233, v220, v217
	v_fmac_f32_e32 v234, v128, v218
	v_fmac_f32_e32 v235, v129, v218
	v_fmac_f32_e32 v246, v130, v218
	v_fmac_f32_e32 v247, v131, v218
	v_fmac_f32_e32 v248, v132, v218
	v_fmac_f32_e32 v249, v133, v218
	s_waitcnt lgkmcnt(0)
	v_pk_add_f32 v[216:217], v[216:217], v[232:233]
	v_add3_u32 v196, v218, v196, s31
	v_add3_u32 v197, v219, v197, s31
	v_fmac_f32_e32 v234, v136, v219
	v_fmac_f32_e32 v235, v137, v219
	v_fmac_f32_e32 v246, v146, v219
	v_fmac_f32_e32 v247, v147, v219
	v_fmac_f32_e32 v248, v148, v219
	v_fmac_f32_e32 v249, v149, v219
	ds_bpermute_b32 v218, v221, v216
	ds_bpermute_b32 v219, v221, v217
	v_lshrrev_b32_e32 v196, 16, v196
	v_fmac_f32_e32 v234, v144, v212
	v_and_or_b32 v196, v197, s29, v196
	v_bfe_u32 v197, v212, 16, 1
	s_waitcnt lgkmcnt(0)
	v_pk_add_f32 v[216:217], v[216:217], v[218:219]
	v_fmac_f32_e32 v234, v156, v213
	v_add3_u32 v197, v212, v197, s31
	v_fmac_f32_e32 v235, v145, v212
	v_fmac_f32_e32 v246, v150, v212
	v_fmac_f32_e32 v247, v151, v212
	v_fmac_f32_e32 v248, v152, v212
	v_fmac_f32_e32 v249, v153, v212
	ds_bpermute_b32 v218, v222, v216
	ds_bpermute_b32 v219, v222, v217
	ds_bpermute_b32 v212, v220, v234
	v_fmac_f32_e32 v235, v157, v213
	v_fmac_f32_e32 v246, v158, v213
	ds_bpermute_b32 v233, v220, v235
	s_waitcnt lgkmcnt(2)
	v_pk_add_f32 v[216:217], v[216:217], v[218:219]
	s_waitcnt lgkmcnt(1)
	v_add_f32_e32 v212, v234, v212
	ds_bpermute_b32 v218, v223, v216
	ds_bpermute_b32 v219, v223, v217
	ds_bpermute_b32 v232, v221, v212
	ds_bpermute_b32 v234, v220, v246
	v_fmac_f32_e32 v247, v159, v213
	v_fmac_f32_e32 v248, v160, v213
	s_waitcnt lgkmcnt(2)
	v_pk_add_f32 v[216:217], v[216:217], v[218:219]
	s_waitcnt lgkmcnt(1)
	v_add_f32_e32 v212, v212, v232
	ds_bpermute_b32 v218, v224, v216
	ds_bpermute_b32 v219, v224, v217
	ds_bpermute_b32 v232, v222, v212
	v_fmac_f32_e32 v249, v161, v213
	ds_bpermute_b32 v238, v220, v247
	ds_bpermute_b32 v239, v220, v249
	s_waitcnt lgkmcnt(3)
	v_pk_add_f32 v[216:217], v[216:217], v[218:219]
	v_add_f32_e32 v218, v235, v233
	s_waitcnt lgkmcnt(2)
	v_add_f32_e32 v212, v212, v232
	v_add_f32_e32 v232, v246, v234
	ds_bpermute_b32 v219, v221, v218
	ds_bpermute_b32 v233, v221, v232
	ds_bpermute_b32 v234, v223, v212
	s_waitcnt lgkmcnt(4)
	v_add_f32_e32 v238, v247, v238
	s_waitcnt lgkmcnt(3)
	v_add_f32_e32 v239, v249, v239
	s_waitcnt lgkmcnt(2)
	v_add_f32_e32 v219, v218, v219
	s_waitcnt lgkmcnt(1)
	v_add_f32_e32 v232, v232, v233
	ds_bpermute_b32 v235, v222, v219
	ds_bpermute_b32 v233, v222, v232
	s_waitcnt lgkmcnt(2)
	v_add_f32_e32 v212, v212, v234
	ds_bpermute_b32 v236, v224, v212
	ds_bpermute_b32 v240, v221, v238
	s_waitcnt lgkmcnt(3)
	v_add_f32_e32 v234, v219, v235
	s_waitcnt lgkmcnt(2)
	v_add_f32_e32 v232, v232, v233
	ds_bpermute_b32 v235, v223, v234
	ds_bpermute_b32 v233, v223, v232
	s_waitcnt lgkmcnt(3)
	v_add_f32_e32 v212, v212, v236
	ds_bpermute_b32 v242, v221, v239
	s_waitcnt lgkmcnt(3)
	v_add_f32_e32 v238, v238, v240
	s_waitcnt lgkmcnt(2)
	v_add_f32_e32 v234, v234, v235
	s_waitcnt lgkmcnt(1)
	v_add_f32_e32 v236, v232, v233
	ds_bpermute_b32 v235, v224, v234
	ds_bpermute_b32 v237, v224, v236
	s_waitcnt lgkmcnt(2)
	v_add_f32_e32 v239, v239, v242
	ds_bpermute_b32 v240, v222, v238
	ds_bpermute_b32 v242, v222, v239
	s_waitcnt lgkmcnt(3)
	v_add_f32_e32 v233, v234, v235
	s_waitcnt lgkmcnt(2)
	v_add_f32_e32 v235, v236, v237
	ds_bpermute_b32 v237, v220, v248
	s_waitcnt lgkmcnt(2)
	v_add_f32_e32 v238, v238, v240
	s_waitcnt lgkmcnt(1)
	v_add_f32_e32 v239, v239, v242
	ds_bpermute_b32 v240, v223, v238
	ds_bpermute_b32 v242, v223, v239
	s_waitcnt lgkmcnt(2)
	v_add_f32_e32 v237, v248, v237
	ds_bpermute_b32 v241, v221, v237
	ds_bpermute_b32 v218, v225, v216
	s_waitcnt lgkmcnt(3)
	v_add_f32_e32 v238, v238, v240
	s_waitcnt lgkmcnt(2)
	v_add_f32_e32 v242, v239, v242
	ds_bpermute_b32 v240, v224, v238
	s_waitcnt lgkmcnt(2)
	v_add_f32_e32 v237, v237, v241
	ds_bpermute_b32 v241, v222, v237
	ds_bpermute_b32 v244, v224, v242
	ds_bpermute_b32 v219, v225, v217
	ds_bpermute_b32 v232, v225, v212
	ds_bpermute_b32 v234, v225, v233
	s_waitcnt lgkmcnt(4)
	v_add_f32_e32 v237, v237, v241
	ds_bpermute_b32 v241, v223, v237
	ds_bpermute_b32 v236, v225, v235
	v_lshrrev_b32_e32 v197, 16, v197
	s_waitcnt lgkmcnt(1)
	v_add_f32_e32 v241, v237, v241
	ds_bpermute_b32 v243, v224, v241
	v_add_f32_e32 v237, v238, v240
	ds_bpermute_b32 v238, v225, v237
	s_waitcnt lgkmcnt(1)
	v_add_f32_e32 v239, v241, v243
	v_add_f32_e32 v241, v242, v244
	ds_bpermute_b32 v240, v225, v239
	ds_bpermute_b32 v242, v225, v241
	v_bfe_u32 v243, v213, 16, 1
	v_add3_u32 v213, v213, v243, s31
	v_and_or_b32 v197, v213, s29, v197
	global_store_dwordx4 v[214:215], v[194:197], off offset:1024
	s_and_saveexec_b64 s[24:25], s[2:3]
	s_cbranch_execz .LBB0_1243
	v_pk_add_f32 v[196:197], v[216:217], v[218:219]
	v_add_f32_e32 v212, v212, v232
	v_cmp_gt_f32_e32 vcc, v197, v196
	v_add_f32_e32 v233, v233, v234
	v_add_f32_e32 v215, v235, v236
	v_cndmask_b32_e32 v194, v196, v197, vcc
	v_cmp_gt_f32_e64 s[0:1], v212, v194
	s_waitcnt lgkmcnt(2)
	v_add_f32_e32 v214, v237, v238
	s_waitcnt lgkmcnt(1)
	v_add_f32_e32 v213, v239, v240
	v_cndmask_b32_e64 v194, v194, v212, s[0:1]
	v_cmp_gt_f32_e64 s[4:5], v233, v194
	s_waitcnt lgkmcnt(0)
	v_add_f32_e32 v195, v241, v242
	v_cmp_nlg_f32_e64 s[14:15], s34, v196
	v_cndmask_b32_e64 v194, v194, v233, s[4:5]
	v_cmp_gt_f32_e64 s[6:7], v215, v194
	s_nop 1
	v_cndmask_b32_e64 v194, v194, v215, s[6:7]
	v_cmp_gt_f32_e64 s[8:9], v214, v194
	s_nop 1
	v_cndmask_b32_e64 v194, v194, v214, s[8:9]
	v_cmp_gt_f32_e64 s[10:11], v213, v194
	s_nop 1
	v_cndmask_b32_e64 v216, v194, v213, s[10:11]
	v_cndmask_b32_e64 v194, 0, 1, vcc
	v_cndmask_b32_e64 v194, v194, 2, s[0:1]
	v_cndmask_b32_e64 v194, v194, 3, s[4:5]
	v_cndmask_b32_e64 v194, v194, 4, s[6:7]
	v_cndmask_b32_e64 v194, v194, 5, s[8:9]
	v_cndmask_b32_e64 v194, v194, 6, s[10:11]
	v_cmp_ngt_f32_e32 vcc, v195, v216
	s_and_b64 s[16:17], s[10:11], vcc
	s_nop 0
	v_cndmask_b32_e32 v194, 7, v194, vcc
	v_cmp_eq_u32_e64 s[12:13], 0, v194
	s_or_b64 s[12:13], s[12:13], s[14:15]
	v_cmp_ne_u32_e64 s[10:11], 1, v194
	v_cndmask_b32_e64 v196, v196, v231, s[12:13]
	v_cmp_gt_f32_e64 s[14:15], v197, v196
	s_and_b64 s[10:11], s[10:11], s[14:15]
	v_cndmask_b32_e64 v196, v196, v197, s[10:11]
	v_cmp_ne_u32_e64 s[8:9], 2, v194
	v_cmp_gt_f32_e64 s[14:15], v212, v196
	s_and_b64 s[8:9], s[8:9], s[14:15]
	v_cndmask_b32_e64 v196, v196, v212, s[8:9]
	v_cmp_ne_u32_e64 s[6:7], 3, v194
	v_cmp_gt_f32_e64 s[14:15], v233, v196
	s_and_b64 s[6:7], s[6:7], s[14:15]
	v_cndmask_b32_e64 v196, v196, v233, s[6:7]
	v_cmp_ne_u32_e64 s[4:5], 4, v194
	v_cmp_gt_f32_e64 s[14:15], v215, v196
	s_and_b64 s[4:5], s[4:5], s[14:15]
	v_cndmask_b32_e64 v196, v196, v215, s[4:5]
	v_cmp_ne_u32_e64 s[0:1], 5, v194
	v_cmp_gt_f32_e64 s[14:15], v214, v196
	s_and_b64 s[0:1], s[0:1], s[14:15]
	v_cndmask_b32_e64 v196, v196, v214, s[0:1]
	v_cmp_ngt_f32_e64 s[14:15], v213, v196
	s_or_b64 s[14:15], s[16:17], s[14:15]
	v_cndmask_b32_e64 v197, 0, -1, s[12:13]
	v_cndmask_b32_e64 v196, v213, v196, s[14:15]
	v_cmp_gt_f32_e64 s[16:17], v195, v196
	s_and_b64 s[16:17], vcc, s[16:17]
	v_cndmask_b32_e64 v197, v197, 1, s[10:11]
	v_cndmask_b32_e64 v196, v196, v195, s[16:17]
	v_cndmask_b32_e32 v195, v195, v216, vcc
	v_sub_f32_e32 v195, v196, v195
	v_mul_f32_e32 v195, 0x3fb8aa3b, v195
	v_exp_f32_e32 v213, v195
	v_cndmask_b32_e64 v195, v197, 2, s[8:9]
	v_cndmask_b32_e64 v195, v195, 3, s[6:7]
	v_cndmask_b32_e64 v195, v195, 4, s[4:5]
	v_add_f32_e32 v212, 1.0, v213
	v_div_scale_f32 v196, s[4:5], v212, v212, 1.0
	v_rcp_f32_e32 v214, v196
	v_cndmask_b32_e64 v195, v195, 5, s[0:1]
	v_cndmask_b32_e64 v195, 6, v195, s[14:15]
	v_cndmask_b32_e64 v195, v195, 7, s[16:17]
	v_fma_f32 v197, -v196, v214, 1.0
	v_fmac_f32_e32 v214, v197, v214
	v_div_scale_f32 v197, vcc, 1.0, v212, 1.0
	v_mul_f32_e32 v215, v197, v214
	v_fma_f32 v216, -v196, v215, v197
	v_fmac_f32_e32 v215, v216, v214
	v_fma_f32 v216, -v196, v215, v197
	v_lshl_add_u32 v196, v194, 2, 0
	ds_add_rtn_u32 v196, v196, v230
	v_lshl_add_u32 v197, v195, 2, 0
	ds_add_rtn_u32 v197, v197, v230
	v_div_fmas_f32 v214, v216, v214, v215
	v_div_fixup_f32 v212, v214, v212, 1.0
	v_mul_f32_e32 v213, v213, v212
	s_waitcnt lgkmcnt(0)
	ds_write_b128 v226, v[194:197] offset:32
	v_add_u32_e32 v194, 4, v227
	v_ashrrev_i32_e32 v195, 31, v194
	v_lshl_add_u64 v[194:195], v[194:195], 2, s[36:37]
	global_store_dwordx2 v[194:195], v[212:213], off

.LBB0_1245:
	s_waitcnt vmcnt(7)
	v_lshlrev_b32_e32 v219, 16, v187
	v_lshlrev_b32_e32 v218, 16, v186
	v_and_b32_e32 v187, 0xffff0000, v187
	v_and_b32_e32 v186, 0xffff0000, v186
	s_waitcnt vmcnt(6)
	v_lshlrev_b32_e32 v194, 16, v190
	v_and_b32_e32 v195, 0xffff0000, v190
	v_lshlrev_b32_e32 v196, 16, v191
	v_and_b32_e32 v197, 0xffff0000, v191
	v_pk_add_f32 v[190:191], v[218:219], v[186:187]
	v_lshlrev_b32_e32 v233, 16, v189
	v_add_f32_e32 v190, v190, v191
	v_lshlrev_b32_e32 v232, 16, v188
	v_and_b32_e32 v189, 0xffff0000, v189
	v_and_b32_e32 v188, 0xffff0000, v188
	v_add_f32_e32 v217, 0, v190
	v_pk_add_f32 v[190:191], v[232:233], v[188:189]
	v_lshlrev_b32_e32 v212, 16, v192
	v_pk_add_f32 v[190:191], v[190:191], v[190:191] op_sel_hi:[0,1]
	v_and_b32_e32 v192, 0xffff0000, v192
	v_lshlrev_b32_e32 v214, 16, v193
	v_and_b32_e32 v216, 0xffff0000, v193
	v_add_f32_e32 v213, v194, v195
	v_add_f32_e32 v193, v196, v197
	v_mov_b32_e32 v215, v191
	v_pk_add_f32 v[234:235], v[212:213], v[192:193]
	v_pk_add_f32 v[190:191], v[214:215], v[216:217]
	s_nop 0
	v_pk_add_f32 v[190:191], v[234:235], v[190:191]
	s_nop 0
	v_add_f32_e32 v190, v190, v191
	s_waitcnt lgkmcnt(0)
	s_nop 1
	v_add_f32_dpp v190, v190, v190 quad_perm:[1,0,3,2] row_mask:0xf bank_mask:0xf
	s_nop 1
	v_add_f32_dpp v190, v190, v190 quad_perm:[2,3,0,1] row_mask:0xf bank_mask:0xf
	s_nop 1
	v_add_f32_dpp v190, v190, v190 row_half_mirror row_mask:0xf bank_mask:0xf
	s_nop 1
	v_add_f32_dpp v190, v190, v190 row_mirror row_mask:0xf bank_mask:0xf
	v_mov_b32_e32 v191, v190
	s_nop 1
	v_permlane16_swap_b32_e32 v190, v191
	v_add_f32_e32 v190, v190, v191
	v_mov_b32_e32 v191, v190
	s_nop 1
	v_permlane32_swap_b32_e32 v190, v191
	v_add_f32_e32 v193, v190, v191
	v_fmac_f32_e32 v186, 0xba800000, v193
	v_fmac_f32_e32 v187, 0xba800000, v193
	v_fmac_f32_e32 v219, 0xba800000, v193
	v_fmac_f32_e32 v218, 0xba800000, v193
	v_mov_b32_e32 v234, v219
	v_mov_b32_e32 v235, v187
	v_mov_b32_e32 v219, v186
	v_pk_mul_f32 v[190:191], v[234:235], v[234:235]
	v_pk_mul_f32 v[186:187], v[218:219], v[218:219]
	v_fmac_f32_e32 v188, 0xba800000, v193
	v_pk_mov_b32 v[236:237], v[186:187], v[190:191] op_sel:[1,0]
	v_mov_b32_e32 v187, v191
	v_fmac_f32_e32 v189, 0xba800000, v193
	v_fmac_f32_e32 v233, 0xba800000, v193
	v_pk_add_f32 v[186:187], v[236:237], v[186:187]
	v_fmac_f32_e32 v232, 0xba800000, v193
	v_mov_b32_e32 v236, v233
	v_mov_b32_e32 v237, v189
	v_mov_b32_e32 v233, v188
	v_pk_add_f32 v[186:187], v[186:187], v[186:187] op_sel_hi:[0,1]
	v_pk_mul_f32 v[190:191], v[236:237], v[236:237]
	v_pk_mul_f32 v[188:189], v[232:233], v[232:233]
	v_fmac_f32_e32 v194, 0xba800000, v193
	v_pk_mov_b32 v[238:239], v[188:189], v[190:191] op_sel:[1,0]
	v_mov_b32_e32 v189, v191
	v_fmac_f32_e32 v195, 0xba800000, v193
	v_fmac_f32_e32 v196, 0xba800000, v193
	v_mul_f32_e32 v186, v194, v194
	v_pk_add_f32 v[188:189], v[238:239], v[188:189]
	v_fmac_f32_e32 v197, 0xba800000, v193
	v_pk_fma_f32 v[190:191], v[194:195], v[194:195], v[186:187] op_sel_hi:[1,1,0]
	v_mul_f32_e32 v186, v196, v196
	v_pk_add_f32 v[188:189], v[188:189], v[188:189] op_sel_hi:[0,1]
	v_pk_fma_f32 v[238:239], v[196:197], v[196:197], v[186:187] op_sel_hi:[1,1,0]
	v_fmac_f32_e32 v216, 0xba800000, v193
	v_fmac_f32_e32 v214, 0xba800000, v193
	v_fmac_f32_e32 v192, 0xba800000, v193
	v_fmac_f32_e32 v212, 0xba800000, v193
	v_mul_f32_e32 v190, v212, v212
	v_mul_f32_e32 v238, v192, v192
	v_mul_f32_e32 v186, v214, v214
	v_mul_f32_e32 v188, v216, v216
	v_pk_add_f32 v[190:191], v[190:191], v[238:239]
	v_pk_add_f32 v[186:187], v[186:187], v[188:189]
	v_lshl_add_u64 v[238:239], v[210:211], 0, s[18:19]
	v_pk_add_f32 v[186:187], v[190:191], v[186:187]
	v_lshl_add_u64 v[190:191], v[210:211], 0, s[20:21]
	v_add_f32_e32 v186, v186, v187
	ds_bpermute_b32 v187, v220, v186
	v_mov_b32_e32 v213, v192
	v_mov_b32_e32 v215, v216
	s_waitcnt lgkmcnt(0)
	v_add_f32_e32 v186, v186, v187
	ds_bpermute_b32 v187, v221, v186
	s_waitcnt lgkmcnt(0)
	v_add_f32_e32 v186, v186, v187
	ds_bpermute_b32 v187, v222, v186
	s_waitcnt lgkmcnt(0)
	v_add_f32_e32 v186, v186, v187
	ds_bpermute_b32 v187, v223, v186
	s_waitcnt lgkmcnt(0)
	v_add_f32_e32 v186, v186, v187
	ds_bpermute_b32 v187, v224, v186
	s_waitcnt lgkmcnt(0)
	v_add_f32_e32 v186, v186, v187
	ds_bpermute_b32 v187, v225, v186
	s_waitcnt lgkmcnt(0)
	v_add_f32_e32 v186, v186, v187
	v_fmamk_f32 v186, v186, 0x3a800000, v228
	v_mul_f32_e32 v187, 0x4f800000, v186
	v_cmp_gt_f32_e32 vcc, s30, v186
	s_nop 1
	v_cndmask_b32_e32 v186, v186, v187, vcc
	v_sqrt_f32_e32 v187, v186
	s_nop 0
	v_add_u32_e32 v188, -1, v187
	v_fma_f32 v189, -v188, v187, v186
	v_cmp_ge_f32_e64 s[0:1], 0, v189
	v_add_u32_e32 v189, 1, v187
	s_nop 0
	v_cndmask_b32_e64 v188, v187, v188, s[0:1]
	v_fma_f32 v187, -v189, v187, v186
	v_cmp_lt_f32_e64 s[0:1], 0, v187
	s_nop 1
	v_cndmask_b32_e64 v187, v188, v189, s[0:1]
	v_mul_f32_e32 v188, 0x37800000, v187
	v_cndmask_b32_e32 v187, v187, v188, vcc
	v_cmp_class_f32_e32 vcc, v186, v229
	s_nop 1
	v_cndmask_b32_e32 v186, v187, v186, vcc
	v_div_scale_f32 v187, s[0:1], v186, v186, 1.0
	v_rcp_f32_e32 v188, v187
	s_nop 0
	v_fma_f32 v189, -v187, v188, 1.0
	v_fmac_f32_e32 v188, v189, v188
	v_div_scale_f32 v189, vcc, 1.0, v186, 1.0
	v_mul_f32_e32 v193, v189, v188
	v_fma_f32 v210, -v187, v193, v189
	v_fmac_f32_e32 v193, v210, v188
	v_fma_f32 v187, -v187, v193, v189
	v_div_fmas_f32 v187, v187, v188, v193
	v_div_fixup_f32 v186, v187, v186, 1.0
	v_pk_mul_f32 v[188:189], v[218:219], v[186:187] op_sel_hi:[1,0]
	v_pk_mul_f32 v[210:211], v[234:235], v[186:187] op_sel_hi:[1,0]
	v_pk_fma_f32 v[218:219], v[2:3], v[188:189], v[6:7]
	v_pk_mul_f32 v[188:189], v[232:233], v[186:187] op_sel_hi:[1,0]
	v_pk_mul_f32 v[232:233], v[236:237], v[186:187] op_sel_hi:[1,0]
	v_pk_fma_f32 v[234:235], v[14:15], v[188:189], v[26:27]
	v_pk_mul_f32 v[188:189], v[194:195], v[186:187] op_sel_hi:[1,0]
	v_pk_mul_f32 v[194:195], v[196:197], v[186:187] op_sel_hi:[1,0]
	v_pk_fma_f32 v[236:237], v[18:19], v[188:189], v[30:31]
	v_pk_mul_f32 v[188:189], v[212:213], v[186:187] op_sel_hi:[1,0]
	v_pk_mul_f32 v[186:187], v[214:215], v[186:187] op_sel_hi:[1,0]
	v_pk_fma_f32 v[210:211], v[4:5], v[210:211], v[8:9]
	v_pk_fma_f32 v[192:193], v[12:13], v[186:187], v[24:25]
	v_cvt_pk_bf16_f32 v186, v218, v219
	v_pk_fma_f32 v[196:197], v[10:11], v[188:189], v[22:23]
	v_cvt_pk_bf16_f32 v187, v210, v211
	v_pk_fma_f32 v[232:233], v[16:17], v[232:233], v[28:29]
	v_cvt_pk_bf16_f32 v188, v234, v235
	v_cvt_pk_bf16_f32 v189, v232, v233
	global_store_dwordx4 v[238:239], v[186:189], off
	v_fma_f32 v214, v36, v218, 0
	v_fma_f32 v215, v37, v218, 0
	v_fma_f32 v216, v38, v218, 0
	v_fma_f32 v217, v39, v218, 0
	v_fma_f32 v238, v40, v218, 0
	v_fma_f32 v239, v41, v218, 0
	v_pk_fma_f32 v[212:213], v[34:35], v[218:219], 0 op_sel_hi:[1,0,0]
	v_fmac_f32_e32 v214, v44, v219
	v_fmac_f32_e32 v215, v45, v219
	v_fmac_f32_e32 v216, v46, v219
	v_fmac_f32_e32 v217, v47, v219
	v_fmac_f32_e32 v238, v48, v219
	v_fmac_f32_e32 v239, v49, v219
	v_pk_fma_f32 v[212:213], v[42:43], v[218:219], v[212:213] op_sel:[0,1,0]
	v_fmac_f32_e32 v214, v52, v210
	v_fmac_f32_e32 v215, v53, v210
	v_fmac_f32_e32 v216, v54, v210
	v_fmac_f32_e32 v217, v55, v210
	v_fmac_f32_e32 v238, v56, v210
	v_fmac_f32_e32 v239, v57, v210
	v_pk_fma_f32 v[212:213], v[50:51], v[210:211], v[212:213] op_sel_hi:[1,0,1]
	v_fmac_f32_e32 v214, v60, v211
	v_fmac_f32_e32 v215, v61, v211
	v_fmac_f32_e32 v216, v62, v211
	v_fmac_f32_e32 v217, v63, v211
	v_fmac_f32_e32 v238, v64, v211
	v_fmac_f32_e32 v239, v65, v211
	v_pk_fma_f32 v[210:211], v[58:59], v[210:211], v[212:213] op_sel:[0,1,0]
	v_fmac_f32_e32 v214, v68, v234
	v_fmac_f32_e32 v215, v69, v234
	v_fmac_f32_e32 v216, v70, v234
	v_fmac_f32_e32 v217, v71, v234
	v_fmac_f32_e32 v238, v72, v234
	v_fmac_f32_e32 v239, v73, v234
	v_pk_fma_f32 v[210:211], v[66:67], v[234:235], v[210:211] op_sel_hi:[1,0,1]
	v_fmac_f32_e32 v214, v76, v235
	v_fmac_f32_e32 v215, v77, v235
	v_fmac_f32_e32 v216, v78, v235
	v_fmac_f32_e32 v217, v79, v235
	v_fmac_f32_e32 v238, v80, v235
	v_fmac_f32_e32 v239, v81, v235
	v_pk_fma_f32 v[210:211], v[74:75], v[234:235], v[210:211] op_sel:[0,1,0]
	v_fmac_f32_e32 v214, v84, v232
	v_fmac_f32_e32 v215, v85, v232
	v_fmac_f32_e32 v216, v86, v232
	v_fmac_f32_e32 v217, v87, v232
	v_fmac_f32_e32 v238, v88, v232
	v_fmac_f32_e32 v239, v89, v232
	v_pk_fma_f32 v[210:211], v[82:83], v[232:233], v[210:211] op_sel_hi:[1,0,1]
	v_fmac_f32_e32 v214, v92, v233
	v_fmac_f32_e32 v215, v93, v233
	v_fmac_f32_e32 v216, v94, v233
	v_fmac_f32_e32 v217, v95, v233
	v_fmac_f32_e32 v238, v96, v233
	v_fmac_f32_e32 v239, v97, v233
	v_pk_fma_f32 v[210:211], v[90:91], v[232:233], v[210:211] op_sel:[0,1,0]
	v_fmac_f32_e32 v214, v108, v236
	v_fmac_f32_e32 v215, v109, v236
	v_fmac_f32_e32 v216, v98, v236
	v_fmac_f32_e32 v217, v99, v236
	v_fmac_f32_e32 v238, v100, v236
	v_fmac_f32_e32 v239, v101, v236
	v_pk_fma_f32 v[210:211], v[106:107], v[236:237], v[210:211] op_sel_hi:[1,0,1]
	v_pk_fma_f32 v[194:195], v[20:21], v[194:195], v[32:33]
	v_pk_fma_f32 v[210:211], v[102:103], v[236:237], v[210:211] op_sel:[0,1,0]
	v_fmac_f32_e32 v214, v104, v237
	v_fmac_f32_e32 v215, v105, v237
	v_fmac_f32_e32 v216, v110, v237
	v_fmac_f32_e32 v217, v111, v237
	v_fmac_f32_e32 v238, v112, v237
	v_fmac_f32_e32 v239, v113, v237
	v_cvt_pk_bf16_f32 v186, v236, v237
	v_bfe_u32 v187, v194, 16, 1
	v_bfe_u32 v188, v195, 16, 1
	v_fmac_f32_e32 v214, v124, v194
	v_fmac_f32_e32 v215, v125, v194
	v_fmac_f32_e32 v216, v138, v194
	v_fmac_f32_e32 v217, v139, v194
	v_fmac_f32_e32 v238, v140, v194
	v_fmac_f32_e32 v239, v141, v194
	v_pk_fma_f32 v[210:211], v[122:123], v[194:195], v[210:211] op_sel_hi:[1,0,1]
	v_add3_u32 v187, v194, v187, s31
	v_add3_u32 v188, v195, v188, s31
	v_fmac_f32_e32 v214, v116, v195
	v_fmac_f32_e32 v215, v117, v195
	v_fmac_f32_e32 v216, v118, v195
	v_fmac_f32_e32 v217, v119, v195
	v_fmac_f32_e32 v238, v120, v195
	v_fmac_f32_e32 v239, v121, v195
	v_pk_fma_f32 v[194:195], v[114:115], v[194:195], v[210:211] op_sel:[0,1,0]
	v_lshrrev_b32_e32 v187, 16, v187
	v_pk_fma_f32 v[194:195], v[126:127], v[196:197], v[194:195] op_sel_hi:[1,0,1]
	v_and_or_b32 v187, v188, s29, v187
	v_pk_fma_f32 v[194:195], v[134:135], v[196:197], v[194:195] op_sel:[0,1,0]
	v_bfe_u32 v188, v196, 16, 1
	v_pk_fma_f32 v[194:195], v[142:143], v[192:193], v[194:195] op_sel_hi:[1,0,1]
	v_bfe_u32 v189, v197, 16, 1
	v_pk_fma_f32 v[194:195], v[154:155], v[192:193], v[194:195] op_sel:[0,1,0]
	ds_bpermute_b32 v210, v220, v194
	ds_bpermute_b32 v211, v220, v195
	v_fmac_f32_e32 v214, v128, v196
	v_fmac_f32_e32 v215, v129, v196
	v_fmac_f32_e32 v216, v130, v196
	v_fmac_f32_e32 v217, v131, v196
	v_fmac_f32_e32 v238, v132, v196
	v_fmac_f32_e32 v239, v133, v196
	s_waitcnt lgkmcnt(0)
	v_pk_add_f32 v[194:195], v[194:195], v[210:211]
	v_add3_u32 v188, v196, v188, s31
	v_add3_u32 v189, v197, v189, s31
	v_fmac_f32_e32 v214, v136, v197
	v_fmac_f32_e32 v215, v137, v197
	v_fmac_f32_e32 v216, v146, v197
	v_fmac_f32_e32 v217, v147, v197
	v_fmac_f32_e32 v238, v148, v197
	v_fmac_f32_e32 v239, v149, v197
	ds_bpermute_b32 v196, v221, v194
	ds_bpermute_b32 v197, v221, v195
	v_lshrrev_b32_e32 v188, 16, v188
	v_fmac_f32_e32 v214, v144, v192
	v_and_or_b32 v188, v189, s29, v188
	v_bfe_u32 v189, v192, 16, 1
	s_waitcnt lgkmcnt(0)
	v_pk_add_f32 v[194:195], v[194:195], v[196:197]
	v_fmac_f32_e32 v214, v156, v193
	v_add3_u32 v189, v192, v189, s31
	v_fmac_f32_e32 v215, v145, v192
	v_fmac_f32_e32 v216, v150, v192
	v_fmac_f32_e32 v217, v151, v192
	v_fmac_f32_e32 v238, v152, v192
	v_fmac_f32_e32 v239, v153, v192
	ds_bpermute_b32 v196, v222, v194
	ds_bpermute_b32 v197, v222, v195
	ds_bpermute_b32 v192, v220, v214
	v_fmac_f32_e32 v215, v157, v193
	v_fmac_f32_e32 v216, v158, v193
	ds_bpermute_b32 v211, v220, v215
	s_waitcnt lgkmcnt(2)
	v_pk_add_f32 v[194:195], v[194:195], v[196:197]
	s_waitcnt lgkmcnt(1)
	v_add_f32_e32 v192, v214, v192
	ds_bpermute_b32 v196, v223, v194
	ds_bpermute_b32 v197, v223, v195
	ds_bpermute_b32 v210, v221, v192
	ds_bpermute_b32 v212, v220, v216
	v_fmac_f32_e32 v217, v159, v193
	v_fmac_f32_e32 v238, v160, v193
	s_waitcnt lgkmcnt(2)
	v_pk_add_f32 v[194:195], v[194:195], v[196:197]
	s_waitcnt lgkmcnt(1)
	v_add_f32_e32 v192, v192, v210
	ds_bpermute_b32 v196, v224, v194
	ds_bpermute_b32 v197, v224, v195
	ds_bpermute_b32 v210, v222, v192
	v_fmac_f32_e32 v239, v161, v193
	ds_bpermute_b32 v218, v220, v239
	v_lshrrev_b32_e32 v189, 16, v189
	s_waitcnt lgkmcnt(2)
	v_pk_add_f32 v[194:195], v[194:195], v[196:197]
	v_add_f32_e32 v196, v215, v211
	s_waitcnt lgkmcnt(1)
	v_add_f32_e32 v192, v192, v210
	v_add_f32_e32 v210, v216, v212
	ds_bpermute_b32 v197, v221, v196
	ds_bpermute_b32 v211, v221, v210
	ds_bpermute_b32 v212, v223, v192
	ds_bpermute_b32 v216, v220, v217
	s_waitcnt lgkmcnt(4)
	v_add_f32_e32 v218, v239, v218
	s_waitcnt lgkmcnt(3)
	v_add_f32_e32 v197, v196, v197
	s_waitcnt lgkmcnt(2)
	v_add_f32_e32 v210, v210, v211
	ds_bpermute_b32 v213, v222, v197
	ds_bpermute_b32 v211, v222, v210
	s_waitcnt lgkmcnt(3)
	v_add_f32_e32 v192, v192, v212
	ds_bpermute_b32 v214, v224, v192
	s_waitcnt lgkmcnt(3)
	v_add_f32_e32 v216, v217, v216
	s_waitcnt lgkmcnt(2)
	v_add_f32_e32 v212, v197, v213
	s_waitcnt lgkmcnt(1)
	v_add_f32_e32 v210, v210, v211
	ds_bpermute_b32 v213, v223, v212
	ds_bpermute_b32 v211, v223, v210
	s_waitcnt lgkmcnt(2)
	v_add_f32_e32 v192, v192, v214
	ds_bpermute_b32 v217, v221, v216
	ds_bpermute_b32 v232, v221, v218
	s_waitcnt lgkmcnt(3)
	v_add_f32_e32 v212, v212, v213
	s_waitcnt lgkmcnt(2)
	v_add_f32_e32 v214, v210, v211
	ds_bpermute_b32 v213, v224, v212
	ds_bpermute_b32 v215, v224, v214
	s_waitcnt lgkmcnt(3)
	v_add_f32_e32 v216, v216, v217
	s_waitcnt lgkmcnt(2)
	v_add_f32_e32 v218, v218, v232
	ds_bpermute_b32 v217, v222, v216
	s_waitcnt lgkmcnt(2)
	v_add_f32_e32 v211, v212, v213
	s_waitcnt lgkmcnt(1)
	v_add_f32_e32 v213, v214, v215
	ds_bpermute_b32 v215, v220, v238
	ds_bpermute_b32 v232, v222, v218
	s_waitcnt lgkmcnt(2)
	v_add_f32_e32 v216, v216, v217
	ds_bpermute_b32 v217, v223, v216
	ds_bpermute_b32 v196, v225, v194
	s_waitcnt lgkmcnt(3)
	v_add_f32_e32 v215, v238, v215
	ds_bpermute_b32 v219, v221, v215
	s_waitcnt lgkmcnt(3)
	v_add_f32_e32 v218, v218, v232
	ds_bpermute_b32 v232, v223, v218
	s_waitcnt lgkmcnt(3)
	v_add_f32_e32 v216, v216, v217
	ds_bpermute_b32 v217, v224, v216
	s_waitcnt lgkmcnt(2)
	v_add_f32_e32 v215, v215, v219
	ds_bpermute_b32 v219, v222, v215
	s_waitcnt lgkmcnt(2)
	v_add_f32_e32 v232, v218, v232
	ds_bpermute_b32 v234, v224, v232
	ds_bpermute_b32 v197, v225, v195
	ds_bpermute_b32 v210, v225, v192
	s_waitcnt lgkmcnt(3)
	v_add_f32_e32 v215, v215, v219
	ds_bpermute_b32 v219, v223, v215
	ds_bpermute_b32 v212, v225, v211
	ds_bpermute_b32 v214, v225, v213
	s_waitcnt lgkmcnt(2)
	v_add_f32_e32 v219, v215, v219
	ds_bpermute_b32 v233, v224, v219
	v_add_f32_e32 v215, v216, v217
	ds_bpermute_b32 v216, v225, v215
	s_waitcnt lgkmcnt(1)
	v_add_f32_e32 v217, v219, v233
	v_add_f32_e32 v219, v232, v234
	ds_bpermute_b32 v218, v225, v217
	ds_bpermute_b32 v232, v225, v219
	v_bfe_u32 v233, v193, 16, 1
	v_add3_u32 v193, v193, v233, s31
	v_and_or_b32 v189, v193, s29, v189
	global_store_dwordx4 v[190:191], v[186:189], off
	s_and_saveexec_b64 s[24:25], s[2:3]
	s_cbranch_execz .LBB0_1232
	v_pk_add_f32 v[188:189], v[194:195], v[196:197]
	v_add_f32_e32 v192, v192, v210
	v_cmp_gt_f32_e32 vcc, v189, v188
	v_add_f32_e32 v211, v211, v212
	v_add_f32_e32 v193, v213, v214
	v_cndmask_b32_e32 v186, v188, v189, vcc
	v_cmp_gt_f32_e64 s[0:1], v192, v186
	s_waitcnt lgkmcnt(2)
	v_add_f32_e32 v191, v215, v216
	s_waitcnt lgkmcnt(1)
	v_add_f32_e32 v190, v217, v218
	v_cndmask_b32_e64 v186, v186, v192, s[0:1]
	v_cmp_gt_f32_e64 s[4:5], v211, v186
	s_waitcnt lgkmcnt(0)
	v_add_f32_e32 v187, v219, v232
	v_cmp_nlg_f32_e64 s[14:15], s34, v188
	v_cndmask_b32_e64 v186, v186, v211, s[4:5]
	v_cmp_gt_f32_e64 s[6:7], v193, v186
	s_nop 1
	v_cndmask_b32_e64 v186, v186, v193, s[6:7]
	v_cmp_gt_f32_e64 s[8:9], v191, v186
	s_nop 1
	v_cndmask_b32_e64 v186, v186, v191, s[8:9]
	v_cmp_gt_f32_e64 s[10:11], v190, v186
	s_nop 1
	v_cndmask_b32_e64 v194, v186, v190, s[10:11]
	v_cndmask_b32_e64 v186, 0, 1, vcc
	v_cndmask_b32_e64 v186, v186, 2, s[0:1]
	v_cndmask_b32_e64 v186, v186, 3, s[4:5]
	v_cndmask_b32_e64 v186, v186, 4, s[6:7]
	v_cndmask_b32_e64 v186, v186, 5, s[8:9]
	v_cndmask_b32_e64 v186, v186, 6, s[10:11]
	v_cmp_ngt_f32_e32 vcc, v187, v194
	s_and_b64 s[16:17], s[10:11], vcc
	s_nop 0
	v_cndmask_b32_e32 v186, 7, v186, vcc
	v_cmp_eq_u32_e64 s[12:13], 0, v186
	s_or_b64 s[12:13], s[12:13], s[14:15]
	v_cmp_ne_u32_e64 s[10:11], 1, v186
	v_cndmask_b32_e64 v188, v188, v231, s[12:13]
	v_cmp_gt_f32_e64 s[14:15], v189, v188
	s_and_b64 s[10:11], s[10:11], s[14:15]
	v_cndmask_b32_e64 v188, v188, v189, s[10:11]
	v_cmp_ne_u32_e64 s[8:9], 2, v186
	v_cmp_gt_f32_e64 s[14:15], v192, v188
	s_and_b64 s[8:9], s[8:9], s[14:15]
	v_cndmask_b32_e64 v188, v188, v192, s[8:9]
	v_cmp_ne_u32_e64 s[6:7], 3, v186
	v_cmp_gt_f32_e64 s[14:15], v211, v188
	s_and_b64 s[6:7], s[6:7], s[14:15]
	v_cndmask_b32_e64 v188, v188, v211, s[6:7]
	v_cmp_ne_u32_e64 s[4:5], 4, v186
	v_cmp_gt_f32_e64 s[14:15], v193, v188
	s_and_b64 s[4:5], s[4:5], s[14:15]
	v_cndmask_b32_e64 v188, v188, v193, s[4:5]
	v_cmp_ne_u32_e64 s[0:1], 5, v186
	v_cmp_gt_f32_e64 s[14:15], v191, v188
	s_and_b64 s[0:1], s[0:1], s[14:15]
	v_cndmask_b32_e64 v188, v188, v191, s[0:1]
	v_cmp_ngt_f32_e64 s[14:15], v190, v188
	s_or_b64 s[14:15], s[16:17], s[14:15]
	v_cndmask_b32_e64 v189, 0, -1, s[12:13]
	v_cndmask_b32_e64 v188, v190, v188, s[14:15]
	v_cmp_gt_f32_e64 s[16:17], v187, v188
	s_and_b64 s[16:17], vcc, s[16:17]
	v_cndmask_b32_e64 v189, v189, 1, s[10:11]
	v_cndmask_b32_e64 v188, v188, v187, s[16:17]
	v_cndmask_b32_e32 v187, v187, v194, vcc
	v_sub_f32_e32 v187, v188, v187
	v_mul_f32_e32 v187, 0x3fb8aa3b, v187
	v_exp_f32_e32 v191, v187
	v_cndmask_b32_e64 v187, v189, 2, s[8:9]
	v_cndmask_b32_e64 v187, v187, 3, s[6:7]
	v_cndmask_b32_e64 v187, v187, 4, s[4:5]
	v_add_f32_e32 v190, 1.0, v191
	v_div_scale_f32 v188, s[4:5], v190, v190, 1.0
	v_rcp_f32_e32 v192, v188
	v_cndmask_b32_e64 v187, v187, 5, s[0:1]
	v_cndmask_b32_e64 v187, 6, v187, s[14:15]
	v_cndmask_b32_e64 v187, v187, 7, s[16:17]
	v_fma_f32 v189, -v188, v192, 1.0
	v_fmac_f32_e32 v192, v189, v192
	v_div_scale_f32 v189, vcc, 1.0, v190, 1.0
	v_mul_f32_e32 v193, v189, v192
	v_fma_f32 v194, -v188, v193, v189
	v_fmac_f32_e32 v193, v194, v192
	v_fma_f32 v194, -v188, v193, v189
	v_lshl_add_u32 v188, v186, 2, 0
	ds_add_rtn_u32 v188, v188, v230
	v_lshl_add_u32 v189, v187, 2, 0
	ds_add_rtn_u32 v189, v189, v230
	v_div_fmas_f32 v192, v194, v192, v193
	v_div_fixup_f32 v190, v192, v190, 1.0
	v_mul_f32_e32 v191, v191, v190
	s_waitcnt lgkmcnt(0)
	ds_write_b128 v226, v[186:189] offset:48
	v_add_u32_e32 v186, 6, v227
	v_ashrrev_i32_e32 v187, 31, v186
	v_lshl_add_u64 v[186:187], v[186:187], 2, s[36:37]
	global_store_dwordx2 v[186:187], v[190:191], off
	s_branch .LBB0_1232

.LBB0_1342:
	v_mov_b32_e32 v133, v0
	s_lshl_b32 s38, s61, 8
	s_add_i32 s38, s38, s45
	v_and_or_b32 v132, v133, 15, s38
	v_lshrrev_b32_e32 v133, 1, v133
	v_and_or_b32 v133, v133, 24, s47
	v_lshlrev_b32_e32 v194, 1, v133
	v_ashrrev_i32_e32 v133, 31, v132
	v_lshlrev_b64 v[140:141], 11, v[132:133]
	v_bfe_u32 v133, v126, 16, 1
	v_add3_u32 v126, v126, v133, s27
	v_bfe_u32 v133, v127, 16, 1
	v_lshrrev_b32_e32 v126, 16, v126
	v_add3_u32 v127, v127, v133, s27
	v_and_or_b32 v126, v127, s28, v126
	v_cvt_pk_bf16_f32 v127, v128, v129
	v_cvt_pk_bf16_f32 v128, v122, v123
	v_bfe_u32 v122, v124, 16, 1
	v_add3_u32 v122, v124, v122, s27
	v_bfe_u32 v123, v125, 16, 1
	v_lshrrev_b32_e32 v122, 16, v122
	v_add3_u32 v123, v125, v123, s27
	v_and_or_b32 v129, v123, s28, v122
	v_bfe_u32 v122, v118, 16, 1
	v_add3_u32 v118, v118, v122, s27
	v_bfe_u32 v122, v119, 16, 1
	v_lshrrev_b32_e32 v118, 16, v118
	v_add3_u32 v119, v119, v122, s27
	v_and_or_b32 v118, v119, s28, v118
	v_cvt_pk_bf16_f32 v119, v120, v121
	s_lshl_b32 s38, s64, 8
	s_ashr_i32 s39, s38, 31
	v_cvt_pk_bf16_f32 v120, v110, v111
	s_lshl_b64 s[38:39], s[38:39], 1
	s_add_u32 s38, s77, s38
	s_addc_u32 s39, s6, s39
	v_cvt_pk_bf16_f32 v121, v112, v113
	v_or_b32_e32 v110, 16, v132
	v_lshl_add_u64 v[134:135], s[38:39], 0, v[194:195]
	v_ashrrev_i32_e32 v111, 31, v110
	v_lshl_add_u64 v[140:141], v[134:135], 0, v[140:141]
	v_lshlrev_b64 v[110:111], 11, v[110:111]
	global_store_dwordx4 v[140:141], v[118:121], off offset:256
	s_nop 1
	v_lshl_add_u64 v[118:119], v[134:135], 0, v[110:111]
	v_cvt_pk_bf16_f32 v110, v114, v115
	v_cvt_pk_bf16_f32 v111, v116, v117
	v_cvt_pk_bf16_f32 v112, v106, v107
	v_bfe_u32 v106, v108, 16, 1
	v_add3_u32 v106, v108, v106, s27
	v_bfe_u32 v107, v109, 16, 1
	v_lshrrev_b32_e32 v106, 16, v106
	v_add3_u32 v107, v109, v107, s27
	v_and_or_b32 v113, v107, s28, v106
	v_bfe_u32 v106, v102, 16, 1
	v_add3_u32 v102, v102, v106, s27
	v_bfe_u32 v106, v103, 16, 1
	v_lshrrev_b32_e32 v102, 16, v102
	v_add3_u32 v103, v103, v106, s27
	v_and_or_b32 v102, v103, s28, v102
	v_cvt_pk_bf16_f32 v103, v104, v105
	v_cvt_pk_bf16_f32 v104, v94, v95
	v_cvt_pk_bf16_f32 v105, v96, v97
	v_or_b32_e32 v94, 32, v132
	v_ashrrev_i32_e32 v95, 31, v94
	v_lshlrev_b64 v[94:95], 11, v[94:95]
	global_store_dwordx4 v[118:119], v[102:105], off offset:256
	s_nop 1
	v_lshl_add_u64 v[102:103], v[134:135], 0, v[94:95]
	v_cvt_pk_bf16_f32 v94, v98, v99
	v_cvt_pk_bf16_f32 v95, v100, v101
	v_cvt_pk_bf16_f32 v96, v90, v91
	v_bfe_u32 v90, v92, 16, 1
	v_add3_u32 v90, v92, v90, s27
	v_bfe_u32 v91, v93, 16, 1
	v_lshrrev_b32_e32 v90, 16, v90
	v_add3_u32 v91, v93, v91, s27
	v_and_or_b32 v97, v91, s28, v90
	v_bfe_u32 v90, v86, 16, 1
	v_add3_u32 v86, v86, v90, s27
	v_bfe_u32 v90, v87, 16, 1
	v_lshrrev_b32_e32 v86, 16, v86
	v_add3_u32 v87, v87, v90, s27
	v_and_or_b32 v86, v87, s28, v86
	v_cvt_pk_bf16_f32 v87, v88, v89
	v_cvt_pk_bf16_f32 v88, v78, v79
	v_cvt_pk_bf16_f32 v89, v80, v81
	v_or_b32_e32 v78, 48, v132
	v_ashrrev_i32_e32 v79, 31, v78
	v_lshlrev_b64 v[78:79], 11, v[78:79]
	global_store_dwordx4 v[102:103], v[86:89], off offset:256
	s_nop 1
	v_lshl_add_u64 v[86:87], v[134:135], 0, v[78:79]
	v_cvt_pk_bf16_f32 v78, v82, v83
	v_cvt_pk_bf16_f32 v79, v84, v85
	v_cvt_pk_bf16_f32 v80, v74, v75
	v_bfe_u32 v74, v76, 16, 1
	v_add3_u32 v74, v76, v74, s27
	v_bfe_u32 v75, v77, 16, 1
	v_lshrrev_b32_e32 v74, 16, v74
	v_add3_u32 v75, v77, v75, s27
	v_and_or_b32 v81, v75, s28, v74
	v_bfe_u32 v74, v70, 16, 1
	v_add3_u32 v70, v70, v74, s27
	v_bfe_u32 v74, v71, 16, 1
	v_lshrrev_b32_e32 v70, 16, v70
	v_add3_u32 v71, v71, v74, s27
	v_and_or_b32 v70, v71, s28, v70
	v_cvt_pk_bf16_f32 v71, v72, v73
	v_cvt_pk_bf16_f32 v72, v66, v67
	v_bfe_u32 v66, v68, 16, 1
	v_add3_u32 v66, v68, v66, s27
	v_bfe_u32 v68, v62, 16, 1
	v_add3_u32 v62, v62, v68, s27
	v_bfe_u32 v68, v63, 16, 1
	v_lshrrev_b32_e32 v62, 16, v62
	v_add3_u32 v63, v63, v68, s27
	v_and_or_b32 v62, v63, s28, v62
	v_cvt_pk_bf16_f32 v63, v64, v65
	v_cvt_pk_bf16_f32 v64, v58, v59
	v_bfe_u32 v58, v60, 16, 1
	v_add3_u32 v58, v60, v58, s27
	v_bfe_u32 v59, v61, 16, 1
	v_lshrrev_b32_e32 v58, 16, v58
	v_add3_u32 v59, v61, v59, s27
	v_and_or_b32 v65, v59, s28, v58
	v_bfe_u32 v58, v54, 16, 1
	v_add3_u32 v54, v54, v58, s27
	v_bfe_u32 v58, v55, 16, 1
	v_lshrrev_b32_e32 v54, 16, v54
	v_add3_u32 v55, v55, v58, s27
	v_and_or_b32 v54, v55, s28, v54
	v_cvt_pk_bf16_f32 v55, v56, v57
	v_bfe_u32 v67, v69, 16, 1
	v_cvt_pk_bf16_f32 v56, v46, v47
	v_lshrrev_b32_e32 v66, 16, v66
	v_add3_u32 v67, v69, v67, s27
	v_and_or_b32 v73, v67, s28, v66
	v_add_u32_e32 v66, 0x80, v132
	v_ashrrev_i32_e32 v67, 31, v66
	v_cvt_pk_bf16_f32 v57, v48, v49
	v_add_u32_e32 v46, 0x90, v132
	v_lshlrev_b64 v[66:67], 11, v[66:67]
	v_ashrrev_i32_e32 v47, 31, v46
	v_lshl_add_u64 v[66:67], v[134:135], 0, v[66:67]
	v_lshlrev_b64 v[46:47], 11, v[46:47]
	global_store_dwordx4 v[66:67], v[54:57], off offset:256
	s_nop 1
	v_lshl_add_u64 v[54:55], v[134:135], 0, v[46:47]
	v_cvt_pk_bf16_f32 v46, v50, v51
	v_cvt_pk_bf16_f32 v47, v52, v53
	v_cvt_pk_bf16_f32 v48, v42, v43
	v_bfe_u32 v42, v44, 16, 1
	v_add3_u32 v42, v44, v42, s27
	v_bfe_u32 v43, v45, 16, 1
	v_lshrrev_b32_e32 v42, 16, v42
	v_add3_u32 v43, v45, v43, s27
	v_and_or_b32 v49, v43, s28, v42
	v_bfe_u32 v42, v38, 16, 1
	v_add3_u32 v38, v38, v42, s27
	v_bfe_u32 v42, v39, 16, 1
	v_lshrrev_b32_e32 v38, 16, v38
	v_add3_u32 v39, v39, v42, s27
	v_and_or_b32 v38, v39, s28, v38
	v_cvt_pk_bf16_f32 v39, v40, v41
	v_cvt_pk_bf16_f32 v40, v30, v31
	v_cvt_pk_bf16_f32 v41, v32, v33
	v_add_u32_e32 v30, 0xa0, v132
	v_ashrrev_i32_e32 v31, 31, v30
	v_lshlrev_b64 v[30:31], 11, v[30:31]
	global_store_dwordx4 v[54:55], v[38:41], off offset:256
	s_nop 1
	v_lshl_add_u64 v[38:39], v[134:135], 0, v[30:31]
	v_cvt_pk_bf16_f32 v30, v34, v35
	v_cvt_pk_bf16_f32 v31, v36, v37
	v_cvt_pk_bf16_f32 v32, v26, v27
	v_bfe_u32 v26, v28, 16, 1
	v_add3_u32 v26, v28, v26, s27
	v_bfe_u32 v27, v29, 16, 1
	v_lshrrev_b32_e32 v26, 16, v26
	v_add3_u32 v27, v29, v27, s27
	v_and_or_b32 v33, v27, s28, v26
	v_bfe_u32 v26, v22, 16, 1
	v_add3_u32 v22, v22, v26, s27
	v_bfe_u32 v26, v23, 16, 1
	v_lshrrev_b32_e32 v22, 16, v22
	v_add3_u32 v23, v23, v26, s27
	v_and_or_b32 v22, v23, s28, v22
	v_cvt_pk_bf16_f32 v23, v24, v25
	v_cvt_pk_bf16_f32 v24, v14, v15
	v_cvt_pk_bf16_f32 v25, v16, v17
	v_add_u32_e32 v14, 0xb0, v132
	v_ashrrev_i32_e32 v15, 31, v14
	v_lshlrev_b64 v[14:15], 11, v[14:15]
	global_store_dwordx4 v[38:39], v[22:25], off offset:256
	s_nop 1
	v_lshl_add_u64 v[22:23], v[134:135], 0, v[14:15]
	v_cvt_pk_bf16_f32 v14, v18, v19
	v_cvt_pk_bf16_f32 v15, v20, v21
	v_cvt_pk_bf16_f32 v16, v10, v11
	v_bfe_u32 v10, v12, 16, 1
	v_add3_u32 v10, v12, v10, s27
	v_bfe_u32 v11, v13, 16, 1
	v_lshrrev_b32_e32 v10, 16, v10
	v_add3_u32 v11, v13, v11, s27
	v_and_or_b32 v17, v11, s28, v10
	v_bfe_u32 v10, v6, 16, 1
	v_add3_u32 v6, v6, v10, s27
	v_bfe_u32 v10, v7, 16, 1
	v_lshrrev_b32_e32 v6, 16, v6
	v_add3_u32 v7, v7, v10, s27
	v_and_or_b32 v6, v7, s28, v6
	v_cvt_pk_bf16_f32 v7, v8, v9
	v_cvt_pk_bf16_f32 v8, v2, v3
	v_cvt_pk_bf16_f32 v9, v4, v5
	s_and_b64 vcc, exec, s[36:37]
	s_mov_b64 s[36:37], -1
	global_store_dwordx4 v[140:141], v[126:129], off
	global_store_dwordx4 v[118:119], v[110:113], off
	global_store_dwordx4 v[102:103], v[94:97], off
	global_store_dwordx4 v[86:87], v[78:81], off
	global_store_dwordx4 v[86:87], v[70:73], off offset:256
	global_store_dwordx4 v[66:67], v[62:65], off
	global_store_dwordx4 v[54:55], v[46:49], off
	global_store_dwordx4 v[38:39], v[30:33], off
	global_store_dwordx4 v[22:23], v[14:17], off
	global_store_dwordx4 v[22:23], v[6:9], off offset:256
	s_cbranch_vccnz .LBB0_1321
	s_andn2_b64 vcc, exec, s[82:83]
	s_cbranch_vccnz .LBB0_1320
	s_barrier
	s_branch .LBB0_1320
